# LayerNorm/router wave sums: intra-row xor-butterfly steps (1,2,4,8) via DPP adds instead of ds_bpermute round trips (same association order)
# baseline (speedup 1.0000x reference)
; __device__ __forceinline__ float wave_sum(float v) {
; #pragma unroll
;     for (int o = 1; o < 64; o <<= 1) v += __shfl_xor(v, o);
;     return v;
; }
; __device__ __forceinline__ void ln_regs(f32x4 (&v)[8], const float* g, const float* bt, int lane) {
;     float s = 0.f;
; #pragma unroll
;     for (int j = 0; j < 8; ++j) s += (v[j].x + v[j].y) + (v[j].z + v[j].w);
;     const float mean = wave_sum(s) * (1.f / D); float s2 = 0.f;
; #pragma unroll
;     for (int j = 0; j < 8; ++j) { v[j] = v[j] - mean; s2 += (v[j].x * v[j].x + v[j].y * v[j].y) + (v[j].z * v[j].z + v[j].w * v[j].w); }
;     const float rstd = 1.f / sqrtf(wave_sum(s2) * (1.f / D) + LN_EPS);
.LBB0_1076:
	v_pk_add_f32 v[66:67], v[52:53], v[54:55]
	v_pk_add_f32 v[68:69], v[32:33], v[36:37]
	v_add_f32_e32 v31, v28, v29
	v_pk_add_f32 v[66:67], v[66:67], v[68:69]
	v_add_f32_e32 v43, v40, v41
	v_add_f32_e32 v27, 0, v67
	v_add_f32_e32 v45, v66, v27
	v_pk_add_f32 v[66:67], v[64:65], v[22:23]
	v_add_f32_e32 v27, v24, v25
	v_pk_add_f32 v[66:67], v[66:67], v[66:67] op_sel_hi:[0,1]
	v_mov_b32_e32 v39, v67
	v_pk_add_f32 v[68:69], v[26:27], v[30:31]
	v_pk_add_f32 v[66:67], v[38:39], v[44:45]
	v_and_b32_e32 v31, 64, v84
	v_pk_add_f32 v[66:67], v[68:69], v[66:67]
	v_pk_add_f32 v[68:69], v[62:63], v[34:35]
	v_pk_add_f32 v[66:67], v[66:67], v[66:67] op_sel_hi:[0,1]
	v_pk_add_f32 v[68:69], v[68:69], v[68:69] op_sel_hi:[0,1]
	v_add_f32_e32 v47, v48, v49
	v_mov_b32_e32 v51, v69
	v_mov_b32_e32 v57, v67
	v_add_u32_e32 v31, 64, v31
	v_xor_b32_e32 v39, 1, v84
	v_pk_add_f32 v[70:71], v[42:43], v[46:47]
	v_pk_add_f32 v[66:67], v[50:51], v[56:57]
	v_cmp_lt_i32_e32 vcc, v39, v31
	v_pk_add_f32 v[66:67], v[70:71], v[66:67]
	s_waitcnt lgkmcnt(0)
	v_readlane_b32 s40, v255, 28
	v_cndmask_b32_e32 v39, v84, v39, vcc
	v_add_f32_e32 v27, v66, v67
	v_lshlrev_b32_e32 v39, 2, v39
	v_readlane_b32 s54, v255, 42
	v_readlane_b32 s55, v255, 43
	v_ashrrev_i32_e32 v59, 31, v58
	v_readlane_b32 s41, v255, 29
	s_waitcnt lgkmcnt(0)
	s_nop 1
	v_add_f32_dpp v27, v27, v27 quad_perm:[1,0,3,2] row_mask:0xf bank_mask:0xf
	v_xor_b32_e32 v43, 2, v84
	v_cmp_lt_i32_e32 vcc, v43, v31
	v_readlane_b32 s42, v255, 30
	v_readlane_b32 s43, v255, 31
	v_cndmask_b32_e32 v43, v84, v43, vcc
	v_lshlrev_b32_e32 v43, 2, v43
	v_readlane_b32 s44, v255, 32
	v_readlane_b32 s45, v255, 33
	v_readlane_b32 s46, v255, 34
	v_readlane_b32 s47, v255, 35
	s_waitcnt lgkmcnt(0)
	s_nop 1
	v_add_f32_dpp v27, v27, v27 quad_perm:[2,3,0,1] row_mask:0xf bank_mask:0xf
	v_xor_b32_e32 v45, 4, v84
	v_cmp_lt_i32_e32 vcc, v45, v31
	v_readlane_b32 s48, v255, 36
	v_readlane_b32 s49, v255, 37
	v_cndmask_b32_e32 v45, v84, v45, vcc
	v_lshlrev_b32_e32 v45, 2, v45
	v_readlane_b32 s50, v255, 38
	v_readlane_b32 s51, v255, 39
	v_readlane_b32 s52, v255, 40
	v_readlane_b32 s53, v255, 41
	s_waitcnt lgkmcnt(0)
	s_nop 1
	v_add_f32_dpp v27, v27, v27 row_half_mirror row_mask:0xf bank_mask:0xf
	v_xor_b32_e32 v47, 8, v84
	v_cmp_lt_i32_e32 vcc, v47, v31
	s_nop 1
	v_cndmask_b32_e32 v47, v84, v47, vcc
	v_lshlrev_b32_e32 v47, 2, v47
	s_waitcnt lgkmcnt(0)
	s_nop 1
	v_add_f32_dpp v27, v27, v27 row_mirror row_mask:0xf bank_mask:0xf
	v_xor_b32_e32 v51, 16, v84
	v_cmp_lt_i32_e32 vcc, v51, v31
	s_nop 1
	v_cndmask_b32_e32 v51, v84, v51, vcc
	v_lshlrev_b32_e32 v51, 2, v51
	ds_bpermute_b32 v57, v51, v27
	s_waitcnt lgkmcnt(0)
	v_add_f32_e32 v27, v27, v57
	v_xor_b32_e32 v57, 32, v84
	v_cmp_lt_i32_e32 vcc, v57, v31
	s_nop 1
	v_cndmask_b32_e32 v31, v84, v57, vcc
	v_lshlrev_b32_e32 v31, 2, v31
	ds_bpermute_b32 v57, v31, v27
	s_waitcnt lgkmcnt(0)
	v_add_f32_e32 v27, v27, v57
	v_fmac_f32_e32 v55, 0xba000000, v27
	v_fmac_f32_e32 v54, 0xba000000, v27
	v_fmac_f32_e32 v37, 0xba000000, v27
	v_fmac_f32_e32 v53, 0xba000000, v27
	v_fmac_f32_e32 v36, 0xba000000, v27
	v_fmac_f32_e32 v52, 0xba000000, v27
	v_mov_b32_e32 v68, v55
	v_mov_b32_e32 v69, v54
	v_fmac_f32_e32 v33, 0xba000000, v27
	v_fmac_f32_e32 v32, 0xba000000, v27
	v_mov_b32_e32 v66, v53
	v_mov_b32_e32 v67, v52
	v_pk_mul_f32 v[68:69], v[68:69], v[68:69]
	v_mov_b32_e32 v70, v37
	v_mov_b32_e32 v71, v36
	v_pk_fma_f32 v[66:67], v[66:67], v[66:67], v[68:69]
	v_mov_b32_e32 v68, v33
	v_mov_b32_e32 v69, v32
	v_pk_mul_f32 v[70:71], v[70:71], v[70:71]
	v_fmac_f32_e32 v64, 0xba000000, v27
	v_pk_fma_f32 v[68:69], v[68:69], v[68:69], v[70:71]
	v_fmac_f32_e32 v23, 0xba000000, v27
	v_pk_add_f32 v[66:67], v[66:67], v[68:69]
	v_fmac_f32_e32 v65, 0xba000000, v27
	v_pk_add_f32 v[68:69], v[66:67], v[66:67] op_sel_hi:[0,1]
	v_fmac_f32_e32 v22, 0xba000000, v27
	v_mov_b32_e32 v66, v65
	v_mov_b32_e32 v67, v23
	v_mov_b32_e32 v23, v64
	v_pk_mul_f32 v[70:71], v[66:67], v[66:67]
	v_pk_mul_f32 v[64:65], v[22:23], v[22:23]
	v_fmac_f32_e32 v24, 0xba000000, v27
	v_pk_mov_b32 v[72:73], v[64:65], v[70:71] op_sel:[1,0]
	v_mov_b32_e32 v65, v71
	v_pk_add_f32 v[64:65], v[72:73], v[64:65]
	v_fmac_f32_e32 v25, 0xba000000, v27
	v_pk_add_f32 v[64:65], v[64:65], v[64:65] op_sel_hi:[0,1]
	v_fmac_f32_e32 v28, 0xba000000, v27
	v_mul_f32_e32 v64, v24, v24
	v_fmac_f32_e32 v29, 0xba000000, v27
	v_pk_fma_f32 v[70:71], v[24:25], v[24:25], v[64:65] op_sel_hi:[1,1,0]
	v_mul_f32_e32 v64, v28, v28
	v_pk_fma_f32 v[72:73], v[28:29], v[28:29], v[64:65] op_sel_hi:[1,1,0]
	v_fmac_f32_e32 v44, 0xba000000, v27
	v_fmac_f32_e32 v38, 0xba000000, v27
	v_fmac_f32_e32 v30, 0xba000000, v27
	v_fmac_f32_e32 v26, 0xba000000, v27
	v_mul_f32_e32 v70, v26, v26
	v_mul_f32_e32 v72, v30, v30
	v_mul_f32_e32 v64, v38, v38
	v_mul_f32_e32 v68, v44, v44
	v_pk_add_f32 v[70:71], v[70:71], v[72:73]
	v_pk_add_f32 v[64:65], v[64:65], v[68:69]
	v_fmac_f32_e32 v62, 0xba000000, v27
	v_pk_add_f32 v[64:65], v[70:71], v[64:65]
	v_fmac_f32_e32 v35, 0xba000000, v27
	v_fmac_f32_e32 v63, 0xba000000, v27
	v_pk_add_f32 v[68:69], v[64:65], v[64:65] op_sel_hi:[0,1]
	v_fmac_f32_e32 v34, 0xba000000, v27
	v_mov_b32_e32 v64, v63
	v_mov_b32_e32 v65, v35
	v_mov_b32_e32 v35, v62
	v_pk_mul_f32 v[70:71], v[64:65], v[64:65]
	v_pk_mul_f32 v[62:63], v[34:35], v[34:35]
	v_fmac_f32_e32 v40, 0xba000000, v27
	v_pk_mov_b32 v[72:73], v[62:63], v[70:71] op_sel:[1,0]
	v_mov_b32_e32 v63, v71
	v_pk_add_f32 v[62:63], v[72:73], v[62:63]
	v_fmac_f32_e32 v41, 0xba000000, v27
	v_pk_add_f32 v[62:63], v[62:63], v[62:63] op_sel_hi:[0,1]
	v_fmac_f32_e32 v48, 0xba000000, v27
	v_mul_f32_e32 v62, v40, v40
	v_fmac_f32_e32 v49, 0xba000000, v27
; __device__ __forceinline__ void stx4(XT* p, f32x4 v) { st_bf4(p, v); }
; __device__ __forceinline__ void ln_regs(f32x4 (&v)[8], const float* g, const float* bt, int lane) {
;     ...
;     const float mean = wave_sum(s) * (1.f / D); float s2 = 0.f;
; #pragma unroll
;     for (int j = 0; j < 8; ++j) { v[j] = v[j] - mean; s2 += (v[j].x * v[j].x + v[j].y * v[j].y) + (v[j].z * v[j].z + v[j].w * v[j].w); }
;     const float rstd = 1.f / sqrtf(wave_sum(s2) * (1.f / D) + LN_EPS);
; #pragma unroll
;     for (int j = 0; j < 8; ++j) { const f32x4 gv = *(const f32x4*)(g + j * 256 + lane * 4), bv = *(const f32x4*)(bt + j * 256 + lane * 4); v[j] = v[j] * rstd * gv + bv; }
; template <int L, bool ROUTER, bool WRITE_HB> __device__ __forceinline__ void p_ln_mix(const Args& a, LAS unsigned char* lds, XT* X) {
;     ...
;             ln_regs(v, g, bt, lane);
; #pragma unroll
;             for (int j = 0; j < 8; ++j) stx4(xr + j * 256 + lane * 4, v[j]);
	v_pk_fma_f32 v[70:71], v[40:41], v[40:41], v[62:63] op_sel_hi:[1,1,0]
	v_mul_f32_e32 v62, v48, v48
	v_pk_fma_f32 v[72:73], v[48:49], v[48:49], v[62:63] op_sel_hi:[1,1,0]
	v_fmac_f32_e32 v56, 0xba000000, v27
	v_fmac_f32_e32 v50, 0xba000000, v27
	v_fmac_f32_e32 v46, 0xba000000, v27
	v_fmac_f32_e32 v42, 0xba000000, v27
	v_mul_f32_e32 v70, v42, v42
	v_mul_f32_e32 v72, v46, v46
	v_mul_f32_e32 v62, v50, v50
	v_mul_f32_e32 v68, v56, v56
	v_pk_add_f32 v[70:71], v[70:71], v[72:73]
	v_pk_add_f32 v[62:63], v[62:63], v[68:69]
	v_mov_b32_e32 v136, v52
	v_pk_add_f32 v[62:63], v[70:71], v[62:63]
	v_mov_b32_e32 v52, v32
	v_add_f32_e32 v27, v62, v63
	v_lshlrev_b64 v[62:63], 2, v[20:21]
	v_lshl_add_u64 v[104:105], s[54:55], 0, v[62:63]
	v_add_co_u32_e32 v128, vcc, s31, v104
	v_lshl_add_u64 v[108:109], s[80:81], 0, v[62:63]
	s_nop 0
	v_addc_co_u32_e32 v129, vcc, 0, v105, vcc
	v_add_co_u32_e32 v132, vcc, s31, v108
	global_load_dwordx4 v[68:71], v[104:105], off
	global_load_dwordx4 v[72:75], v[108:109], off
	global_load_dwordx4 v[76:79], v[104:105], off offset:1024
	global_load_dwordx4 v[80:83], v[108:109], off offset:1024
	global_load_dwordx4 v[88:91], v[104:105], off offset:2048
	global_load_dwordx4 v[92:95], v[104:105], off offset:3072
	global_load_dwordx4 v[96:99], v[108:109], off offset:2048
	global_load_dwordx4 v[100:103], v[108:109], off offset:3072
	v_addc_co_u32_e32 v133, vcc, 0, v109, vcc
	global_load_dwordx4 v[104:107], v[128:129], off
	global_load_dwordx4 v[108:111], v[132:133], off
	global_load_dwordx4 v[112:115], v[128:129], off offset:1024
	global_load_dwordx4 v[116:119], v[132:133], off offset:1024
	global_load_dwordx4 v[120:123], v[128:129], off offset:2048
	global_load_dwordx4 v[124:127], v[132:133], off offset:2048
	global_load_dwordx4 v[128:131], v[128:129], off offset:3072
	s_nop 0
	global_load_dwordx4 v[132:135], v[132:133], off offset:3072
	v_mov_b32_e32 v137, v54
	v_mov_b32_e32 v54, v53
	v_mov_b32_e32 v53, v36
	s_waitcnt lgkmcnt(0)
	s_nop 1
	v_add_f32_dpp v27, v27, v27 quad_perm:[1,0,3,2] row_mask:0xf bank_mask:0xf
	v_mov_b32_e32 v36, v33
	s_waitcnt lgkmcnt(0)
	s_nop 1
	v_add_f32_dpp v27, v27, v27 quad_perm:[2,3,0,1] row_mask:0xf bank_mask:0xf
	s_waitcnt lgkmcnt(0)
	s_nop 1
	v_add_f32_dpp v27, v27, v27 row_half_mirror row_mask:0xf bank_mask:0xf
	s_waitcnt lgkmcnt(0)
	s_nop 1
	v_add_f32_dpp v27, v27, v27 row_mirror row_mask:0xf bank_mask:0xf
	ds_bpermute_b32 v39, v51, v27
	v_mov_b32_e32 v51, v56
	s_waitcnt lgkmcnt(0)
	v_add_f32_e32 v27, v27, v39
	ds_bpermute_b32 v31, v31, v27
	s_waitcnt lgkmcnt(0)
	v_add_f32_e32 v27, v27, v31
	v_fmamk_f32 v27, v27, 0x3a000000, v85
	v_mul_f32_e32 v31, 0x4f800000, v27
	v_cmp_gt_f32_e32 vcc, s30, v27
	s_nop 1
	v_cndmask_b32_e32 v27, v27, v31, vcc
	v_sqrt_f32_e32 v31, v27
	s_nop 0
	v_add_u32_e32 v32, -1, v31
	v_fma_f32 v39, -v32, v31, v27
	v_cmp_ge_f32_e64 s[6:7], 0, v39
	v_add_u32_e32 v39, 1, v31
	s_nop 0
	v_cndmask_b32_e64 v32, v31, v32, s[6:7]
	v_fma_f32 v31, -v39, v31, v27
	v_cmp_lt_f32_e64 s[6:7], 0, v31
	s_nop 1
	v_cndmask_b32_e64 v31, v32, v39, s[6:7]
	v_mul_f32_e32 v32, 0x37800000, v31
	v_cndmask_b32_e32 v31, v31, v32, vcc
	v_cmp_class_f32_e32 vcc, v27, v86
	s_nop 1
	v_cndmask_b32_e32 v27, v31, v27, vcc
	v_div_scale_f32 v31, s[6:7], v27, v27, 1.0
	v_rcp_f32_e32 v32, v31
	s_nop 0
	v_fma_f32 v33, -v31, v32, 1.0
	v_fmac_f32_e32 v32, v33, v32
	v_div_scale_f32 v33, vcc, 1.0, v27, 1.0
	v_mul_f32_e32 v39, v33, v32
	v_fma_f32 v43, -v31, v39, v33
	v_fmac_f32_e32 v39, v43, v32
	v_fma_f32 v31, -v31, v39, v33
	v_div_fmas_f32 v31, v31, v32, v39
	v_div_fixup_f32 v138, v31, v27, 1.0
	v_pk_mul_f32 v[32:33], v[54:55], v[138:139] op_sel_hi:[1,0]
	v_pk_mul_f32 v[36:37], v[36:37], v[138:139] op_sel_hi:[1,0]
	v_pk_mul_f32 v[24:25], v[24:25], v[138:139] op_sel_hi:[1,0]
	v_mov_b32_e32 v27, v30
	s_waitcnt vmcnt(14)
	v_pk_fma_f32 v[140:141], v[70:71], v[36:37], v[74:75]
	v_pk_fma_f32 v[142:143], v[68:69], v[32:33], v[72:73]
	v_pk_mul_f32 v[32:33], v[136:137], v[138:139] op_sel_hi:[1,0]
	v_pk_mul_f32 v[36:37], v[52:53], v[138:139] op_sel_hi:[1,0]
	s_waitcnt vmcnt(8)
	v_pk_fma_f32 v[54:55], v[92:93], v[24:25], v[100:101]
	v_pk_mul_f32 v[24:25], v[26:27], v[138:139] op_sel_hi:[1,0]
	v_pk_fma_f32 v[82:83], v[78:79], v[36:37], v[82:83]
	v_pk_fma_f32 v[136:137], v[76:77], v[32:33], v[80:81]
	v_pk_mul_f32 v[22:23], v[22:23], v[138:139] op_sel_hi:[1,0]
	v_pk_mul_f32 v[32:33], v[66:67], v[138:139] op_sel_hi:[1,0]
	s_waitcnt vmcnt(6)
	v_pk_fma_f32 v[36:37], v[104:105], v[24:25], v[108:109]
	v_pk_mul_f32 v[24:25], v[34:35], v[138:139] op_sel_hi:[1,0]
	v_pk_fma_f32 v[66:67], v[90:91], v[32:33], v[98:99]
	v_pk_fma_f32 v[68:69], v[88:89], v[22:23], v[96:97]
	v_pk_mul_f32 v[22:23], v[28:29], v[138:139] op_sel_hi:[1,0]
	v_mov_b32_e32 v39, v44
	s_waitcnt vmcnt(4)
	v_pk_fma_f32 v[32:33], v[112:113], v[24:25], v[116:117]
	v_pk_mul_f32 v[24:25], v[40:41], v[138:139] op_sel_hi:[1,0]
	v_bfe_u32 v40, v142, 16, 1
	v_pk_fma_f32 v[52:53], v[94:95], v[22:23], v[102:103]
	v_pk_mul_f32 v[22:23], v[38:39], v[138:139] op_sel_hi:[1,0]
	v_add3_u32 v40, v142, v40, s33
	v_bfe_u32 v41, v143, 16, 1
	v_pk_fma_f32 v[38:39], v[106:107], v[22:23], v[110:111]
	v_pk_mul_f32 v[22:23], v[64:65], v[138:139] op_sel_hi:[1,0]
	v_lshrrev_b32_e32 v40, 16, v40
	v_add3_u32 v41, v143, v41, s33
	v_pk_fma_f32 v[30:31], v[114:115], v[22:23], v[118:119]
	v_pk_mul_f32 v[22:23], v[48:49], v[138:139] op_sel_hi:[1,0]
	v_mov_b32_e32 v43, v46
	v_and_or_b32 v40, v41, s29, v40
	v_bfe_u32 v41, v140, 16, 1
	s_waitcnt vmcnt(2)
; __device__ __forceinline__ void stx4(XT* p, f32x4 v) { st_bf4(p, v); }
; template <int L, bool ROUTER, bool WRITE_HB> __device__ __forceinline__ void p_ln_mix(const Args& a, LAS unsigned char* lds, XT* X) {
;     ...
;             for (int j = 0; j < 8; ++j) stx4(xr + j * 256 + lane * 4, v[j]);
;             if (WRITE_HB) { const float* md = mod + (size_t)(m >> 12) * D6; bf16* hb = (bf16*)(a.ws + WS_HB) + (size_t)m * D;
;                 f32x4 shv[8], scv[8];
; #pragma unroll
;                 for (int j = 0; j < 8; ++j) { const int k = j * 256 + lane * 4; shv[j] = *(const f32x4*)(md + 6144 + k); scv[j] = *(const f32x4*)(md + 8192 + k); }
	v_pk_fma_f32 v[28:29], v[122:123], v[22:23], v[126:127]
	v_pk_mul_f32 v[22:23], v[42:43], v[138:139] op_sel_hi:[1,0]
	v_lshl_add_u64 v[34:35], s[66:67], 0, v[60:61]
	v_add3_u32 v41, v140, v41, s33
	v_bfe_u32 v42, v141, 16, 1
	v_lshrrev_b32_e32 v41, 16, v41
	v_add3_u32 v42, v141, v42, s33
	v_add_co_u32_e32 v34, vcc, s34, v34
	v_and_or_b32 v41, v42, s29, v41
	s_nop 0
	v_addc_co_u32_e32 v35, vcc, 0, v35, vcc
	global_store_dwordx2 v[34:35], v[40:41], off
	v_bfe_u32 v40, v136, 16, 1
	v_add3_u32 v40, v136, v40, s33
	v_bfe_u32 v41, v137, 16, 1
	v_lshrrev_b32_e32 v40, 16, v40
	v_add3_u32 v41, v137, v41, s33
	v_and_or_b32 v40, v41, s29, v40
	v_bfe_u32 v41, v82, 16, 1
	v_add3_u32 v41, v82, v41, s33
	v_bfe_u32 v42, v83, 16, 1
	v_lshrrev_b32_e32 v41, 16, v41
	v_add3_u32 v42, v83, v42, s33
	v_and_or_b32 v41, v42, s29, v41
	global_store_dwordx2 v[34:35], v[40:41], off offset:512
	v_bfe_u32 v40, v68, 16, 1
	v_add3_u32 v40, v68, v40, s33
	v_bfe_u32 v41, v69, 16, 1
	v_lshrrev_b32_e32 v40, 16, v40
	v_add3_u32 v41, v69, v41, s33
	v_and_or_b32 v40, v41, s29, v40
	v_bfe_u32 v41, v66, 16, 1
	v_add3_u32 v41, v66, v41, s33
	v_bfe_u32 v42, v67, 16, 1
	v_lshrrev_b32_e32 v41, 16, v41
	v_add3_u32 v42, v67, v42, s33
	v_and_or_b32 v41, v42, s29, v41
	global_store_dwordx2 v[34:35], v[40:41], off offset:1024
	v_bfe_u32 v40, v54, 16, 1
	v_add3_u32 v40, v54, v40, s33
	v_bfe_u32 v41, v55, 16, 1
	v_lshrrev_b32_e32 v40, 16, v40
	v_add3_u32 v41, v55, v41, s33
	v_and_or_b32 v40, v41, s29, v40
	v_bfe_u32 v41, v52, 16, 1
	v_add3_u32 v41, v52, v41, s33
	v_bfe_u32 v42, v53, 16, 1
	v_lshrrev_b32_e32 v41, 16, v41
	v_add3_u32 v42, v53, v42, s33
	v_and_or_b32 v41, v42, s29, v41
	global_store_dwordx2 v[34:35], v[40:41], off offset:1536
	v_bfe_u32 v40, v36, 16, 1
	v_add3_u32 v40, v36, v40, s33
	v_bfe_u32 v41, v37, 16, 1
	v_lshrrev_b32_e32 v40, 16, v40
	v_add3_u32 v41, v37, v41, s33
	v_and_or_b32 v40, v41, s29, v40
	v_bfe_u32 v41, v38, 16, 1
	v_add3_u32 v41, v38, v41, s33
	v_bfe_u32 v42, v39, 16, 1
	v_lshrrev_b32_e32 v41, 16, v41
	v_add3_u32 v42, v39, v42, s33
	v_and_or_b32 v41, v42, s29, v41
	global_store_dwordx2 v[34:35], v[40:41], off offset:2048
	v_bfe_u32 v40, v32, 16, 1
	v_add3_u32 v40, v32, v40, s33
	v_bfe_u32 v41, v33, 16, 1
	v_lshrrev_b32_e32 v40, 16, v40
	v_add3_u32 v41, v33, v41, s33
	v_and_or_b32 v40, v41, s29, v40
	v_bfe_u32 v41, v30, 16, 1
	v_add3_u32 v41, v30, v41, s33
	v_bfe_u32 v42, v31, 16, 1
	v_lshrrev_b32_e32 v41, 16, v41
	v_add3_u32 v42, v31, v42, s33
	v_pk_fma_f32 v[26:27], v[120:121], v[24:25], v[124:125]
	v_and_or_b32 v41, v42, s29, v41
	global_store_dwordx2 v[34:35], v[40:41], off offset:2560
	v_bfe_u32 v40, v26, 16, 1
	v_add3_u32 v40, v26, v40, s33
	v_bfe_u32 v41, v27, 16, 1
	v_lshrrev_b32_e32 v40, 16, v40
	v_add3_u32 v41, v27, v41, s33
	v_and_or_b32 v40, v41, s29, v40
	v_bfe_u32 v41, v28, 16, 1
	v_add3_u32 v41, v28, v41, s33
	v_bfe_u32 v42, v29, 16, 1
	v_lshrrev_b32_e32 v41, 16, v41
	v_add3_u32 v42, v29, v42, s33
	s_waitcnt vmcnt(6)
	v_pk_fma_f32 v[22:23], v[128:129], v[22:23], v[132:133]
	v_and_or_b32 v41, v42, s29, v41
	global_store_dwordx2 v[34:35], v[40:41], off offset:3072
	v_bfe_u32 v40, v22, 16, 1
	v_pk_mul_f32 v[24:25], v[50:51], v[138:139] op_sel_hi:[1,0]
	v_add3_u32 v40, v22, v40, s33
	v_bfe_u32 v41, v23, 16, 1
	v_pk_fma_f32 v[24:25], v[130:131], v[24:25], v[134:135]
	v_lshrrev_b32_e32 v40, 16, v40
	v_add3_u32 v41, v23, v41, s33
	v_and_or_b32 v40, v41, s29, v40
	v_bfe_u32 v41, v24, 16, 1
	v_add3_u32 v41, v24, v41, s33
	v_bfe_u32 v42, v25, 16, 1
	v_lshrrev_b32_e32 v41, 16, v41
	v_add3_u32 v42, v25, v42, s33
	v_and_or_b32 v41, v42, s29, v41
	global_store_dwordx2 v[34:35], v[40:41], off offset:3584
	v_lshl_add_u64 v[34:35], s[22:23], 0, v[62:63]
	v_lshl_add_u64 v[44:45], s[24:25], 0, v[62:63]
	global_load_dwordx4 v[40:43], v[34:35], off
	s_nop 0
	global_load_dwordx4 v[44:47], v[44:45], off
	v_lshlrev_b64 v[34:35], 2, v[58:59]
	v_lshl_add_u64 v[48:49], v[34:35], 0, s[4:5]
	v_lshl_add_u64 v[60:61], v[34:35], 0, s[8:9]
	v_lshl_add_u64 v[50:51], s[22:23], 0, v[48:49]
	v_lshl_add_u64 v[56:57], s[24:25], 0, v[48:49]
	v_lshl_add_u64 v[62:63], s[22:23], 0, v[60:61]
	v_lshl_add_u64 v[64:65], s[24:25], 0, v[60:61]
	global_load_dwordx4 v[48:51], v[50:51], off
	s_nop 0
	global_load_dwordx4 v[56:59], v[56:57], off
	s_nop 0
	global_load_dwordx4 v[60:63], v[62:63], off
	s_nop 0
	global_load_dwordx4 v[70:73], v[64:65], off
	v_lshl_add_u64 v[64:65], v[34:35], 0, s[10:11]
	v_lshl_add_u64 v[74:75], s[22:23], 0, v[64:65]
	v_lshl_add_u64 v[64:65], s[24:25], 0, v[64:65]
	global_load_dwordx4 v[74:77], v[74:75], off
	s_nop 0
	global_load_dwordx4 v[78:81], v[64:65], off
	v_lshl_add_u64 v[64:65], v[34:35], 0, s[12:13]
	v_lshl_add_u64 v[88:89], s[22:23], 0, v[64:65]
	v_lshl_add_u64 v[64:65], s[24:25], 0, v[64:65]
	global_load_dwordx4 v[88:91], v[88:89], off
	s_nop 0
	global_load_dwordx4 v[92:95], v[64:65], off
	v_lshl_add_u64 v[64:65], v[34:35], 0, s[14:15]
	v_lshl_add_u64 v[96:97], s[22:23], 0, v[64:65]
	v_lshl_add_u64 v[64:65], s[24:25], 0, v[64:65]
	global_load_dwordx4 v[96:99], v[96:97], off
	s_nop 0
	global_load_dwordx4 v[100:103], v[64:65], off
	v_lshl_add_u64 v[64:65], v[34:35], 0, s[16:17]
	v_lshl_add_u64 v[104:105], s[22:23], 0, v[64:65]
	v_lshl_add_u64 v[64:65], s[24:25], 0, v[64:65]
	v_lshl_add_u64 v[34:35], v[34:35], 0, s[18:19]
	global_load_dwordx4 v[104:107], v[104:105], off
	s_nop 0
	global_load_dwordx4 v[108:111], v[64:65], off
	v_lshl_add_u64 v[64:65], s[22:23], 0, v[34:35]
	v_lshl_add_u64 v[34:35], s[24:25], 0, v[34:35]
	global_load_dwordx4 v[112:115], v[64:65], off
	global_load_dwordx4 v[116:119], v[34:35], off
	s_waitcnt vmcnt(14)
; __device__ __forceinline__ void st_bf4(bf16* p, f32x4 v) { u32x2 w; w.x = pk2(v.x, v.y); w.y = pk2(v.z, v.w); *(u32x2*)p = w; }
; __device__ __forceinline__ f32x4 xr2f(XRaw w) { return (f32x4){bflo(w.x), bfhi(w.x), bflo(w.y), bfhi(w.y)}; }
; template <int L, bool ROUTER, bool WRITE_HB> __device__ __forceinline__ void p_ln_mix(const Args& a, LAS unsigned char* lds, XT* X) {
;     ...
;                 __builtin_amdgcn_sched_barrier(0);
; #pragma unroll
;                 for (int j = 0; j < 8; ++j) { const int k = j * 256 + lane * 4; const f32x4 hv = v[j] * (1.f + scv[j]) + shv[j];
;                     if (FFN8_GU) *(unsigned*)((unsigned char*)(a.ws + WS_HB) + (size_t)m * D + k) = pk4_fp8(hv.x, hv.y, hv.z, hv.w); else st_bf4(hb + k, hv); }
;                 __builtin_amdgcn_sched_barrier(0); }
;             if (ROUTER) {
;                 const float* md = mod + (size_t)(m >> 12) * D6;
;                 float lg[8] = {0.f, 0.f, 0.f, 0.f, 0.f, 0.f, 0.f, 0.f};
; #pragma unroll
;                 for (int j = 0; j < 8; ++j) { const int k = j * 256 + lane * 4; const f32x4 sh = *(const f32x4*)(md + 6144 + k), scf = *(const f32x4*)(md + 8192 + k); const f32x4 hv = v[j] * (1.f + scf) + sh;
; #pragma unroll
;                     for (int i = 0; i < 4; ++i) { const f32x4 w0 = *(const f32x4*)(wr + (size_t)(k + i) * 8), w1 = *(const f32x4*)(wr + (size_t)(k + i) * 8 + 4); const float hx = hv[i];
;                         lg[0] += hx * w0.x; lg[1] += hx * w0.y; lg[2] += hx * w0.z; lg[3] += hx * w0.w; lg[4] += hx * w1.x; lg[5] += hx * w1.y; lg[6] += hx * w1.z; lg[7] += hx * w1.w; } }
; #pragma unroll
;                 for (int e = 0; e < 8; ++e) lg[e] = wave_sum(lg[e]);
;                 int i0 = 0; float v0 = lg[0];
; #pragma unroll
;                 for (int e = 1; e < 8; ++e) if (lg[e] > v0) { v0 = lg[e]; i0 = e; }
;                 int i1 = -1; float v1 = -INFINITY;
; #pragma unroll
;                 for (int e = 0; e < 8; ++e) if (e != i0 && lg[e] > v1) { v1 = lg[e]; i1 = e; }
;                 const float ex = __expf(v1 - v0), w0 = 1.f / (1.f + ex), w1 = ex / (1.f + ex);
;                 if (lane == 0) { route_e[m * 2] = i0; route_e[m * 2 + 1] = i1; route_w[m * 2] = w0; route_w[m * 2 + 1] = w1; el[(wave * 8 + r) * 2] = i0; el[(wave * 8 + r) * 2 + 1] = i1; }
;             }
; #pragma unroll
;             for (int j = 0; j < 8; ++j) v[j] = xr2f(vn[j]);
	v_pk_add_f32 v[34:35], v[44:45], 1.0 op_sel_hi:[1,0]
	v_mov_b32_e32 v44, 0
	v_pk_fma_f32 v[34:35], v[142:143], v[34:35], v[40:41]
	s_add_u32 s6, s66, s26
	v_cvt_pk_fp8_f32 v44, v34, v35
	v_pk_add_f32 v[34:35], v[46:47], 1.0 op_sel_hi:[1,0]
	s_addc_u32 s7, s67, s27
	v_pk_fma_f32 v[34:35], v[140:141], v[34:35], v[42:43]
	s_waitcnt vmcnt(12)
	v_pk_add_f32 v[40:41], v[56:57], 1.0 op_sel_hi:[1,0]
	v_cvt_pk_fp8_f32 v44, v34, v35 op_sel:[0,0,1]
	v_lshl_add_u64 v[34:35], s[6:7], 0, v[20:21]
	v_pk_fma_f32 v[40:41], v[136:137], v[40:41], v[48:49]
	v_mov_b32_e32 v42, 0
	v_add_co_u32_e32 v34, vcc, s35, v34
	v_cvt_pk_fp8_f32 v42, v40, v41
	s_waitcnt vmcnt(10)
	v_pk_add_f32 v[40:41], v[70:71], 1.0 op_sel_hi:[1,0]
	v_addc_co_u32_e32 v35, vcc, 0, v35, vcc
	v_pk_fma_f32 v[40:41], v[68:69], v[40:41], v[60:61]
	v_mov_b32_e32 v43, 0
	global_store_dword v[34:35], v44, off
	v_pk_add_f32 v[34:35], v[58:59], 1.0 op_sel_hi:[1,0]
	v_cvt_pk_fp8_f32 v43, v40, v41
	s_waitcnt vmcnt(9)
	v_pk_add_f32 v[40:41], v[78:79], 1.0 op_sel_hi:[1,0]
	v_pk_fma_f32 v[34:35], v[82:83], v[34:35], v[50:51]
	v_pk_fma_f32 v[40:41], v[54:55], v[40:41], v[74:75]
	v_mov_b32_e32 v44, 0
	v_cvt_pk_fp8_f32 v42, v34, v35 op_sel:[0,0,1]
	v_pk_add_f32 v[34:35], v[72:73], 1.0 op_sel_hi:[1,0]
	v_cvt_pk_fp8_f32 v44, v40, v41
	v_pk_fma_f32 v[34:35], v[66:67], v[34:35], v[62:63]
	s_waitcnt vmcnt(7)
	v_pk_add_f32 v[40:41], v[92:93], 1.0 op_sel_hi:[1,0]
	v_cvt_pk_fp8_f32 v43, v34, v35 op_sel:[0,0,1]
	v_pk_add_f32 v[34:35], v[80:81], 1.0 op_sel_hi:[1,0]
	v_pk_fma_f32 v[36:37], v[36:37], v[40:41], v[88:89]
	v_pk_fma_f32 v[34:35], v[52:53], v[34:35], v[76:77]
	v_lshl_add_u64 v[20:21], s[6:7], 0, v[20:21]
	v_cvt_pk_fp8_f32 v44, v34, v35 op_sel:[0,0,1]
	v_pk_add_f32 v[34:35], v[94:95], 1.0 op_sel_hi:[1,0]
	v_add_co_u32_e32 v20, vcc, s35, v20
	v_pk_fma_f32 v[34:35], v[38:39], v[34:35], v[90:91]
	v_mov_b32_e32 v38, 0
	v_cvt_pk_fp8_f32 v38, v36, v37
	s_waitcnt vmcnt(5)
	v_pk_add_f32 v[36:37], v[100:101], 1.0 op_sel_hi:[1,0]
	v_addc_co_u32_e32 v21, vcc, 0, v21, vcc
	v_pk_fma_f32 v[32:33], v[32:33], v[36:37], v[96:97]
	v_mov_b32_e32 v36, 0
	v_cvt_pk_fp8_f32 v36, v32, v33
	v_pk_add_f32 v[32:33], v[102:103], 1.0 op_sel_hi:[1,0]
	v_cvt_pk_fp8_f32 v38, v34, v35 op_sel:[0,0,1]
	v_pk_fma_f32 v[30:31], v[30:31], v[32:33], v[98:99]
	s_waitcnt vmcnt(3)
	v_pk_add_f32 v[32:33], v[108:109], 1.0 op_sel_hi:[1,0]
	v_cvt_pk_fp8_f32 v36, v30, v31 op_sel:[0,0,1]
	v_pk_add_f32 v[30:31], v[110:111], 1.0 op_sel_hi:[1,0]
	v_pk_fma_f32 v[26:27], v[26:27], v[32:33], v[104:105]
	v_pk_fma_f32 v[28:29], v[28:29], v[30:31], v[106:107]
	v_mov_b32_e32 v30, 0
	v_cvt_pk_fp8_f32 v30, v26, v27
	s_waitcnt vmcnt(1)
	v_pk_add_f32 v[26:27], v[116:117], 1.0 op_sel_hi:[1,0]
	global_store_dword v[20:21], v42, off offset:256
	global_store_dword v[20:21], v43, off offset:512
	global_store_dword v[20:21], v44, off offset:768
	v_pk_fma_f32 v[22:23], v[22:23], v[26:27], v[112:113]
	v_mov_b32_e32 v26, 0
	v_cvt_pk_fp8_f32 v26, v22, v23
	v_pk_add_f32 v[22:23], v[118:119], 1.0 op_sel_hi:[1,0]
	v_cvt_pk_fp8_f32 v30, v28, v29 op_sel:[0,0,1]
	v_pk_fma_f32 v[22:23], v[24:25], v[22:23], v[114:115]
	s_nop 0
	v_cvt_pk_fp8_f32 v26, v22, v23 op_sel:[0,0,1]
	global_store_dword v[20:21], v38, off offset:1024
	global_store_dword v[20:21], v36, off offset:1280
	global_store_dword v[20:21], v30, off offset:1536
	global_store_dword v[20:21], v26, off offset:1792
	s_add_i32 s37, s37, -1
	s_add_u32 s20, s20, 0x1000
	s_addc_u32 s21, s21, 0
	s_add_u32 s26, s26, 0x800
	s_addc_u32 s27, s27, 0
	v_lshlrev_b32_e32 v53, 16, v6
	v_and_b32_e32 v55, 0xffff0000, v6
	v_lshlrev_b32_e32 v33, 16, v7
	v_and_b32_e32 v37, 0xffff0000, v7
	v_lshlrev_b32_e32 v52, 16, v8
	v_and_b32_e32 v54, 0xffff0000, v8
	v_lshlrev_b32_e32 v32, 16, v9
	v_and_b32_e32 v36, 0xffff0000, v9
	v_lshlrev_b32_e32 v22, 16, v10
	v_and_b32_e32 v64, 0xffff0000, v10
	v_lshlrev_b32_e32 v65, 16, v11
	v_and_b32_e32 v23, 0xffff0000, v11
	v_lshlrev_b32_e32 v24, 16, v12
	v_and_b32_e32 v25, 0xffff0000, v12
	v_lshlrev_b32_e32 v28, 16, v13
	v_and_b32_e32 v29, 0xffff0000, v13
	v_lshlrev_b32_e32 v26, 16, v14
	v_and_b32_e32 v30, 0xffff0000, v14
	v_lshlrev_b32_e32 v38, 16, v15
	v_and_b32_e32 v44, 0xffff0000, v15
	v_lshlrev_b32_e32 v34, 16, v16
	v_and_b32_e32 v62, 0xffff0000, v16
	v_lshlrev_b32_e32 v63, 16, v17
	v_and_b32_e32 v35, 0xffff0000, v17
	v_lshlrev_b32_e32 v40, 16, v18
	v_and_b32_e32 v41, 0xffff0000, v18
	v_lshlrev_b32_e32 v48, 16, v19
	v_and_b32_e32 v49, 0xffff0000, v19
	v_lshlrev_b32_e32 v42, 16, v4
	v_and_b32_e32 v46, 0xffff0000, v4
	v_lshlrev_b32_e32 v50, 16, v5
	s_cmp_eq_u32 s37, 0
	v_and_b32_e32 v56, 0xffff0000, v5
	s_cbranch_scc1 .LBB0_1070
	v_mov_b64_e32 v[66:67], v[6:7]
	v_mov_b64_e32 v[68:69], v[8:9]
	v_mov_b64_e32 v[70:71], v[10:11]
	v_mov_b64_e32 v[72:73], v[12:13]
	v_mov_b64_e32 v[74:75], v[14:15]
	v_mov_b64_e32 v[76:77], v[16:17]
	v_mov_b64_e32 v[78:79], v[18:19]
	s_branch .LBB0_1072

; __device__ __forceinline__ void ln_regs(f32x4 (&v)[8], const float* g, const float* bt, int lane) {
;     float s = 0.f;
; #pragma unroll
;     for (int j = 0; j < 8; ++j) s += (v[j].x + v[j].y) + (v[j].z + v[j].w);
;     const float mean = wave_sum(s) * (1.f / D); float s2 = 0.f;
; #pragma unroll
;     for (int j = 0; j < 8; ++j) { v[j] = v[j] - mean; s2 += (v[j].x * v[j].x + v[j].y * v[j].y) + (v[j].z * v[j].z + v[j].w * v[j].w); }
;     const float rstd = 1.f / sqrtf(wave_sum(s2) * (1.f / D) + LN_EPS);
; template <int L, bool NEXT_HB> __device__ __forceinline__ void p_ln_ffn(const Args& a, XT* X) {
;     ...
;     for (int m = gw; m < M; m += NGW) { int lane = lane_; asm volatile("" : "+v"(lane)); XT* xr = X + (size_t)m * D; const int mn = m + NGW;
;         if (mn < M) {
; #pragma unroll
;             for (int j = 0; j < 8; ++j) vn[j] = ldxr(X + (size_t)mn * D + j * 256 + lane * 4); }
;         ln_regs(v, g, bt, lane);
.LBB0_1289:
	v_pk_add_f32 v[62:63], v[48:49], v[50:51]
	v_pk_add_f32 v[68:69], v[28:29], v[32:33]
	v_add_f32_e32 v27, v24, v25
	v_pk_add_f32 v[62:63], v[62:63], v[68:69]
	v_add_f32_e32 v39, v36, v37
	v_add_f32_e32 v23, 0, v63
	v_add_f32_e32 v41, v62, v23
	v_pk_add_f32 v[62:63], v[60:61], v[18:19]
	v_add_f32_e32 v23, v20, v21
	v_pk_add_f32 v[62:63], v[62:63], v[62:63] op_sel_hi:[0,1]
	v_mov_b32_e32 v35, v63
	v_pk_add_f32 v[68:69], v[22:23], v[26:27]
	v_pk_add_f32 v[62:63], v[34:35], v[40:41]
	v_and_b32_e32 v27, 64, v66
	v_pk_add_f32 v[62:63], v[68:69], v[62:63]
	v_pk_add_f32 v[68:69], v[58:59], v[30:31]
	v_pk_add_f32 v[62:63], v[62:63], v[62:63] op_sel_hi:[0,1]
	v_pk_add_f32 v[68:69], v[68:69], v[68:69] op_sel_hi:[0,1]
	v_add_f32_e32 v43, v44, v45
	v_mov_b32_e32 v47, v69
	v_mov_b32_e32 v53, v63
	v_add_u32_e32 v27, 64, v27
	v_xor_b32_e32 v35, 1, v66
	v_pk_add_f32 v[70:71], v[38:39], v[42:43]
	v_pk_add_f32 v[62:63], v[46:47], v[52:53]
	v_cmp_lt_i32_e32 vcc, v35, v27
	v_pk_add_f32 v[62:63], v[70:71], v[62:63]
	s_ashr_i32 s3, s24, 12
	v_cndmask_b32_e32 v35, v66, v35, vcc
	v_add_f32_e32 v23, v62, v63
	v_lshlrev_b32_e32 v35, 2, v35
	v_ashrrev_i32_e32 v55, 31, v54
	s_waitcnt lgkmcnt(0)
	s_nop 1
	v_add_f32_dpp v23, v23, v23 quad_perm:[1,0,3,2] row_mask:0xf bank_mask:0xf
	v_xor_b32_e32 v39, 2, v66
	v_cmp_lt_i32_e32 vcc, v39, v27
	s_nop 1
	v_cndmask_b32_e32 v39, v66, v39, vcc
	v_lshlrev_b32_e32 v39, 2, v39
	s_waitcnt lgkmcnt(0)
	s_nop 1
	v_add_f32_dpp v23, v23, v23 quad_perm:[2,3,0,1] row_mask:0xf bank_mask:0xf
	v_xor_b32_e32 v41, 4, v66
	v_cmp_lt_i32_e32 vcc, v41, v27
	s_nop 1
	v_cndmask_b32_e32 v41, v66, v41, vcc
	v_lshlrev_b32_e32 v41, 2, v41
	s_waitcnt lgkmcnt(0)
	s_nop 1
	v_add_f32_dpp v23, v23, v23 row_half_mirror row_mask:0xf bank_mask:0xf
	v_xor_b32_e32 v43, 8, v66
	v_cmp_lt_i32_e32 vcc, v43, v27
	s_nop 1
	v_cndmask_b32_e32 v43, v66, v43, vcc
	v_lshlrev_b32_e32 v43, 2, v43
	s_waitcnt lgkmcnt(0)
	s_nop 1
	v_add_f32_dpp v23, v23, v23 row_mirror row_mask:0xf bank_mask:0xf
	v_xor_b32_e32 v47, 16, v66
	v_cmp_lt_i32_e32 vcc, v47, v27
	s_nop 1
	v_cndmask_b32_e32 v47, v66, v47, vcc
	v_lshlrev_b32_e32 v47, 2, v47
	ds_bpermute_b32 v53, v47, v23
	s_waitcnt lgkmcnt(0)
	v_add_f32_e32 v23, v23, v53
	v_xor_b32_e32 v53, 32, v66
	v_cmp_lt_i32_e32 vcc, v53, v27
	s_nop 1
	v_cndmask_b32_e32 v27, v66, v53, vcc
	v_lshlrev_b32_e32 v27, 2, v27
	ds_bpermute_b32 v53, v27, v23
	s_waitcnt lgkmcnt(0)
	v_add_f32_e32 v23, v23, v53
	v_fmac_f32_e32 v51, 0xba000000, v23
	v_fmac_f32_e32 v50, 0xba000000, v23
	v_fmac_f32_e32 v33, 0xba000000, v23
	v_fmac_f32_e32 v49, 0xba000000, v23
	v_fmac_f32_e32 v32, 0xba000000, v23
	v_fmac_f32_e32 v48, 0xba000000, v23
	v_mov_b32_e32 v68, v51
	v_mov_b32_e32 v69, v50
	v_fmac_f32_e32 v29, 0xba000000, v23
	v_fmac_f32_e32 v28, 0xba000000, v23
	v_mov_b32_e32 v62, v49
	v_mov_b32_e32 v63, v48
	v_pk_mul_f32 v[68:69], v[68:69], v[68:69]
	v_mov_b32_e32 v70, v33
	v_mov_b32_e32 v71, v32
	v_pk_fma_f32 v[62:63], v[62:63], v[62:63], v[68:69]
	v_mov_b32_e32 v68, v29
	v_mov_b32_e32 v69, v28
	v_pk_mul_f32 v[70:71], v[70:71], v[70:71]
	v_fmac_f32_e32 v60, 0xba000000, v23
	v_pk_fma_f32 v[68:69], v[68:69], v[68:69], v[70:71]
	v_fmac_f32_e32 v19, 0xba000000, v23
	v_pk_add_f32 v[62:63], v[62:63], v[68:69]
	v_fmac_f32_e32 v61, 0xba000000, v23
	v_pk_add_f32 v[68:69], v[62:63], v[62:63] op_sel_hi:[0,1]
	v_fmac_f32_e32 v18, 0xba000000, v23
	v_mov_b32_e32 v62, v61
	v_mov_b32_e32 v63, v19
	v_mov_b32_e32 v19, v60
	v_pk_mul_f32 v[70:71], v[62:63], v[62:63]
	v_pk_mul_f32 v[60:61], v[18:19], v[18:19]
	v_fmac_f32_e32 v20, 0xba000000, v23
	v_pk_mov_b32 v[72:73], v[60:61], v[70:71] op_sel:[1,0]
	v_mov_b32_e32 v61, v71
	v_pk_add_f32 v[60:61], v[72:73], v[60:61]
	v_fmac_f32_e32 v21, 0xba000000, v23
	v_pk_add_f32 v[60:61], v[60:61], v[60:61] op_sel_hi:[0,1]
	v_fmac_f32_e32 v24, 0xba000000, v23
	v_mul_f32_e32 v60, v20, v20
	v_fmac_f32_e32 v25, 0xba000000, v23
	v_pk_fma_f32 v[70:71], v[20:21], v[20:21], v[60:61] op_sel_hi:[1,1,0]
	v_mul_f32_e32 v60, v24, v24
	v_pk_fma_f32 v[72:73], v[24:25], v[24:25], v[60:61] op_sel_hi:[1,1,0]
	v_fmac_f32_e32 v40, 0xba000000, v23
	v_fmac_f32_e32 v34, 0xba000000, v23
	v_fmac_f32_e32 v26, 0xba000000, v23
	v_fmac_f32_e32 v22, 0xba000000, v23
	v_fmac_f32_e32 v58, 0xba000000, v23
	v_fmac_f32_e32 v31, 0xba000000, v23
	v_fmac_f32_e32 v59, 0xba000000, v23
	v_mul_f32_e32 v70, v22, v22
	v_mul_f32_e32 v72, v26, v26
	v_mul_f32_e32 v60, v34, v34
	v_mul_f32_e32 v68, v40, v40
	v_fmac_f32_e32 v30, 0xba000000, v23
	v_mov_b32_e32 v132, v59
	v_mov_b32_e32 v133, v31
	v_mov_b32_e32 v31, v58
	v_pk_add_f32 v[70:71], v[70:71], v[72:73]
	v_pk_add_f32 v[60:61], v[60:61], v[68:69]
	v_pk_mul_f32 v[68:69], v[132:133], v[132:133]
	v_pk_mul_f32 v[58:59], v[30:31], v[30:31]
	v_pk_add_f32 v[60:61], v[70:71], v[60:61]
	v_pk_mov_b32 v[70:71], v[58:59], v[68:69] op_sel:[1,0]
	v_mov_b32_e32 v59, v69
	v_pk_add_f32 v[58:59], v[70:71], v[58:59]
	v_fmac_f32_e32 v36, 0xba000000, v23
	v_pk_add_f32 v[58:59], v[58:59], v[58:59] op_sel_hi:[0,1]
	v_fmac_f32_e32 v37, 0xba000000, v23
	v_fmac_f32_e32 v44, 0xba000000, v23
	v_mul_f32_e32 v58, v36, v36
	v_fmac_f32_e32 v45, 0xba000000, v23
	v_pk_fma_f32 v[68:69], v[36:37], v[36:37], v[58:59] op_sel_hi:[1,1,0]
	v_mul_f32_e32 v58, v44, v44
	v_pk_add_f32 v[60:61], v[60:61], v[60:61] op_sel_hi:[0,1]
	v_pk_fma_f32 v[70:71], v[44:45], v[44:45], v[58:59] op_sel_hi:[1,1,0]
	v_fmac_f32_e32 v52, 0xba000000, v23
	v_fmac_f32_e32 v46, 0xba000000, v23
	v_fmac_f32_e32 v42, 0xba000000, v23
	v_fmac_f32_e32 v38, 0xba000000, v23
	v_mul_f32_e32 v68, v38, v38
	v_mul_f32_e32 v70, v42, v42
	v_mul_f32_e32 v58, v46, v46
	v_mul_f32_e32 v60, v52, v52
	v_pk_add_f32 v[68:69], v[68:69], v[70:71]
	v_pk_add_f32 v[58:59], v[58:59], v[60:61]
	s_nop 0
	v_pk_add_f32 v[58:59], v[68:69], v[58:59]
	s_nop 0
	v_add_f32_e32 v23, v58, v59
	v_lshlrev_b64 v[58:59], 2, v[56:57]
	v_lshl_add_u64 v[60:61], s[82:83], 0, v[58:59]
	v_lshl_add_u64 v[104:105], s[84:85], 0, v[58:59]
	global_load_dwordx4 v[68:71], v[60:61], off
	global_load_dwordx4 v[72:75], v[104:105], off
	global_load_dwordx4 v[76:79], v[60:61], off offset:1024
	global_load_dwordx4 v[80:83], v[104:105], off offset:1024
	global_load_dwordx4 v[84:87], v[60:61], off offset:2048
	global_load_dwordx4 v[88:91], v[60:61], off offset:3072
	global_load_dwordx4 v[92:95], v[104:105], off offset:2048
	global_load_dwordx4 v[96:99], v[104:105], off offset:3072
	v_add_co_u32_e32 v60, vcc, s29, v60
	s_nop 0
	v_addc_co_u32_e32 v61, vcc, 0, v61, vcc
	v_add_co_u32_e32 v128, vcc, s29, v104
	global_load_dwordx4 v[100:103], v[60:61], off
	s_nop 0
	v_addc_co_u32_e32 v129, vcc, 0, v105, vcc
	global_load_dwordx4 v[104:107], v[128:129], off
	global_load_dwordx4 v[108:111], v[60:61], off offset:1024
	global_load_dwordx4 v[112:115], v[128:129], off offset:1024
	global_load_dwordx4 v[116:119], v[60:61], off offset:2048
	global_load_dwordx4 v[120:123], v[128:129], off offset:2048
	global_load_dwordx4 v[124:127], v[60:61], off offset:3072
	s_nop 0
	global_load_dwordx4 v[128:131], v[128:129], off offset:3072
	s_waitcnt lgkmcnt(0)
; __device__ __forceinline__ void stx4(XT* p, f32x4 v) { st_bf4(p, v); }
; __device__ __forceinline__ void ln_regs(f32x4 (&v)[8], const float* g, const float* bt, int lane) {
;     ...
;     const float mean = wave_sum(s) * (1.f / D); float s2 = 0.f;
; #pragma unroll
;     for (int j = 0; j < 8; ++j) { v[j] = v[j] - mean; s2 += (v[j].x * v[j].x + v[j].y * v[j].y) + (v[j].z * v[j].z + v[j].w * v[j].w); }
;     const float rstd = 1.f / sqrtf(wave_sum(s2) * (1.f / D) + LN_EPS);
; #pragma unroll
;     for (int j = 0; j < 8; ++j) { const f32x4 gv = *(const f32x4*)(g + j * 256 + lane * 4), bv = *(const f32x4*)(bt + j * 256 + lane * 4); v[j] = v[j] * rstd * gv + bv; }
; template <int L, bool NEXT_HB> __device__ __forceinline__ void p_ln_ffn(const Args& a, XT* X) {
;     ...
;         ln_regs(v, g, bt, lane);
; #pragma unroll
;         for (int j = 0; j < 8; ++j) stx4(xr + j * 256 + lane * 4, v[j]);
	s_nop 1
	v_add_f32_dpp v23, v23, v23 quad_perm:[1,0,3,2] row_mask:0xf bank_mask:0xf
	v_mov_b32_e32 v60, v48
	v_mov_b32_e32 v48, v28
	v_mov_b32_e32 v61, v50
	v_mov_b32_e32 v50, v49
	s_waitcnt lgkmcnt(0)
	s_nop 1
	v_add_f32_dpp v23, v23, v23 quad_perm:[2,3,0,1] row_mask:0xf bank_mask:0xf
	v_mov_b32_e32 v49, v32
	v_mov_b32_e32 v32, v29
	s_waitcnt lgkmcnt(0)
	s_nop 1
	v_add_f32_dpp v23, v23, v23 row_half_mirror row_mask:0xf bank_mask:0xf
	s_waitcnt lgkmcnt(0)
	s_nop 1
	v_add_f32_dpp v23, v23, v23 row_mirror row_mask:0xf bank_mask:0xf
	ds_bpermute_b32 v35, v47, v23
	v_mov_b32_e32 v47, v52
	s_waitcnt lgkmcnt(0)
	v_add_f32_e32 v23, v23, v35
	ds_bpermute_b32 v27, v27, v23
	s_waitcnt lgkmcnt(0)
	v_add_f32_e32 v23, v23, v27
	v_fmamk_f32 v23, v23, 0x3a000000, v64
	v_mul_f32_e32 v27, 0x4f800000, v23
	v_cmp_gt_f32_e32 vcc, s28, v23
	s_nop 1
	v_cndmask_b32_e32 v23, v23, v27, vcc
	v_sqrt_f32_e32 v27, v23
	s_nop 0
	v_add_u32_e32 v28, -1, v27
	v_fma_f32 v35, -v28, v27, v23
	v_cmp_ge_f32_e64 s[6:7], 0, v35
	v_add_u32_e32 v35, 1, v27
	s_nop 0
	v_cndmask_b32_e64 v28, v27, v28, s[6:7]
	v_fma_f32 v27, -v35, v27, v23
	v_cmp_lt_f32_e64 s[6:7], 0, v27
	s_nop 1
	v_cndmask_b32_e64 v27, v28, v35, s[6:7]
	v_mul_f32_e32 v28, 0x37800000, v27
	v_cndmask_b32_e32 v27, v27, v28, vcc
	v_cmp_class_f32_e32 vcc, v23, v65
	s_nop 1
	v_cndmask_b32_e32 v23, v27, v23, vcc
	v_div_scale_f32 v27, s[6:7], v23, v23, 1.0
	v_rcp_f32_e32 v28, v27
	s_mul_hi_i32 s7, s3, 0xc000
	s_mul_i32 s3, s3, 0xc000
	s_add_u32 s6, s26, s3
	v_fma_f32 v29, -v27, v28, 1.0
	v_fmac_f32_e32 v28, v29, v28
	v_div_scale_f32 v29, vcc, 1.0, v23, 1.0
	v_mul_f32_e32 v35, v29, v28
	v_fma_f32 v39, -v27, v35, v29
	v_fmac_f32_e32 v35, v39, v28
	v_fma_f32 v27, -v27, v35, v29
	v_div_fmas_f32 v27, v27, v28, v35
	v_div_fixup_f32 v134, v27, v23, 1.0
	v_pk_mul_f32 v[28:29], v[50:51], v[134:135] op_sel_hi:[1,0]
	v_pk_mul_f32 v[32:33], v[32:33], v[134:135] op_sel_hi:[1,0]
	v_pk_mul_f32 v[20:21], v[20:21], v[134:135] op_sel_hi:[1,0]
	v_mov_b32_e32 v23, v26
	s_waitcnt vmcnt(14)
	v_pk_fma_f32 v[136:137], v[70:71], v[32:33], v[74:75]
	v_pk_fma_f32 v[138:139], v[68:69], v[28:29], v[72:73]
	v_pk_mul_f32 v[28:29], v[60:61], v[134:135] op_sel_hi:[1,0]
	v_pk_mul_f32 v[32:33], v[48:49], v[134:135] op_sel_hi:[1,0]
	s_waitcnt vmcnt(8)
	v_pk_fma_f32 v[48:49], v[88:89], v[20:21], v[96:97]
	v_pk_mul_f32 v[20:21], v[22:23], v[134:135] op_sel_hi:[1,0]
	v_pk_fma_f32 v[140:141], v[78:79], v[32:33], v[82:83]
	v_pk_fma_f32 v[142:143], v[76:77], v[28:29], v[80:81]
	v_pk_mul_f32 v[18:19], v[18:19], v[134:135] op_sel_hi:[1,0]
	v_pk_mul_f32 v[28:29], v[62:63], v[134:135] op_sel_hi:[1,0]
	s_waitcnt vmcnt(6)
	v_pk_fma_f32 v[32:33], v[100:101], v[20:21], v[104:105]
	v_pk_mul_f32 v[20:21], v[30:31], v[134:135] op_sel_hi:[1,0]
	v_pk_fma_f32 v[60:61], v[86:87], v[28:29], v[94:95]
	v_pk_fma_f32 v[62:63], v[84:85], v[18:19], v[92:93]
	v_pk_mul_f32 v[18:19], v[24:25], v[134:135] op_sel_hi:[1,0]
	v_mov_b32_e32 v35, v40
	s_waitcnt vmcnt(4)
	v_pk_fma_f32 v[28:29], v[108:109], v[20:21], v[112:113]
	v_pk_mul_f32 v[20:21], v[36:37], v[134:135] op_sel_hi:[1,0]
	v_bfe_u32 v36, v138, 16, 1
	v_pk_fma_f32 v[50:51], v[90:91], v[18:19], v[98:99]
	v_pk_mul_f32 v[18:19], v[34:35], v[134:135] op_sel_hi:[1,0]
	v_add3_u32 v36, v138, v36, s30
	v_bfe_u32 v37, v139, 16, 1
	v_pk_fma_f32 v[34:35], v[102:103], v[18:19], v[106:107]
	v_pk_mul_f32 v[18:19], v[132:133], v[134:135] op_sel_hi:[1,0]
	v_lshrrev_b32_e32 v36, 16, v36
	v_add3_u32 v37, v139, v37, s30
	v_pk_fma_f32 v[30:31], v[110:111], v[18:19], v[114:115]
	v_pk_mul_f32 v[18:19], v[44:45], v[134:135] op_sel_hi:[1,0]
	v_mov_b32_e32 v39, v42
	v_and_or_b32 v36, v37, s25, v36
	v_bfe_u32 v37, v136, 16, 1
	s_waitcnt vmcnt(2)
	v_pk_fma_f32 v[24:25], v[116:117], v[20:21], v[120:121]
	v_pk_fma_f32 v[26:27], v[118:119], v[18:19], v[122:123]
	v_pk_mul_f32 v[18:19], v[46:47], v[134:135] op_sel_hi:[1,0]
	v_pk_mul_f32 v[20:21], v[38:39], v[134:135] op_sel_hi:[1,0]
	v_add3_u32 v37, v136, v37, s30
	v_bfe_u32 v38, v137, 16, 1
	s_waitcnt vmcnt(0)
	v_pk_fma_f32 v[22:23], v[126:127], v[18:19], v[130:131]
	v_lshl_add_u64 v[18:19], v[56:57], 1, s[14:15]
	v_lshrrev_b32_e32 v37, 16, v37
	v_add3_u32 v38, v137, v38, s30
	v_and_or_b32 v37, v38, s25, v37
	v_add_co_u32_e32 v38, vcc, s31, v18
	v_bfe_u32 v40, v61, 16, 1
	s_nop 0
	v_addc_co_u32_e32 v39, vcc, -1, v19, vcc
	global_store_dwordx2 v[38:39], v[36:37], off
	v_bfe_u32 v36, v142, 16, 1
	v_add3_u32 v36, v142, v36, s30
	v_bfe_u32 v37, v143, 16, 1
	v_lshrrev_b32_e32 v36, 16, v36
	v_add3_u32 v37, v143, v37, s30
	v_and_or_b32 v36, v37, s25, v36
	v_bfe_u32 v37, v140, 16, 1
	v_add3_u32 v37, v140, v37, s30
	v_bfe_u32 v38, v141, 16, 1
	v_lshrrev_b32_e32 v37, 16, v37
	v_add3_u32 v38, v141, v38, s30
	v_and_or_b32 v37, v38, s25, v37
	v_add_co_u32_e32 v38, vcc, s33, v18
	v_add3_u32 v40, v61, v40, s30
	s_nop 0
	v_addc_co_u32_e32 v39, vcc, -1, v19, vcc
	global_store_dwordx2 v[38:39], v[36:37], off offset:-3584
	v_bfe_u32 v36, v62, 16, 1
	v_add3_u32 v36, v62, v36, s30
	v_bfe_u32 v37, v63, 16, 1
	v_lshrrev_b32_e32 v36, 16, v36
	v_add3_u32 v37, v63, v37, s30
	v_and_or_b32 v36, v37, s25, v36
	v_bfe_u32 v37, v60, 16, 1
	v_add3_u32 v37, v60, v37, s30
	v_lshrrev_b32_e32 v37, 16, v37
	v_and_or_b32 v37, v40, s25, v37
	global_store_dwordx2 v[38:39], v[36:37], off offset:-3072
	v_bfe_u32 v36, v48, 16, 1
	v_add3_u32 v36, v48, v36, s30
	v_bfe_u32 v37, v49, 16, 1
	v_lshrrev_b32_e32 v36, 16, v36
	v_add3_u32 v37, v49, v37, s30
	v_and_or_b32 v36, v37, s25, v36
	v_bfe_u32 v37, v50, 16, 1
	v_add3_u32 v37, v50, v37, s30
	v_bfe_u32 v40, v51, 16, 1
	v_lshrrev_b32_e32 v37, 16, v37
	v_add3_u32 v40, v51, v40, s30
	v_and_or_b32 v37, v40, s25, v37
; __device__ __forceinline__ void st_bf4(bf16* p, f32x4 v) { u32x2 w; w.x = pk2(v.x, v.y); w.y = pk2(v.z, v.w); *(u32x2*)p = w; }
; __device__ __forceinline__ f32x4 xr2f(XRaw w) { return (f32x4){bflo(w.x), bfhi(w.x), bflo(w.y), bfhi(w.y)}; }
; __device__ __forceinline__ void stx4(XT* p, f32x4 v) { st_bf4(p, v); }
; template <int L, bool NEXT_HB> __device__ __forceinline__ void p_ln_ffn(const Args& a, XT* X) {
;     ...
;         for (int j = 0; j < 8; ++j) stx4(xr + j * 256 + lane * 4, v[j]);
;         if (NEXT_HB) { const float* md = modn + (size_t)(m >> 12) * D6; bf16* hb = (bf16*)(a.ws + WS_HB) + (size_t)m * D; f32x4 shv[8], scv[8];
; #pragma unroll
;             for (int j = 0; j < 8; ++j) { const int k = j * 256 + lane * 4; shv[j] = *(const f32x4*)(md + k); scv[j] = *(const f32x4*)(md + 2048 + k); }
;             __builtin_amdgcn_sched_barrier(0);
; #pragma unroll
;             for (int j = 0; j < 8; ++j) st_bf4(hb + j * 256 + lane * 4, v[j] * (1.f + scv[j]) + shv[j]);
;             __builtin_amdgcn_sched_barrier(0); }
; #pragma unroll
;         for (int j = 0; j < 8; ++j) v[j] = xr2f(vn[j]); }
	global_store_dwordx2 v[38:39], v[36:37], off offset:-2560
	v_bfe_u32 v36, v32, 16, 1
	v_add3_u32 v36, v32, v36, s30
	v_bfe_u32 v37, v33, 16, 1
	v_lshrrev_b32_e32 v36, 16, v36
	v_add3_u32 v37, v33, v37, s30
	v_and_or_b32 v36, v37, s25, v36
	v_bfe_u32 v37, v34, 16, 1
	v_add3_u32 v37, v34, v37, s30
	v_bfe_u32 v40, v35, 16, 1
	v_lshrrev_b32_e32 v37, 16, v37
	v_add3_u32 v40, v35, v40, s30
	v_and_or_b32 v37, v40, s25, v37
	global_store_dwordx2 v[38:39], v[36:37], off offset:-2048
	v_bfe_u32 v36, v28, 16, 1
	v_add3_u32 v36, v28, v36, s30
	v_bfe_u32 v37, v29, 16, 1
	v_lshrrev_b32_e32 v36, 16, v36
	v_add3_u32 v37, v29, v37, s30
	v_and_or_b32 v36, v37, s25, v36
	v_bfe_u32 v37, v30, 16, 1
	v_add3_u32 v37, v30, v37, s30
	v_bfe_u32 v40, v31, 16, 1
	v_lshrrev_b32_e32 v37, 16, v37
	v_add3_u32 v40, v31, v40, s30
	v_and_or_b32 v37, v40, s25, v37
	global_store_dwordx2 v[38:39], v[36:37], off offset:-1536
	v_bfe_u32 v36, v24, 16, 1
	v_add3_u32 v36, v24, v36, s30
	v_bfe_u32 v37, v25, 16, 1
	v_lshrrev_b32_e32 v36, 16, v36
	v_add3_u32 v37, v25, v37, s30
	v_and_or_b32 v36, v37, s25, v36
	v_bfe_u32 v37, v26, 16, 1
	v_add3_u32 v37, v26, v37, s30
	v_bfe_u32 v40, v27, 16, 1
	v_lshrrev_b32_e32 v37, 16, v37
	v_add3_u32 v40, v27, v40, s30
	v_pk_fma_f32 v[20:21], v[124:125], v[20:21], v[128:129]
	v_and_or_b32 v37, v40, s25, v37
	global_store_dwordx2 v[38:39], v[36:37], off offset:-1024
	v_bfe_u32 v36, v20, 16, 1
	v_add3_u32 v36, v20, v36, s30
	v_bfe_u32 v37, v21, 16, 1
	v_lshrrev_b32_e32 v36, 16, v36
	v_add3_u32 v37, v21, v37, s30
	v_and_or_b32 v36, v37, s25, v36
	v_bfe_u32 v37, v22, 16, 1
	v_add3_u32 v37, v22, v37, s30
	v_bfe_u32 v40, v23, 16, 1
	s_addc_u32 s7, s27, s7
	v_lshrrev_b32_e32 v37, 16, v37
	v_add3_u32 v40, v23, v40, s30
	s_add_u32 s34, s6, 0x2000
	v_and_or_b32 v37, v40, s25, v37
	s_addc_u32 s35, s7, 0
	v_lshlrev_b64 v[104:105], 2, v[54:55]
	global_store_dwordx2 v[38:39], v[36:37], off offset:-512
	v_lshl_add_u64 v[36:37], s[6:7], 0, v[58:59]
	v_lshl_add_u64 v[40:41], s[34:35], 0, v[58:59]
	v_lshl_add_u64 v[68:69], v[56:57], 2, s[6:7]
	v_lshl_add_u64 v[76:77], s[34:35], 0, v[104:105]
	global_load_dwordx4 v[36:39], v[36:37], off
	s_nop 0
	global_load_dwordx4 v[40:43], v[40:41], off
	s_nop 0
	global_load_dwordx4 v[44:47], v[68:69], off offset:1024
	global_load_dwordx4 v[52:55], v[68:69], off offset:2048
	global_load_dwordx4 v[56:59], v[76:77], off offset:1024
	s_nop 0
	global_load_dwordx4 v[68:71], v[68:69], off offset:3072
	s_nop 0
	global_load_dwordx4 v[72:75], v[76:77], off offset:2048
	s_nop 0
	global_load_dwordx4 v[76:79], v[76:77], off offset:3072
	v_lshl_add_u64 v[80:81], v[104:105], 0, s[8:9]
	v_lshl_add_u64 v[88:89], v[104:105], 0, s[10:11]
	v_lshl_add_u64 v[96:97], v[104:105], 0, s[12:13]
	v_lshl_add_u64 v[104:105], v[104:105], 0, s[18:19]
	v_lshl_add_u64 v[82:83], s[6:7], 0, v[80:81]
	v_lshl_add_u64 v[84:85], s[34:35], 0, v[80:81]
	v_lshl_add_u64 v[90:91], s[6:7], 0, v[88:89]
	v_lshl_add_u64 v[92:93], s[34:35], 0, v[88:89]
	v_lshl_add_u64 v[98:99], s[6:7], 0, v[96:97]
	v_lshl_add_u64 v[100:101], s[34:35], 0, v[96:97]
	v_lshl_add_u64 v[106:107], s[6:7], 0, v[104:105]
	v_lshl_add_u64 v[108:109], s[34:35], 0, v[104:105]
	global_load_dwordx4 v[80:83], v[82:83], off
	s_nop 0
	global_load_dwordx4 v[84:87], v[84:85], off
	s_nop 0
	global_load_dwordx4 v[88:91], v[90:91], off
	s_nop 0
	global_load_dwordx4 v[92:95], v[92:93], off
	s_nop 0
	global_load_dwordx4 v[96:99], v[98:99], off
	s_nop 0
	global_load_dwordx4 v[100:103], v[100:101], off
	s_nop 0
	global_load_dwordx4 v[104:107], v[106:107], off
	s_nop 0
	global_load_dwordx4 v[108:111], v[108:109], off
	s_waitcnt vmcnt(14)
	v_pk_add_f32 v[40:41], v[40:41], 1.0 op_sel_hi:[1,0]
	v_pk_add_f32 v[42:43], v[42:43], 1.0 op_sel_hi:[1,0]
	v_pk_fma_f32 v[36:37], v[138:139], v[40:41], v[36:37]
	v_pk_fma_f32 v[38:39], v[136:137], v[42:43], v[38:39]
	v_bfe_u32 v40, v36, 16, 1
	v_add3_u32 v36, v36, v40, s30
	v_bfe_u32 v40, v37, 16, 1
	v_lshrrev_b32_e32 v36, 16, v36
	v_add3_u32 v37, v37, v40, s30
	v_and_or_b32 v36, v37, s25, v36
	v_bfe_u32 v37, v38, 16, 1
	v_add3_u32 v37, v38, v37, s30
	v_bfe_u32 v38, v39, 16, 1
	v_lshrrev_b32_e32 v37, 16, v37
	v_add3_u32 v38, v39, v38, s30
	v_and_or_b32 v37, v38, s25, v37
	s_waitcnt vmcnt(11)
	v_pk_add_f32 v[38:39], v[56:57], 1.0 op_sel_hi:[1,0]
	global_store_dwordx2 v[18:19], v[36:37], off
	v_pk_fma_f32 v[38:39], v[142:143], v[38:39], v[44:45]
	v_pk_add_f32 v[36:37], v[58:59], 1.0 op_sel_hi:[1,0]
	v_bfe_u32 v40, v38, 16, 1
	v_add3_u32 v38, v38, v40, s30
	v_bfe_u32 v40, v39, 16, 1
	v_pk_fma_f32 v[36:37], v[140:141], v[36:37], v[46:47]
	v_lshrrev_b32_e32 v38, 16, v38
	v_add3_u32 v39, v39, v40, s30
	v_and_or_b32 v38, v39, s25, v38
	v_bfe_u32 v39, v36, 16, 1
	v_add3_u32 v36, v36, v39, s30
	v_bfe_u32 v39, v37, 16, 1
	v_lshrrev_b32_e32 v36, 16, v36
	v_add3_u32 v37, v37, v39, s30
	v_and_or_b32 v39, v37, s25, v36
	global_store_dwordx2 v[18:19], v[38:39], off offset:512
	s_waitcnt vmcnt(11)
; __device__ __forceinline__ void st_bf4(bf16* p, f32x4 v) { u32x2 w; w.x = pk2(v.x, v.y); w.y = pk2(v.z, v.w); *(u32x2*)p = w; }
; __device__ __forceinline__ f32x4 xr2f(XRaw w) { return (f32x4){bflo(w.x), bfhi(w.x), bflo(w.y), bfhi(w.y)}; }
; template <int L, bool NEXT_HB> __device__ __forceinline__ void p_ln_ffn(const Args& a, XT* X) {
;     ...
;         if (NEXT_HB) { const float* md = modn + (size_t)(m >> 12) * D6; bf16* hb = (bf16*)(a.ws + WS_HB) + (size_t)m * D; f32x4 shv[8], scv[8];
; #pragma unroll
;             for (int j = 0; j < 8; ++j) { const int k = j * 256 + lane * 4; shv[j] = *(const f32x4*)(md + k); scv[j] = *(const f32x4*)(md + 2048 + k); }
;             __builtin_amdgcn_sched_barrier(0);
; #pragma unroll
;             for (int j = 0; j < 8; ++j) st_bf4(hb + j * 256 + lane * 4, v[j] * (1.f + scv[j]) + shv[j]);
;             __builtin_amdgcn_sched_barrier(0); }
; #pragma unroll
;         for (int j = 0; j < 8; ++j) v[j] = xr2f(vn[j]); }
	v_pk_add_f32 v[38:39], v[72:73], 1.0 op_sel_hi:[1,0]
	v_pk_add_f32 v[36:37], v[74:75], 1.0 op_sel_hi:[1,0]
	v_pk_fma_f32 v[38:39], v[62:63], v[38:39], v[52:53]
	v_pk_fma_f32 v[36:37], v[60:61], v[36:37], v[54:55]
	v_bfe_u32 v40, v38, 16, 1
	v_add3_u32 v38, v38, v40, s30
	v_bfe_u32 v40, v39, 16, 1
	v_lshrrev_b32_e32 v38, 16, v38
	v_add3_u32 v39, v39, v40, s30
	v_and_or_b32 v38, v39, s25, v38
	v_bfe_u32 v39, v36, 16, 1
	v_add3_u32 v36, v36, v39, s30
	v_bfe_u32 v39, v37, 16, 1
	v_lshrrev_b32_e32 v36, 16, v36
	v_add3_u32 v37, v37, v39, s30
	v_and_or_b32 v39, v37, s25, v36
	global_store_dwordx2 v[18:19], v[38:39], off offset:1024
	s_waitcnt vmcnt(11)
	v_pk_add_f32 v[38:39], v[76:77], 1.0 op_sel_hi:[1,0]
	v_pk_add_f32 v[36:37], v[78:79], 1.0 op_sel_hi:[1,0]
	v_pk_fma_f32 v[38:39], v[48:49], v[38:39], v[68:69]
	v_pk_fma_f32 v[36:37], v[50:51], v[36:37], v[70:71]
	v_bfe_u32 v40, v38, 16, 1
	v_add3_u32 v38, v38, v40, s30
	v_bfe_u32 v40, v39, 16, 1
	v_lshrrev_b32_e32 v38, 16, v38
	v_add3_u32 v39, v39, v40, s30
	v_and_or_b32 v38, v39, s25, v38
	v_bfe_u32 v39, v36, 16, 1
	v_add3_u32 v36, v36, v39, s30
	v_bfe_u32 v39, v37, 16, 1
	v_lshrrev_b32_e32 v36, 16, v36
	v_add3_u32 v37, v37, v39, s30
	v_and_or_b32 v39, v37, s25, v36
	global_store_dwordx2 v[18:19], v[38:39], off offset:1536
	s_waitcnt vmcnt(10)
	v_pk_add_f32 v[38:39], v[84:85], 1.0 op_sel_hi:[1,0]
	v_pk_add_f32 v[36:37], v[86:87], 1.0 op_sel_hi:[1,0]
	v_pk_fma_f32 v[32:33], v[32:33], v[38:39], v[80:81]
	v_pk_fma_f32 v[34:35], v[34:35], v[36:37], v[82:83]
	v_bfe_u32 v36, v32, 16, 1
	v_add3_u32 v32, v32, v36, s30
	v_bfe_u32 v36, v33, 16, 1
	v_lshrrev_b32_e32 v32, 16, v32
	v_add3_u32 v33, v33, v36, s30
	v_and_or_b32 v32, v33, s25, v32
	v_bfe_u32 v33, v34, 16, 1
	v_add3_u32 v33, v34, v33, s30
	v_bfe_u32 v34, v35, 16, 1
	v_lshrrev_b32_e32 v33, 16, v33
	v_add3_u32 v34, v35, v34, s30
	v_and_or_b32 v33, v34, s25, v33
	s_waitcnt vmcnt(8)
	v_pk_add_f32 v[34:35], v[92:93], 1.0 op_sel_hi:[1,0]
	global_store_dwordx2 v[18:19], v[32:33], off offset:2048
	v_pk_add_f32 v[32:33], v[94:95], 1.0 op_sel_hi:[1,0]
	v_pk_fma_f32 v[28:29], v[28:29], v[34:35], v[88:89]
	v_pk_fma_f32 v[30:31], v[30:31], v[32:33], v[90:91]
	v_bfe_u32 v32, v28, 16, 1
	v_add3_u32 v28, v28, v32, s30
	v_bfe_u32 v32, v29, 16, 1
	v_lshrrev_b32_e32 v28, 16, v28
	v_add3_u32 v29, v29, v32, s30
	v_and_or_b32 v28, v29, s25, v28
	v_bfe_u32 v29, v30, 16, 1
	v_add3_u32 v29, v30, v29, s30
	v_bfe_u32 v30, v31, 16, 1
	v_lshrrev_b32_e32 v29, 16, v29
	v_add3_u32 v30, v31, v30, s30
	v_and_or_b32 v29, v30, s25, v29
	s_waitcnt vmcnt(7)
	v_pk_add_f32 v[30:31], v[100:101], 1.0 op_sel_hi:[1,0]
	global_store_dwordx2 v[18:19], v[28:29], off offset:2560
	v_pk_add_f32 v[28:29], v[102:103], 1.0 op_sel_hi:[1,0]
	v_pk_fma_f32 v[24:25], v[24:25], v[30:31], v[96:97]
	v_pk_fma_f32 v[26:27], v[26:27], v[28:29], v[98:99]
	v_bfe_u32 v28, v24, 16, 1
	v_add3_u32 v24, v24, v28, s30
	v_bfe_u32 v28, v25, 16, 1
	v_lshrrev_b32_e32 v24, 16, v24
	v_add3_u32 v25, v25, v28, s30
	v_and_or_b32 v24, v25, s25, v24
	v_bfe_u32 v25, v26, 16, 1
	v_add3_u32 v25, v26, v25, s30
	v_bfe_u32 v26, v27, 16, 1
	v_lshrrev_b32_e32 v25, 16, v25
	v_add3_u32 v26, v27, v26, s30
	v_and_or_b32 v25, v26, s25, v25
	s_waitcnt vmcnt(6)
	v_pk_add_f32 v[26:27], v[108:109], 1.0 op_sel_hi:[1,0]
	global_store_dwordx2 v[18:19], v[24:25], off offset:3072
	v_pk_add_f32 v[24:25], v[110:111], 1.0 op_sel_hi:[1,0]
	v_pk_fma_f32 v[20:21], v[20:21], v[26:27], v[104:105]
	v_pk_fma_f32 v[22:23], v[22:23], v[24:25], v[106:107]
	v_bfe_u32 v24, v20, 16, 1
	v_add3_u32 v20, v20, v24, s30
	v_bfe_u32 v24, v21, 16, 1
	v_lshrrev_b32_e32 v20, 16, v20
	v_add3_u32 v21, v21, v24, s30
	v_and_or_b32 v20, v21, s25, v20
	v_bfe_u32 v21, v22, 16, 1
	v_add3_u32 v21, v22, v21, s30
	v_bfe_u32 v22, v23, 16, 1
	v_lshrrev_b32_e32 v21, 16, v21
	v_add3_u32 v22, v23, v22, s30
	v_and_or_b32 v21, v22, s25, v21
	global_store_dwordx2 v[18:19], v[20:21], off offset:3584
	s_add_u32 s14, s14, s16
	v_lshlrev_b32_e32 v49, 16, v2
	v_and_b32_e32 v51, 0xffff0000, v2
	v_lshlrev_b32_e32 v29, 16, v3
	v_and_b32_e32 v33, 0xffff0000, v3
	v_lshlrev_b32_e32 v48, 16, v4
	v_and_b32_e32 v50, 0xffff0000, v4
	v_lshlrev_b32_e32 v28, 16, v5
	v_and_b32_e32 v32, 0xffff0000, v5
	v_lshlrev_b32_e32 v18, 16, v6
	v_and_b32_e32 v60, 0xffff0000, v6
	v_lshlrev_b32_e32 v61, 16, v7
	v_and_b32_e32 v19, 0xffff0000, v7
	v_lshlrev_b32_e32 v20, 16, v8
	v_and_b32_e32 v21, 0xffff0000, v8
	v_lshlrev_b32_e32 v24, 16, v9
	v_and_b32_e32 v25, 0xffff0000, v9
	v_lshlrev_b32_e32 v22, 16, v10
	v_and_b32_e32 v26, 0xffff0000, v10
	v_lshlrev_b32_e32 v34, 16, v11
	v_and_b32_e32 v40, 0xffff0000, v11
	v_lshlrev_b32_e32 v30, 16, v12
	v_and_b32_e32 v58, 0xffff0000, v12
	v_lshlrev_b32_e32 v59, 16, v13
	v_and_b32_e32 v31, 0xffff0000, v13
	v_lshlrev_b32_e32 v36, 16, v14
	v_and_b32_e32 v37, 0xffff0000, v14
	v_lshlrev_b32_e32 v44, 16, v15
	v_and_b32_e32 v45, 0xffff0000, v15
	v_lshlrev_b32_e32 v38, 16, v16
	v_and_b32_e32 v42, 0xffff0000, v16
	v_lshlrev_b32_e32 v46, 16, v17
	v_and_b32_e32 v52, 0xffff0000, v17
	s_addc_u32 s15, s15, s17
	s_andn2_b64 vcc, exec, s[22:23]
	s_mov_b32 s24, s20
	s_cbranch_vccz .LBB0_1294

; __device__ __forceinline__ float wave_sum(float v) {
; #pragma unroll
;     for (int o = 1; o < 64; o <<= 1) v += __shfl_xor(v, o);
;     return v;
; }
; __device__ __forceinline__ void ln_regs(f32x4 (&v)[8], const float* g, const float* bt, int lane) {
;     float s = 0.f;
; #pragma unroll
;     for (int j = 0; j < 8; ++j) s += (v[j].x + v[j].y) + (v[j].z + v[j].w);
;     const float mean = wave_sum(s) * (1.f / D); float s2 = 0.f;
; #pragma unroll
;     for (int j = 0; j < 8; ++j) { v[j] = v[j] - mean; s2 += (v[j].x * v[j].x + v[j].y * v[j].y) + (v[j].z * v[j].z + v[j].w * v[j].w); }
;     const float rstd = 1.f / sqrtf(wave_sum(s2) * (1.f / D) + LN_EPS);
; #pragma unroll
;     for (int j = 0; j < 8; ++j) { const f32x4 gv = *(const f32x4*)(g + j * 256 + lane * 4), bv = *(const f32x4*)(bt + j * 256 + lane * 4); v[j] = v[j] * rstd * gv + bv; }
.LBB0_2022:
	v_pk_add_f32 v[46:47], v[32:33], v[34:35]
	v_pk_add_f32 v[48:49], v[10:11], v[14:15]
	v_add_f32_e32 v19, v8, v9
	v_pk_add_f32 v[46:47], v[46:47], v[48:49]
	v_add_f32_e32 v25, v22, v23
	v_add_f32_e32 v7, 0, v47
	v_add_f32_e32 v21, v46, v7
	v_pk_add_f32 v[46:47], v[44:45], v[2:3]
	v_add_f32_e32 v7, v4, v5
	v_pk_add_f32 v[46:47], v[46:47], v[46:47] op_sel_hi:[0,1]
	v_mov_b32_e32 v13, v47
	v_pk_add_f32 v[48:49], v[6:7], v[18:19]
	v_pk_add_f32 v[46:47], v[12:13], v[20:21]
	v_and_b32_e32 v13, 64, v76
	v_pk_add_f32 v[46:47], v[48:49], v[46:47]
	v_pk_add_f32 v[48:49], v[42:43], v[16:17]
	v_pk_add_f32 v[46:47], v[46:47], v[46:47] op_sel_hi:[0,1]
	v_pk_add_f32 v[48:49], v[48:49], v[48:49] op_sel_hi:[0,1]
	v_add_f32_e32 v31, v28, v29
	v_mov_b32_e32 v27, v49
	v_mov_b32_e32 v37, v47
	v_add_u32_e32 v13, 64, v13
	v_xor_b32_e32 v19, 1, v76
	v_pk_add_f32 v[50:51], v[24:25], v[30:31]
	v_pk_add_f32 v[46:47], v[26:27], v[36:37]
	v_cmp_lt_i32_e32 vcc, v19, v13
	v_pk_add_f32 v[46:47], v[50:51], v[46:47]
	s_nop 0
	v_cndmask_b32_e32 v19, v76, v19, vcc
	v_add_f32_e32 v7, v46, v47
	v_lshlrev_b32_e32 v97, 2, v19
	s_waitcnt lgkmcnt(0)
	s_nop 1
	v_add_f32_dpp v7, v7, v7 quad_perm:[1,0,3,2] row_mask:0xf bank_mask:0xf
	v_xor_b32_e32 v19, 2, v76
	v_cmp_lt_i32_e32 vcc, v19, v13
	s_nop 1
	v_cndmask_b32_e32 v19, v76, v19, vcc
	v_lshlrev_b32_e32 v126, 2, v19
	s_waitcnt lgkmcnt(0)
	s_nop 1
	v_add_f32_dpp v7, v7, v7 quad_perm:[2,3,0,1] row_mask:0xf bank_mask:0xf
	v_xor_b32_e32 v19, 4, v76
	v_cmp_lt_i32_e32 vcc, v19, v13
	s_nop 1
	v_cndmask_b32_e32 v19, v76, v19, vcc
	v_lshlrev_b32_e32 v127, 2, v19
	s_waitcnt lgkmcnt(0)
	s_nop 1
	v_add_f32_dpp v7, v7, v7 row_half_mirror row_mask:0xf bank_mask:0xf
	v_xor_b32_e32 v19, 8, v76
	v_cmp_lt_i32_e32 vcc, v19, v13
	s_nop 1
	v_cndmask_b32_e32 v19, v76, v19, vcc
	v_lshlrev_b32_e32 v128, 2, v19
	s_waitcnt lgkmcnt(0)
	s_nop 1
	v_add_f32_dpp v7, v7, v7 row_mirror row_mask:0xf bank_mask:0xf
	v_xor_b32_e32 v19, 16, v76
	v_cmp_lt_i32_e32 vcc, v19, v13
	s_nop 1
	v_cndmask_b32_e32 v19, v76, v19, vcc
	v_lshlrev_b32_e32 v129, 2, v19
	ds_bpermute_b32 v19, v129, v7
	s_waitcnt lgkmcnt(0)
	v_add_f32_e32 v7, v7, v19
	v_xor_b32_e32 v19, 32, v76
	v_cmp_lt_i32_e32 vcc, v19, v13
	s_nop 1
	v_cndmask_b32_e32 v13, v76, v19, vcc
	v_lshlrev_b32_e32 v130, 2, v13
	ds_bpermute_b32 v13, v130, v7
	s_waitcnt lgkmcnt(0)
	v_add_f32_e32 v7, v7, v13
	v_fmac_f32_e32 v35, 0xba000000, v7
	v_fmac_f32_e32 v34, 0xba000000, v7
	v_fmac_f32_e32 v15, 0xba000000, v7
	v_fmac_f32_e32 v33, 0xba000000, v7
	v_fmac_f32_e32 v14, 0xba000000, v7
	v_fmac_f32_e32 v32, 0xba000000, v7
	v_mov_b32_e32 v48, v35
	v_mov_b32_e32 v49, v34
	v_fmac_f32_e32 v11, 0xba000000, v7
	v_fmac_f32_e32 v10, 0xba000000, v7
	v_mov_b32_e32 v46, v33
	v_mov_b32_e32 v47, v32
	v_pk_mul_f32 v[48:49], v[48:49], v[48:49]
	v_mov_b32_e32 v50, v15
	v_mov_b32_e32 v51, v14
	v_pk_fma_f32 v[46:47], v[46:47], v[46:47], v[48:49]
	v_mov_b32_e32 v48, v11
	v_mov_b32_e32 v49, v10
	v_pk_mul_f32 v[50:51], v[50:51], v[50:51]
	v_fmac_f32_e32 v44, 0xba000000, v7
	v_pk_fma_f32 v[48:49], v[48:49], v[48:49], v[50:51]
	v_fmac_f32_e32 v3, 0xba000000, v7
	v_pk_add_f32 v[46:47], v[46:47], v[48:49]
	v_fmac_f32_e32 v45, 0xba000000, v7
	v_pk_add_f32 v[48:49], v[46:47], v[46:47] op_sel_hi:[0,1]
	v_fmac_f32_e32 v2, 0xba000000, v7
	v_mov_b32_e32 v46, v45
	v_mov_b32_e32 v47, v3
	v_mov_b32_e32 v3, v44
	v_pk_mul_f32 v[50:51], v[46:47], v[46:47]
	v_pk_mul_f32 v[44:45], v[2:3], v[2:3]
	v_fmac_f32_e32 v4, 0xba000000, v7
	v_pk_mov_b32 v[52:53], v[44:45], v[50:51] op_sel:[1,0]
	v_mov_b32_e32 v45, v51
	v_pk_add_f32 v[44:45], v[52:53], v[44:45]
	v_fmac_f32_e32 v5, 0xba000000, v7
	v_pk_add_f32 v[44:45], v[44:45], v[44:45] op_sel_hi:[0,1]
	v_fmac_f32_e32 v8, 0xba000000, v7
	v_mul_f32_e32 v44, v4, v4
	v_fmac_f32_e32 v9, 0xba000000, v7
	v_pk_fma_f32 v[50:51], v[4:5], v[4:5], v[44:45] op_sel_hi:[1,1,0]
	v_mul_f32_e32 v44, v8, v8
	v_pk_fma_f32 v[52:53], v[8:9], v[8:9], v[44:45] op_sel_hi:[1,1,0]
	v_fmac_f32_e32 v20, 0xba000000, v7
	v_fmac_f32_e32 v12, 0xba000000, v7
	v_fmac_f32_e32 v18, 0xba000000, v7
	v_fmac_f32_e32 v6, 0xba000000, v7
	v_fmac_f32_e32 v42, 0xba000000, v7
	v_fmac_f32_e32 v17, 0xba000000, v7
	v_fmac_f32_e32 v43, 0xba000000, v7
	v_mul_f32_e32 v50, v6, v6
	v_mul_f32_e32 v52, v18, v18
	v_mul_f32_e32 v44, v12, v12
	v_mul_f32_e32 v48, v20, v20
	v_fmac_f32_e32 v16, 0xba000000, v7
	v_mov_b32_e32 v66, v43
	v_mov_b32_e32 v67, v17
	v_mov_b32_e32 v17, v42
	v_pk_add_f32 v[50:51], v[50:51], v[52:53]
	v_pk_add_f32 v[44:45], v[44:45], v[48:49]
	v_pk_mul_f32 v[48:49], v[66:67], v[66:67]
	v_pk_mul_f32 v[42:43], v[16:17], v[16:17]
	v_pk_add_f32 v[44:45], v[50:51], v[44:45]
	v_pk_mov_b32 v[50:51], v[42:43], v[48:49] op_sel:[1,0]
	v_mov_b32_e32 v43, v49
	v_pk_add_f32 v[42:43], v[50:51], v[42:43]
	v_fmac_f32_e32 v22, 0xba000000, v7
	v_pk_add_f32 v[42:43], v[42:43], v[42:43] op_sel_hi:[0,1]
	v_fmac_f32_e32 v23, 0xba000000, v7
	v_fmac_f32_e32 v28, 0xba000000, v7
	v_mul_f32_e32 v42, v22, v22
	v_fmac_f32_e32 v29, 0xba000000, v7
	v_pk_fma_f32 v[48:49], v[22:23], v[22:23], v[42:43] op_sel_hi:[1,1,0]
	v_mul_f32_e32 v42, v28, v28
	v_pk_add_f32 v[44:45], v[44:45], v[44:45] op_sel_hi:[0,1]
	v_pk_fma_f32 v[50:51], v[28:29], v[28:29], v[42:43] op_sel_hi:[1,1,0]
	v_fmac_f32_e32 v36, 0xba000000, v7
	v_fmac_f32_e32 v26, 0xba000000, v7
	v_fmac_f32_e32 v30, 0xba000000, v7
	v_fmac_f32_e32 v24, 0xba000000, v7
	v_mul_f32_e32 v48, v24, v24
	v_mul_f32_e32 v50, v30, v30
	v_mul_f32_e32 v42, v26, v26
	v_mul_f32_e32 v44, v36, v36
	v_pk_add_f32 v[48:49], v[48:49], v[50:51]
	v_pk_add_f32 v[42:43], v[42:43], v[44:45]
	v_mov_b32_e32 v68, v10
	v_pk_add_f32 v[42:43], v[48:49], v[42:43]
	v_mov_b32_e32 v69, v14
	v_add_f32_e32 v7, v42, v43
	v_lshlrev_b64 v[42:43], 2, v[38:39]
	v_lshl_add_u64 v[44:45], s[2:3], 0, v[42:43]
	v_lshl_add_u64 v[48:49], s[4:5], 0, v[42:43]
	global_load_dwordx4 v[50:53], v[44:45], off
	global_load_dwordx4 v[54:57], v[48:49], off
	global_load_dwordx4 v[58:61], v[44:45], off offset:1024
	global_load_dwordx4 v[62:65], v[48:49], off offset:1024
	global_load_dwordx4 v[98:101], v[44:45], off offset:2048
	global_load_dwordx4 v[102:105], v[44:45], off offset:3072
	global_load_dwordx4 v[106:109], v[48:49], off offset:2048
	global_load_dwordx4 v[110:113], v[48:49], off offset:3072
	v_add_co_u32_e32 v44, vcc, s46, v44
	s_nop 0
	v_addc_co_u32_e32 v45, vcc, 0, v45, vcc
	v_add_co_u32_e32 v48, vcc, s46, v48
	global_load_dwordx4 v[132:135], v[44:45], off
	s_nop 0
	v_addc_co_u32_e32 v49, vcc, 0, v49, vcc
	global_load_dwordx4 v[136:139], v[48:49], off
	global_load_dwordx4 v[140:143], v[44:45], off offset:1024
	global_load_dwordx4 v[144:147], v[48:49], off offset:1024
	global_load_dwordx4 v[148:151], v[44:45], off offset:2048
	global_load_dwordx4 v[152:155], v[48:49], off offset:2048
	global_load_dwordx4 v[156:159], v[44:45], off offset:3072
	global_load_dwordx4 v[160:163], v[48:49], off offset:3072
	s_waitcnt lgkmcnt(0)
; __device__ __forceinline__ void stx4(XT* p, f32x4 v) { st_bf4(p, v); }
; __device__ __forceinline__ void ln_regs(f32x4 (&v)[8], const float* g, const float* bt, int lane) {
;     ...
;     const float mean = wave_sum(s) * (1.f / D); float s2 = 0.f;
; #pragma unroll
;     for (int j = 0; j < 8; ++j) { v[j] = v[j] - mean; s2 += (v[j].x * v[j].x + v[j].y * v[j].y) + (v[j].z * v[j].z + v[j].w * v[j].w); }
;     const float rstd = 1.f / sqrtf(wave_sum(s2) * (1.f / D) + LN_EPS);
; #pragma unroll
;     for (int j = 0; j < 8; ++j) { const f32x4 gv = *(const f32x4*)(g + j * 256 + lane * 4), bv = *(const f32x4*)(bt + j * 256 + lane * 4); v[j] = v[j] * rstd * gv + bv; }
; template <int L, bool ROUTER, bool WRITE_HB> __device__ __forceinline__ void p_ln_mix(const Args& a, LAS unsigned char* lds, XT* X) {
;     ...
; #pragma unroll
;             for (int j = 0; j < 8; ++j) stx4(xr + j * 256 + lane * 4, v[j]);
	s_nop 1
	v_add_f32_dpp v7, v7, v7 quad_perm:[1,0,3,2] row_mask:0xf bank_mask:0xf
	v_mov_b32_e32 v14, v11
	v_mov_b32_e32 v45, v34
	v_mov_b32_e32 v34, v33
	v_mov_b32_e32 v44, v32
	s_waitcnt lgkmcnt(0)
	s_nop 1
	v_add_f32_dpp v7, v7, v7 quad_perm:[2,3,0,1] row_mask:0xf bank_mask:0xf
	v_mov_b32_e32 v27, v36
	v_mov_b32_e32 v25, v30
	s_waitcnt lgkmcnt(0)
	s_nop 1
	v_add_f32_dpp v7, v7, v7 row_half_mirror row_mask:0xf bank_mask:0xf
	s_waitcnt lgkmcnt(0)
	s_nop 1
	v_add_f32_dpp v7, v7, v7 row_mirror row_mask:0xf bank_mask:0xf
	ds_bpermute_b32 v13, v129, v7
	s_waitcnt lgkmcnt(0)
	v_add_f32_e32 v7, v7, v13
	ds_bpermute_b32 v13, v130, v7
	s_waitcnt lgkmcnt(0)
	v_add_f32_e32 v7, v7, v13
	v_fmamk_f32 v7, v7, 0x3a000000, v120
	v_mul_f32_e32 v13, 0x4f800000, v7
	v_cmp_gt_f32_e32 vcc, s45, v7
	s_nop 1
	v_cndmask_b32_e32 v7, v7, v13, vcc
	v_sqrt_f32_e32 v13, v7
	s_nop 0
	v_add_u32_e32 v10, -1, v13
	v_fma_f32 v19, -v10, v13, v7
	v_cmp_ge_f32_e64 s[8:9], 0, v19
	v_add_u32_e32 v19, 1, v13
	s_nop 0
	v_cndmask_b32_e64 v10, v13, v10, s[8:9]
	v_fma_f32 v13, -v19, v13, v7
	v_cmp_lt_f32_e64 s[8:9], 0, v13
	s_nop 1
	v_cndmask_b32_e64 v10, v10, v19, s[8:9]
	v_mul_f32_e32 v13, 0x37800000, v10
	v_cndmask_b32_e32 v10, v10, v13, vcc
	v_cmp_class_f32_e32 vcc, v7, v121
	s_nop 1
	v_cndmask_b32_e32 v7, v10, v7, vcc
	v_div_scale_f32 v10, s[8:9], v7, v7, 1.0
	v_rcp_f32_e32 v13, v10
	s_nop 0
	v_fma_f32 v11, -v10, v13, 1.0
	v_fmac_f32_e32 v13, v11, v13
	v_div_scale_f32 v11, vcc, 1.0, v7, 1.0
	v_mul_f32_e32 v19, v11, v13
	v_fma_f32 v21, -v10, v19, v11
	v_fmac_f32_e32 v19, v21, v13
	v_fma_f32 v10, -v10, v19, v11
	v_div_fmas_f32 v10, v10, v13, v19
	v_div_fixup_f32 v70, v10, v7, 1.0
	v_pk_mul_f32 v[10:11], v[34:35], v[70:71] op_sel_hi:[1,0]
	v_pk_mul_f32 v[14:15], v[14:15], v[70:71] op_sel_hi:[1,0]
	s_waitcnt vmcnt(14)
	v_pk_fma_f32 v[32:33], v[50:51], v[10:11], v[54:55]
	v_pk_mul_f32 v[10:11], v[44:45], v[70:71] op_sel_hi:[1,0]
	v_pk_fma_f32 v[48:49], v[52:53], v[14:15], v[56:57]
	v_pk_mul_f32 v[14:15], v[68:69], v[70:71] op_sel_hi:[1,0]
	s_waitcnt vmcnt(12)
	v_pk_fma_f32 v[68:69], v[58:59], v[10:11], v[62:63]
	v_pk_mul_f32 v[2:3], v[2:3], v[70:71] op_sel_hi:[1,0]
	v_pk_mul_f32 v[10:11], v[46:47], v[70:71] op_sel_hi:[1,0]
	v_mov_b32_e32 v13, v20
	s_waitcnt vmcnt(9)
	v_pk_fma_f32 v[118:119], v[100:101], v[10:11], v[108:109]
	v_pk_fma_f32 v[10:11], v[98:99], v[2:3], v[106:107]
	v_pk_mul_f32 v[2:3], v[4:5], v[70:71] op_sel_hi:[1,0]
	v_pk_mul_f32 v[4:5], v[8:9], v[70:71] op_sel_hi:[1,0]
	s_waitcnt vmcnt(8)
	v_pk_fma_f32 v[116:117], v[102:103], v[2:3], v[110:111]
	v_pk_fma_f32 v[114:115], v[104:105], v[4:5], v[112:113]
	v_pk_mul_f32 v[4:5], v[12:13], v[70:71] op_sel_hi:[1,0]
	v_mov_b32_e32 v7, v18
	s_waitcnt vmcnt(6)
	v_pk_fma_f32 v[110:111], v[134:135], v[4:5], v[138:139]
	v_pk_mul_f32 v[4:5], v[66:67], v[70:71] op_sel_hi:[1,0]
	v_pk_mul_f32 v[2:3], v[6:7], v[70:71] op_sel_hi:[1,0]
	s_waitcnt vmcnt(4)
	v_pk_fma_f32 v[106:107], v[142:143], v[4:5], v[146:147]
	v_pk_mul_f32 v[4:5], v[28:29], v[70:71] op_sel_hi:[1,0]
	v_pk_fma_f32 v[112:113], v[132:133], v[2:3], v[136:137]
	s_waitcnt vmcnt(2)
	v_pk_fma_f32 v[102:103], v[150:151], v[4:5], v[154:155]
	v_pk_mul_f32 v[4:5], v[26:27], v[70:71] op_sel_hi:[1,0]
	v_pk_mul_f32 v[2:3], v[16:17], v[70:71] op_sel_hi:[1,0]
	s_waitcnt vmcnt(0)
	v_pk_fma_f32 v[98:99], v[158:159], v[4:5], v[162:163]
	v_bfe_u32 v4, v32, 16, 1
	v_add3_u32 v4, v32, v4, s47
	v_bfe_u32 v5, v33, 16, 1
	v_pk_fma_f32 v[108:109], v[140:141], v[2:3], v[144:145]
	v_pk_mul_f32 v[2:3], v[22:23], v[70:71] op_sel_hi:[1,0]
	v_lshrrev_b32_e32 v4, 16, v4
	v_add3_u32 v5, v33, v5, s47
	v_pk_fma_f32 v[104:105], v[148:149], v[2:3], v[152:153]
	v_pk_mul_f32 v[2:3], v[24:25], v[70:71] op_sel_hi:[1,0]
	v_and_or_b32 v4, v5, s44, v4
	v_bfe_u32 v5, v48, 16, 1
	v_pk_fma_f32 v[100:101], v[156:157], v[2:3], v[160:161]
	v_lshl_add_u64 v[2:3], s[66:67], 0, v[40:41]
	v_add3_u32 v5, v48, v5, s47
	v_bfe_u32 v6, v49, 16, 1
	v_lshrrev_b32_e32 v5, 16, v5
	v_add3_u32 v6, v49, v6, s47
	v_add_co_u32_e32 v2, vcc, s48, v2
	v_and_or_b32 v5, v6, s44, v5
	s_nop 0
	v_addc_co_u32_e32 v3, vcc, 0, v3, vcc
	global_store_dwordx2 v[2:3], v[4:5], off
	v_bfe_u32 v4, v68, 16, 1
	v_add3_u32 v4, v68, v4, s47
	v_bfe_u32 v5, v69, 16, 1
	v_pk_fma_f32 v[72:73], v[60:61], v[14:15], v[64:65]
	v_lshrrev_b32_e32 v4, 16, v4
	v_add3_u32 v5, v69, v5, s47
	v_and_or_b32 v4, v5, s44, v4
	v_bfe_u32 v5, v72, 16, 1
	v_add3_u32 v5, v72, v5, s47
	v_bfe_u32 v6, v73, 16, 1
	v_lshrrev_b32_e32 v5, 16, v5
	v_add3_u32 v6, v73, v6, s47
	v_and_or_b32 v5, v6, s44, v5
	global_store_dwordx2 v[2:3], v[4:5], off offset:512
	v_bfe_u32 v4, v10, 16, 1
	v_add3_u32 v4, v10, v4, s47
	v_bfe_u32 v5, v11, 16, 1
	v_lshrrev_b32_e32 v4, 16, v4
	v_add3_u32 v5, v11, v5, s47
	v_and_or_b32 v4, v5, s44, v4
	v_bfe_u32 v5, v118, 16, 1
	v_add3_u32 v5, v118, v5, s47
	v_bfe_u32 v6, v119, 16, 1
	v_lshrrev_b32_e32 v5, 16, v5
	v_add3_u32 v6, v119, v6, s47
	v_and_or_b32 v5, v6, s44, v5
	global_store_dwordx2 v[2:3], v[4:5], off offset:1024
	v_bfe_u32 v4, v116, 16, 1
	v_add3_u32 v4, v116, v4, s47
	v_bfe_u32 v5, v117, 16, 1
	v_lshrrev_b32_e32 v4, 16, v4
	v_add3_u32 v5, v117, v5, s47
	v_and_or_b32 v4, v5, s44, v4
	v_bfe_u32 v5, v114, 16, 1
	v_add3_u32 v5, v114, v5, s47
	v_bfe_u32 v6, v115, 16, 1
	v_lshrrev_b32_e32 v5, 16, v5
	v_add3_u32 v6, v115, v6, s47
	v_and_or_b32 v5, v6, s44, v5
	global_store_dwordx2 v[2:3], v[4:5], off offset:1536
	v_bfe_u32 v4, v112, 16, 1
	v_add3_u32 v4, v112, v4, s47
	v_bfe_u32 v5, v113, 16, 1
	v_lshrrev_b32_e32 v4, 16, v4
	v_add3_u32 v5, v113, v5, s47
	v_and_or_b32 v4, v5, s44, v4
	v_bfe_u32 v5, v110, 16, 1
	v_add3_u32 v5, v110, v5, s47
	v_bfe_u32 v6, v111, 16, 1
; __device__ __forceinline__ void stx4(XT* p, f32x4 v) { st_bf4(p, v); }
; template <int L, bool ROUTER, bool WRITE_HB> __device__ __forceinline__ void p_ln_mix(const Args& a, LAS unsigned char* lds, XT* X) {
;     ...
; #pragma unroll
;             for (int j = 0; j < 8; ++j) stx4(xr + j * 256 + lane * 4, v[j]);
;     ...
;             if (ROUTER) {
;                 const float* md = mod + (size_t)(m >> 12) * D6;
;                 float lg[8] = {0.f, 0.f, 0.f, 0.f, 0.f, 0.f, 0.f, 0.f};
; #pragma unroll
;                 for (int j = 0; j < 8; ++j) { const int k = j * 256 + lane * 4; const f32x4 sh = *(const f32x4*)(md + 6144 + k), scf = *(const f32x4*)(md + 8192 + k); const f32x4 hv = v[j] * (1.f + scf) + sh;
; #pragma unroll
;                     for (int i = 0; i < 4; ++i) { const f32x4 w0 = *(const f32x4*)(wr + (size_t)(k + i) * 8), w1 = *(const f32x4*)(wr + (size_t)(k + i) * 8 + 4); const float hx = hv[i];
;                         lg[0] += hx * w0.x; lg[1] += hx * w0.y; lg[2] += hx * w0.z; lg[3] += hx * w0.w; lg[4] += hx * w1.x; lg[5] += hx * w1.y; lg[6] += hx * w1.z; lg[7] += hx * w1.w; } }
	v_lshrrev_b32_e32 v5, 16, v5
	v_add3_u32 v6, v111, v6, s47
	v_and_or_b32 v5, v6, s44, v5
	global_store_dwordx2 v[2:3], v[4:5], off offset:2048
	v_bfe_u32 v4, v108, 16, 1
	v_add3_u32 v4, v108, v4, s47
	v_bfe_u32 v5, v109, 16, 1
	v_lshrrev_b32_e32 v4, 16, v4
	v_add3_u32 v5, v109, v5, s47
	v_and_or_b32 v4, v5, s44, v4
	v_bfe_u32 v5, v106, 16, 1
	v_add3_u32 v5, v106, v5, s47
	v_bfe_u32 v6, v107, 16, 1
	v_lshrrev_b32_e32 v5, 16, v5
	v_add3_u32 v6, v107, v6, s47
	v_and_or_b32 v5, v6, s44, v5
	global_store_dwordx2 v[2:3], v[4:5], off offset:2560
	v_bfe_u32 v4, v104, 16, 1
	v_add3_u32 v4, v104, v4, s47
	v_bfe_u32 v5, v105, 16, 1
	v_lshrrev_b32_e32 v4, 16, v4
	v_add3_u32 v5, v105, v5, s47
	v_and_or_b32 v4, v5, s44, v4
	v_bfe_u32 v5, v102, 16, 1
	v_add3_u32 v5, v102, v5, s47
	v_bfe_u32 v6, v103, 16, 1
	v_lshrrev_b32_e32 v5, 16, v5
	v_add3_u32 v6, v103, v6, s47
	v_and_or_b32 v5, v6, s44, v5
	global_store_dwordx2 v[2:3], v[4:5], off offset:3072
	v_bfe_u32 v4, v100, 16, 1
	v_add3_u32 v4, v100, v4, s47
	v_bfe_u32 v5, v101, 16, 1
	v_lshrrev_b32_e32 v4, 16, v4
	v_add3_u32 v5, v101, v5, s47
	v_and_or_b32 v4, v5, s44, v4
	v_bfe_u32 v5, v98, 16, 1
	v_add3_u32 v5, v98, v5, s47
	v_bfe_u32 v6, v99, 16, 1
	v_lshrrev_b32_e32 v5, 16, v5
	v_add3_u32 v6, v99, v6, s47
	v_and_or_b32 v5, v6, s44, v5
	global_store_dwordx2 v[2:3], v[4:5], off offset:3584
	v_lshl_add_u64 v[2:3], s[30:31], 0, v[42:43]
	v_lshl_add_u64 v[6:7], s[34:35], 0, v[42:43]
	global_load_dwordx4 v[2:5], v[2:3], off
	s_nop 0
	global_load_dwordx4 v[6:9], v[6:7], off
	v_lshlrev_b64 v[12:13], 5, v[38:39]
	v_lshl_add_u64 v[12:13], s[92:93], 0, v[12:13]
	global_load_dwordx4 v[50:53], v[12:13], off
	global_load_dwordx4 v[16:19], v[12:13], off offset:16
	v_or_b32_e32 v12, 1, v96
	v_ashrrev_i32_e32 v13, 31, v12
	v_lshlrev_b64 v[12:13], 5, v[12:13]
	v_lshl_add_u64 v[12:13], s[92:93], 0, v[12:13]
	global_load_dwordx4 v[54:57], v[12:13], off
	global_load_dwordx4 v[42:45], v[12:13], off offset:16
	global_load_dwordx4 v[58:61], v[12:13], off offset:32
	global_load_dwordx4 v[62:65], v[12:13], off offset:48
	v_or_b32_e32 v12, 3, v96
	v_ashrrev_i32_e32 v13, 31, v12
	v_lshlrev_b64 v[12:13], 5, v[12:13]
	v_add_u32_e32 v20, 0x100, v96
	v_lshl_add_u64 v[12:13], s[92:93], 0, v[12:13]
	v_ashrrev_i32_e32 v21, 31, v20
	global_load_dwordx4 v[138:141], v[12:13], off offset:16
	global_load_dwordx4 v[142:145], v[12:13], off
	v_lshlrev_b64 v[12:13], 2, v[20:21]
	v_lshl_add_u64 v[14:15], s[30:31], 0, v[12:13]
	v_lshl_add_u64 v[22:23], s[34:35], 0, v[12:13]
	global_load_dwordx4 v[12:15], v[14:15], off
	s_nop 0
	global_load_dwordx4 v[146:149], v[22:23], off
	v_lshlrev_b64 v[20:21], 5, v[20:21]
	v_add_u32_e32 v40, 0x200, v96
	v_lshl_add_u64 v[20:21], s[92:93], 0, v[20:21]
	v_ashrrev_i32_e32 v41, 31, v40
	global_load_dwordx4 v[28:31], v[20:21], off
	global_load_dwordx4 v[150:153], v[20:21], off offset:16
	global_load_dwordx4 v[154:157], v[20:21], off offset:48
	global_load_dwordx4 v[24:27], v[20:21], off offset:32
	v_cmp_eq_u32_e32 vcc, 0, v125
	s_waitcnt vmcnt(14)
	v_add_f32_e32 v6, 1.0, v6
	v_fma_f32 v2, v32, v6, v2
	v_add_f32_e32 v6, 1.0, v7
	s_waitcnt vmcnt(12)
	v_fma_f32 v134, v16, v2, 0
	v_add_u32_e32 v16, 0x102, v96
	v_fma_f32 v133, v17, v2, 0
	v_ashrrev_i32_e32 v17, 31, v16
	v_lshlrev_b64 v[16:17], 5, v[16:17]
	v_lshl_add_u64 v[16:17], s[92:93], 0, v[16:17]
	global_load_dwordx4 v[158:161], v[16:17], off offset:16
	global_load_dwordx4 v[36:39], v[16:17], off
	global_load_dwordx4 v[162:165], v[16:17], off offset:48
	global_load_dwordx4 v[20:23], v[16:17], off offset:32
	v_lshlrev_b64 v[16:17], 2, v[40:41]
	v_fma_f32 v132, v18, v2, 0
	v_fma_f32 v131, v19, v2, 0
	v_lshl_add_u64 v[18:19], s[30:31], 0, v[16:17]
	v_lshl_add_u64 v[16:17], s[34:35], 0, v[16:17]
	v_fma_f32 v6, v33, v6, v3
	global_load_dwordx4 v[32:35], v[18:19], off
	s_nop 0
	global_load_dwordx4 v[16:19], v[16:17], off
	v_lshlrev_b64 v[40:41], 5, v[40:41]
	v_lshl_add_u64 v[46:47], s[92:93], 0, v[40:41]
	s_waitcnt vmcnt(16)
	v_fmac_f32_e32 v134, v6, v42
	v_fmac_f32_e32 v133, v6, v43
	global_load_dwordx4 v[166:169], v[46:47], off offset:16
	global_load_dwordx4 v[40:43], v[46:47], off
	v_add_f32_e32 v3, 1.0, v8
	v_fma_f32 v4, v48, v3, v4
	v_add_f32_e32 v3, 1.0, v9
	v_fma_f32 v136, v52, v2, 0
	v_fma_f32 v135, v53, v2, 0
	v_fmac_f32_e32 v5, v49, v3
	v_pk_fma_f32 v[2:3], v[50:51], v[2:3], 0 op_sel_hi:[1,0,0]
	v_fmac_f32_e32 v136, v6, v56
	v_fmac_f32_e32 v135, v6, v57
	v_fmac_f32_e32 v132, v6, v44
	v_fmac_f32_e32 v131, v6, v45
	v_pk_fma_f32 v[2:3], v[6:7], v[54:55], v[2:3] op_sel_hi:[0,1,1]
	s_waitcnt vmcnt(17)
	v_fmac_f32_e32 v136, v4, v60
	v_fmac_f32_e32 v135, v4, v61
	s_waitcnt vmcnt(16)
	v_fmac_f32_e32 v134, v4, v62
	v_fmac_f32_e32 v133, v4, v63
	v_fmac_f32_e32 v132, v4, v64
	v_fmac_f32_e32 v131, v4, v65
	v_pk_fma_f32 v[2:3], v[4:5], v[58:59], v[2:3] op_sel_hi:[0,1,1]
	v_mov_b32_e32 v4, v5
	v_add_u32_e32 v6, 0x202, v96
	s_waitcnt vmcnt(14)
	v_pk_fma_f32 v[178:179], v[4:5], v[142:143], v[2:3] op_sel_hi:[0,1,1]
	s_waitcnt vmcnt(12)
	v_add_f32_e32 v2, 1.0, v146
	v_ashrrev_i32_e32 v7, 31, v6
	v_fma_f32 v180, v68, v2, v12
	v_add_u32_e32 v2, 0x300, v96
	v_lshlrev_b64 v[6:7], 5, v[6:7]
	v_ashrrev_i32_e32 v3, 31, v2
	v_lshl_add_u64 v[6:7], s[92:93], 0, v[6:7]
	v_fmac_f32_e32 v136, v5, v144
	v_fmac_f32_e32 v135, v5, v145
	v_fmac_f32_e32 v134, v5, v138
	v_fmac_f32_e32 v133, v5, v139
	v_fmac_f32_e32 v132, v5, v140
	v_fmac_f32_e32 v131, v5, v141
	v_lshlrev_b64 v[4:5], 2, v[2:3]
	global_load_dwordx4 v[170:173], v[46:47], off offset:48
	s_nop 0
	global_load_dwordx4 v[44:47], v[46:47], off offset:32
	s_nop 0
	global_load_dwordx4 v[174:177], v[6:7], off offset:16
	global_load_dwordx4 v[48:51], v[6:7], off
	global_load_dwordx4 v[138:141], v[6:7], off offset:48
	global_load_dwordx4 v[52:55], v[6:7], off offset:32
	v_lshl_add_u64 v[6:7], s[30:31], 0, v[4:5]
	v_lshl_add_u64 v[4:5], s[34:35], 0, v[4:5]
	global_load_dwordx4 v[56:59], v[6:7], off
	global_load_dwordx4 v[60:63], v[4:5], off
	v_lshlrev_b64 v[2:3], 5, v[2:3]
	v_lshl_add_u64 v[2:3], s[92:93], 0, v[2:3]
	v_add_f32_e32 v4, 1.0, v147
	s_waitcnt vmcnt(19)
; template <int L, bool ROUTER, bool WRITE_HB> __device__ __forceinline__ void p_ln_mix(const Args& a, LAS unsigned char* lds, XT* X) {
;     ...
;                 const float* md = mod + (size_t)(m >> 12) * D6;
;                 float lg[8] = {0.f, 0.f, 0.f, 0.f, 0.f, 0.f, 0.f, 0.f};
; #pragma unroll
;                 for (int j = 0; j < 8; ++j) { const int k = j * 256 + lane * 4; const f32x4 sh = *(const f32x4*)(md + 6144 + k), scf = *(const f32x4*)(md + 8192 + k); const f32x4 hv = v[j] * (1.f + scf) + sh;
; #pragma unroll
;                     for (int i = 0; i < 4; ++i) { const f32x4 w0 = *(const f32x4*)(wr + (size_t)(k + i) * 8), w1 = *(const f32x4*)(wr + (size_t)(k + i) * 8 + 4); const float hx = hv[i];
;                         lg[0] += hx * w0.x; lg[1] += hx * w0.y; lg[2] += hx * w0.z; lg[3] += hx * w0.w; lg[4] += hx * w1.x; lg[5] += hx * w1.y; lg[6] += hx * w1.z; lg[7] += hx * w1.w; } }
	v_fmac_f32_e32 v136, v30, v180
	s_waitcnt vmcnt(18)
	v_fmac_f32_e32 v134, v150, v180
	v_fmac_f32_e32 v133, v151, v180
	v_fmac_f32_e32 v132, v152, v180
	v_fmac_f32_e32 v131, v153, v180
	global_load_dwordx4 v[142:145], v[2:3], off offset:16
	global_load_dwordx4 v[64:67], v[2:3], off
	v_fma_f32 v30, v69, v4, v13
	global_load_dwordx4 v[150:153], v[2:3], off offset:48
	global_load_dwordx4 v[68:71], v[2:3], off offset:32
	v_add_f32_e32 v2, 1.0, v148
	s_waitcnt vmcnt(20)
	v_fmac_f32_e32 v136, v30, v26
	v_fma_f32 v14, v72, v2, v14
	v_add_f32_e32 v2, 1.0, v149
	v_fmac_f32_e32 v15, v73, v2
	v_fmac_f32_e32 v134, v30, v154
	v_fmac_f32_e32 v133, v30, v155
	v_fmac_f32_e32 v132, v30, v156
	v_fmac_f32_e32 v131, v30, v157
	v_fmac_f32_e32 v135, v31, v180
	v_fmac_f32_e32 v135, v30, v27
	v_add_u32_e32 v26, 0x402, v96
	s_waitcnt vmcnt(19)
	v_fmac_f32_e32 v134, v14, v158
	s_waitcnt vmcnt(18)
	v_fmac_f32_e32 v136, v14, v38
	s_waitcnt vmcnt(16)
	v_fmac_f32_e32 v136, v15, v22
	v_fmac_f32_e32 v133, v14, v159
	v_fmac_f32_e32 v132, v14, v160
	v_fmac_f32_e32 v131, v14, v161
	v_fmac_f32_e32 v134, v15, v162
	v_fmac_f32_e32 v133, v15, v163
	v_fmac_f32_e32 v132, v15, v164
	s_waitcnt vmcnt(14)
	v_add_f32_e32 v2, 1.0, v16
	v_fma_f32 v182, v10, v2, v32
	v_add_f32_e32 v2, 1.0, v17
	v_add_u32_e32 v10, 0x400, v96
	v_add_f32_e32 v4, 1.0, v18
	s_waitcnt vmcnt(12)
	v_fmac_f32_e32 v136, v42, v182
	v_fma_f32 v42, v11, v2, v33
	v_add_u32_e32 v2, 0x302, v96
	v_ashrrev_i32_e32 v3, 31, v2
	v_lshlrev_b64 v[2:3], 5, v[2:3]
	v_lshl_add_u64 v[2:3], s[92:93], 0, v[2:3]
	v_ashrrev_i32_e32 v11, 31, v10
	global_load_dwordx4 v[146:149], v[2:3], off offset:16
	global_load_dwordx4 v[154:157], v[2:3], off
	v_lshlrev_b64 v[6:7], 2, v[10:11]
	v_lshl_add_u64 v[8:9], s[30:31], 0, v[6:7]
	v_fma_f32 v34, v118, v4, v34
	global_load_dwordx4 v[158:161], v[2:3], off offset:48
	s_nop 0
	global_load_dwordx4 v[2:5], v[2:3], off offset:32
	v_lshl_add_u64 v[12:13], s[34:35], 0, v[6:7]
	global_load_dwordx4 v[6:9], v[8:9], off
	s_nop 0
	global_load_dwordx4 v[72:75], v[12:13], off
	v_lshlrev_b64 v[10:11], 5, v[10:11]
	v_lshl_add_u64 v[16:17], s[92:93], 0, v[10:11]
	v_fmac_f32_e32 v131, v15, v165
	global_load_dwordx4 v[162:165], v[16:17], off offset:16
	global_load_dwordx4 v[10:13], v[16:17], off
	v_fmac_f32_e32 v135, v14, v39
	v_fmac_f32_e32 v135, v15, v23
	v_fmac_f32_e32 v134, v166, v182
	v_fmac_f32_e32 v133, v167, v182
	v_fmac_f32_e32 v132, v168, v182
	v_fmac_f32_e32 v131, v169, v182
	v_add_f32_e32 v18, 1.0, v19
	v_ashrrev_i32_e32 v27, 31, v26
	v_fmac_f32_e32 v35, v119, v18
	v_lshlrev_b64 v[26:27], 5, v[26:27]
	v_fmac_f32_e32 v135, v43, v182
	v_lshl_add_u64 v[32:33], s[92:93], 0, v[26:27]
	s_waitcnt vmcnt(19)
	v_fmac_f32_e32 v134, v42, v170
	s_waitcnt vmcnt(18)
	v_fmac_f32_e32 v136, v42, v46
	s_waitcnt vmcnt(16)
	v_fmac_f32_e32 v136, v34, v50
	v_fmac_f32_e32 v133, v42, v171
	v_fmac_f32_e32 v132, v42, v172
	v_fmac_f32_e32 v131, v42, v173
	s_waitcnt vmcnt(12)
	v_add_f32_e32 v22, 1.0, v61
	v_fma_f32 v50, v117, v22, v57
	v_add_f32_e32 v22, 1.0, v62
	v_fma_f32 v58, v114, v22, v58
	v_pk_fma_f32 v[22:23], v[28:29], v[180:181], v[178:179] op_sel_hi:[1,0,1]
	v_fmac_f32_e32 v134, v34, v174
	v_pk_fma_f32 v[22:23], v[30:31], v[24:25], v[22:23] op_sel_hi:[0,1,1]
	v_fmac_f32_e32 v133, v34, v175
	v_fmac_f32_e32 v132, v34, v176
	v_fmac_f32_e32 v131, v34, v177
	v_add_f32_e32 v18, 1.0, v60
	v_pk_fma_f32 v[60:61], v[14:15], v[36:37], v[22:23] op_sel_hi:[0,1,1]
	v_add_u32_e32 v36, 0x500, v96
	v_fmac_f32_e32 v134, v35, v138
	v_fmac_f32_e32 v133, v35, v139
	v_fmac_f32_e32 v132, v35, v140
	v_fmac_f32_e32 v131, v35, v141
	v_fma_f32 v46, v116, v18, v56
	global_load_dwordx4 v[138:141], v[16:17], off offset:48
	s_nop 0
	global_load_dwordx4 v[16:19], v[16:17], off offset:32
	v_mov_b32_e32 v14, v15
	v_ashrrev_i32_e32 v37, 31, v36
	v_fmac_f32_e32 v135, v42, v47
	global_load_dwordx4 v[116:119], v[32:33], off offset:16
	global_load_dwordx4 v[26:29], v[32:33], off
	v_lshlrev_b64 v[30:31], 2, v[36:37]
	v_pk_fma_f32 v[14:15], v[14:15], v[20:21], v[60:61] op_sel_hi:[0,1,1]
	v_fmac_f32_e32 v135, v34, v51
	s_waitcnt vmcnt(15)
	v_fmac_f32_e32 v134, v142, v46
	v_fmac_f32_e32 v133, v143, v46
	v_fmac_f32_e32 v132, v144, v46
	v_fmac_f32_e32 v131, v145, v46
	global_load_dwordx4 v[142:145], v[32:33], off offset:48
	global_load_dwordx4 v[22:25], v[32:33], off offset:32
	v_lshl_add_u64 v[32:33], s[30:31], 0, v[30:31]
	v_pk_fma_f32 v[14:15], v[40:41], v[182:183], v[14:15] op_sel_hi:[1,0,1]
	v_fmac_f32_e32 v136, v35, v54
	v_fmac_f32_e32 v135, v35, v55
	v_lshl_add_u64 v[38:39], s[34:35], 0, v[30:31]
	global_load_dwordx4 v[30:33], v[32:33], off
	s_nop 0
	global_load_dwordx4 v[54:57], v[38:39], off
	v_lshlrev_b64 v[36:37], 5, v[36:37]
	v_pk_fma_f32 v[14:15], v[42:43], v[44:45], v[14:15] op_sel_hi:[0,1,1]
	s_waitcnt vmcnt(18)
	v_fmac_f32_e32 v136, v66, v46
	v_fmac_f32_e32 v135, v67, v46
	v_lshl_add_u64 v[66:67], s[92:93], 0, v[36:37]
	v_pk_fma_f32 v[14:15], v[34:35], v[48:49], v[14:15] op_sel_hi:[0,1,1]
	v_mov_b32_e32 v20, v35
	s_waitcnt vmcnt(17)
	v_fmac_f32_e32 v134, v50, v150
	v_fmac_f32_e32 v133, v50, v151
	v_fmac_f32_e32 v132, v50, v152
	v_fmac_f32_e32 v131, v50, v153
	global_load_dwordx4 v[150:153], v[66:67], off offset:16
	global_load_dwordx4 v[36:39], v[66:67], off
	v_pk_fma_f32 v[14:15], v[20:21], v[52:53], v[14:15] op_sel_hi:[0,1,1]
	v_pk_fma_f32 v[14:15], v[64:65], v[46:47], v[14:15] op_sel_hi:[1,0,1]
	s_waitcnt vmcnt(18)
	v_fmac_f32_e32 v136, v50, v70
	v_pk_fma_f32 v[14:15], v[50:51], v[68:69], v[14:15] op_sel_hi:[0,1,1]
	s_waitcnt vmcnt(16)
; template <int L, bool ROUTER, bool WRITE_HB> __device__ __forceinline__ void p_ln_mix(const Args& a, LAS unsigned char* lds, XT* X) {
;     ...
;                 const float* md = mod + (size_t)(m >> 12) * D6;
;                 float lg[8] = {0.f, 0.f, 0.f, 0.f, 0.f, 0.f, 0.f, 0.f};
; #pragma unroll
;                 for (int j = 0; j < 8; ++j) { const int k = j * 256 + lane * 4; const f32x4 sh = *(const f32x4*)(md + 6144 + k), scf = *(const f32x4*)(md + 8192 + k); const f32x4 hv = v[j] * (1.f + scf) + sh;
; #pragma unroll
;                     for (int i = 0; i < 4; ++i) { const f32x4 w0 = *(const f32x4*)(wr + (size_t)(k + i) * 8), w1 = *(const f32x4*)(wr + (size_t)(k + i) * 8 + 4); const float hx = hv[i];
;                         lg[0] += hx * w0.x; lg[1] += hx * w0.y; lg[2] += hx * w0.z; lg[3] += hx * w0.w; lg[4] += hx * w1.x; lg[5] += hx * w1.y; lg[6] += hx * w1.z; lg[7] += hx * w1.w; } }
	v_pk_fma_f32 v[34:35], v[58:59], v[154:155], v[14:15] op_sel_hi:[0,1,1]
	v_add_f32_e32 v14, 1.0, v63
	v_fmac_f32_e32 v136, v58, v156
	v_fmac_f32_e32 v59, v115, v14
	v_fmac_f32_e32 v135, v50, v71
	s_waitcnt vmcnt(14)
	v_fmac_f32_e32 v136, v59, v4
	s_waitcnt vmcnt(12)
	v_add_f32_e32 v4, 1.0, v72
	v_fmac_f32_e32 v135, v58, v157
	v_fma_f32 v46, v112, v4, v6
	v_add_u32_e32 v4, 0x502, v96
	v_fmac_f32_e32 v135, v59, v5
	v_ashrrev_i32_e32 v5, 31, v4
	v_lshlrev_b64 v[4:5], 5, v[4:5]
	v_fmac_f32_e32 v134, v58, v146
	v_fmac_f32_e32 v133, v58, v147
	v_fmac_f32_e32 v132, v58, v148
	v_fmac_f32_e32 v131, v58, v149
	global_load_dwordx4 v[50:53], v[66:67], off offset:48
	global_load_dwordx4 v[40:43], v[66:67], off offset:32
	v_lshl_add_u64 v[4:5], s[92:93], 0, v[4:5]
	v_mov_b32_e32 v44, v59
	v_fmac_f32_e32 v134, v59, v158
	v_fmac_f32_e32 v133, v59, v159
	v_fmac_f32_e32 v132, v59, v160
	v_fmac_f32_e32 v131, v59, v161
	s_waitcnt vmcnt(12)
	v_fmac_f32_e32 v136, v12, v46
	v_fmac_f32_e32 v135, v13, v46
	global_load_dwordx4 v[58:61], v[4:5], off offset:16
	global_load_dwordx4 v[12:15], v[4:5], off
	v_add_f32_e32 v6, 1.0, v73
	v_fma_f32 v48, v113, v6, v7
	v_add_f32_e32 v6, 1.0, v74
	v_fma_f32 v8, v110, v6, v8
	v_add_u32_e32 v70, 0x600, v96
	v_fmac_f32_e32 v134, v162, v46
	v_fmac_f32_e32 v133, v163, v46
	v_fmac_f32_e32 v132, v164, v46
	v_fmac_f32_e32 v131, v165, v46
	v_ashrrev_i32_e32 v71, 31, v70
	v_pk_fma_f32 v[2:3], v[44:45], v[2:3], v[34:35] op_sel_hi:[0,1,1]
	v_pk_fma_f32 v[2:3], v[10:11], v[46:47], v[2:3] op_sel_hi:[1,0,1]
	s_waitcnt vmcnt(13)
	v_fmac_f32_e32 v134, v48, v138
	s_waitcnt vmcnt(12)
	v_fmac_f32_e32 v136, v48, v18
	v_fmac_f32_e32 v135, v48, v19
	v_fmac_f32_e32 v133, v48, v139
	v_fmac_f32_e32 v132, v48, v140
	s_waitcnt vmcnt(10)
	v_fmac_f32_e32 v136, v8, v28
	v_add_f32_e32 v28, 1.0, v75
	v_fmac_f32_e32 v9, v111, v28
	v_add_u32_e32 v28, 0x602, v96
	v_fmac_f32_e32 v135, v8, v29
	v_ashrrev_i32_e32 v29, 31, v28
	v_fmac_f32_e32 v131, v48, v141
	global_load_dwordx4 v[62:65], v[4:5], off offset:48
	global_load_dwordx4 v[18:21], v[4:5], off offset:32
	s_waitcnt vmcnt(10)
	v_fmac_f32_e32 v136, v9, v24
	v_lshlrev_b64 v[4:5], 2, v[70:71]
	v_lshlrev_b64 v[70:71], 5, v[70:71]
	v_fmac_f32_e32 v135, v9, v25
	v_lshlrev_b64 v[28:29], 5, v[28:29]
	v_lshl_add_u64 v[6:7], s[30:31], 0, v[4:5]
	s_waitcnt vmcnt(8)
	v_add_f32_e32 v24, 1.0, v54
	v_fma_f32 v24, v108, v24, v30
	v_lshl_add_u64 v[66:67], s[34:35], 0, v[4:5]
	v_lshl_add_u64 v[138:139], s[92:93], 0, v[70:71]
	v_fmac_f32_e32 v134, v8, v116
	v_fmac_f32_e32 v133, v8, v117
	v_fmac_f32_e32 v132, v8, v118
	v_fmac_f32_e32 v131, v8, v119
	v_add_f32_e32 v25, 1.0, v55
	global_load_dwordx4 v[4:7], v[6:7], off
	s_nop 0
	global_load_dwordx4 v[66:69], v[66:67], off
	s_nop 0
	global_load_dwordx4 v[70:73], v[138:139], off offset:16
	global_load_dwordx4 v[112:115], v[138:139], off
	v_fmac_f32_e32 v134, v9, v142
	s_waitcnt vmcnt(10)
	v_fmac_f32_e32 v136, v38, v24
	v_fmac_f32_e32 v135, v39, v24
	v_lshl_add_u64 v[38:39], s[92:93], 0, v[28:29]
	v_fmac_f32_e32 v133, v9, v143
	v_fmac_f32_e32 v132, v9, v144
	v_fmac_f32_e32 v131, v9, v145
	global_load_dwordx4 v[116:119], v[138:139], off offset:48
	s_nop 0
	global_load_dwordx4 v[138:141], v[138:139], off offset:32
	s_nop 0
	global_load_dwordx4 v[142:145], v[38:39], off offset:16
	global_load_dwordx4 v[146:149], v[38:39], off
	v_fma_f32 v54, v109, v25, v31
	global_load_dwordx4 v[28:31], v[38:39], off offset:48
	global_load_dwordx4 v[108:111], v[38:39], off offset:32
	v_add_u32_e32 v38, 0x700, v96
	v_ashrrev_i32_e32 v39, 31, v38
	v_lshlrev_b64 v[74:75], 2, v[38:39]
	v_fmac_f32_e32 v134, v150, v24
	v_fmac_f32_e32 v133, v151, v24
	v_lshl_add_u64 v[150:151], s[30:31], 0, v[74:75]
	v_fmac_f32_e32 v132, v152, v24
	v_fmac_f32_e32 v131, v153, v24
	v_lshl_add_u64 v[74:75], s[34:35], 0, v[74:75]
	global_load_dwordx4 v[150:153], v[150:151], off
	s_nop 0
	global_load_dwordx4 v[154:157], v[74:75], off
	v_add_f32_e32 v25, 1.0, v56
	v_lshlrev_b64 v[38:39], 5, v[38:39]
	s_waitcnt vmcnt(16)
	v_fmac_f32_e32 v136, v54, v42
	v_fma_f32 v32, v106, v25, v32
	v_lshl_add_u64 v[38:39], s[92:93], 0, v[38:39]
	v_fmac_f32_e32 v135, v54, v43
	global_load_dwordx4 v[158:161], v[38:39], off offset:16
	global_load_dwordx4 v[162:165], v[38:39], off
	v_fmac_f32_e32 v134, v54, v50
	v_fmac_f32_e32 v133, v54, v51
	v_fmac_f32_e32 v132, v54, v52
	v_fmac_f32_e32 v131, v54, v53
	s_waitcnt vmcnt(16)
	v_fmac_f32_e32 v136, v32, v14
	v_add_u32_e32 v14, 0x702, v96
	v_fmac_f32_e32 v135, v32, v15
	v_ashrrev_i32_e32 v15, 31, v14
	global_load_dwordx4 v[50:53], v[38:39], off offset:48
	global_load_dwordx4 v[166:169], v[38:39], off offset:32
	v_lshlrev_b64 v[14:15], 5, v[14:15]
	v_lshl_add_u64 v[14:15], s[92:93], 0, v[14:15]
	global_load_dwordx4 v[170:173], v[14:15], off offset:16
	global_load_dwordx4 v[174:177], v[14:15], off
	global_load_dwordx4 v[178:181], v[14:15], off offset:48
	global_load_dwordx4 v[182:185], v[14:15], off offset:32
	v_pk_fma_f32 v[2:3], v[48:49], v[16:17], v[2:3] op_sel_hi:[0,1,1]
	v_pk_fma_f32 v[2:3], v[8:9], v[26:27], v[2:3] op_sel_hi:[0,1,1]
	v_mov_b32_e32 v8, v9
	v_pk_fma_f32 v[2:3], v[8:9], v[22:23], v[2:3] op_sel_hi:[0,1,1]
	v_add_f32_e32 v14, 1.0, v57
	v_pk_fma_f32 v[2:3], v[36:37], v[24:25], v[2:3] op_sel_hi:[1,0,1]
	v_fmac_f32_e32 v33, v107, v14
	v_pk_fma_f32 v[2:3], v[54:55], v[40:41], v[2:3] op_sel_hi:[0,1,1]
	v_pk_fma_f32 v[2:3], v[32:33], v[12:13], v[2:3] op_sel_hi:[0,1,1]
	v_mov_b32_e32 v8, v33
	v_fmac_f32_e32 v134, v32, v58
	v_fmac_f32_e32 v133, v32, v59
	v_fmac_f32_e32 v132, v32, v60
	v_fmac_f32_e32 v131, v32, v61
	s_waitcnt vmcnt(21)
	v_fmac_f32_e32 v134, v33, v62
	s_waitcnt vmcnt(20)
; __device__ __forceinline__ float wave_sum(float v) {
; #pragma unroll
;     for (int o = 1; o < 64; o <<= 1) v += __shfl_xor(v, o);
;     return v;
; }
; template <int L, bool ROUTER, bool WRITE_HB> __device__ __forceinline__ void p_ln_mix(const Args& a, LAS unsigned char* lds, XT* X) {
;     ...
;                     for (int i = 0; i < 4; ++i) { const f32x4 w0 = *(const f32x4*)(wr + (size_t)(k + i) * 8), w1 = *(const f32x4*)(wr + (size_t)(k + i) * 8 + 4); const float hx = hv[i];
;                         lg[0] += hx * w0.x; lg[1] += hx * w0.y; lg[2] += hx * w0.z; lg[3] += hx * w0.w; lg[4] += hx * w1.x; lg[5] += hx * w1.y; lg[6] += hx * w1.z; lg[7] += hx * w1.w; } }
; #pragma unroll
;                 for (int e = 0; e < 8; ++e) lg[e] = wave_sum(lg[e]);
	v_pk_fma_f32 v[2:3], v[8:9], v[18:19], v[2:3] op_sel_hi:[0,1,1]
	v_fmac_f32_e32 v136, v33, v20
	v_fmac_f32_e32 v135, v33, v21
	v_fmac_f32_e32 v133, v33, v63
	v_fmac_f32_e32 v132, v33, v64
	v_fmac_f32_e32 v131, v33, v65
	s_waitcnt vmcnt(18)
	v_add_f32_e32 v14, 1.0, v66
	v_fma_f32 v4, v104, v14, v4
	v_add_f32_e32 v14, 1.0, v67
	v_fma_f32 v14, v105, v14, v5
	s_waitcnt vmcnt(16)
	v_pk_fma_f32 v[2:3], v[112:113], v[4:5], v[2:3] op_sel_hi:[1,0,1]
	v_add_f32_e32 v5, 1.0, v69
	v_fmac_f32_e32 v136, v114, v4
	v_fmac_f32_e32 v135, v115, v4
	v_fmac_f32_e32 v134, v70, v4
	v_fmac_f32_e32 v133, v71, v4
	v_fmac_f32_e32 v132, v72, v4
	v_fmac_f32_e32 v131, v73, v4
	v_add_f32_e32 v4, 1.0, v68
	v_fmac_f32_e32 v7, v103, v5
	v_fma_f32 v4, v102, v4, v6
	s_waitcnt vmcnt(14)
	v_pk_fma_f32 v[2:3], v[14:15], v[138:139], v[2:3] op_sel_hi:[0,1,1]
	v_fmac_f32_e32 v136, v14, v140
	v_fmac_f32_e32 v135, v14, v141
	v_fmac_f32_e32 v134, v14, v116
	v_fmac_f32_e32 v133, v14, v117
	v_fmac_f32_e32 v132, v14, v118
	v_fmac_f32_e32 v131, v14, v119
	s_waitcnt vmcnt(8)
	v_add_f32_e32 v5, 1.0, v154
	v_fma_f32 v6, v100, v5, v150
	v_add_f32_e32 v5, 1.0, v155
	v_fma_f32 v8, v101, v5, v151
	v_add_f32_e32 v5, 1.0, v156
	v_fma_f32 v10, v98, v5, v152
	v_add_f32_e32 v5, 1.0, v157
	v_fmac_f32_e32 v136, v4, v148
	v_fmac_f32_e32 v135, v4, v149
	v_fmac_f32_e32 v134, v4, v142
	v_fmac_f32_e32 v133, v4, v143
	v_fmac_f32_e32 v132, v4, v144
	v_fmac_f32_e32 v131, v4, v145
	v_pk_fma_f32 v[2:3], v[4:5], v[146:147], v[2:3] op_sel_hi:[0,1,1]
	v_mov_b32_e32 v4, v7
	v_pk_fma_f32 v[2:3], v[4:5], v[108:109], v[2:3] op_sel_hi:[0,1,1]
	s_waitcnt vmcnt(6)
	v_pk_fma_f32 v[2:3], v[162:163], v[6:7], v[2:3] op_sel_hi:[1,0,1]
	v_fmac_f32_e32 v153, v99, v5
	s_waitcnt vmcnt(4)
	v_pk_fma_f32 v[2:3], v[8:9], v[166:167], v[2:3] op_sel_hi:[0,1,1]
	s_waitcnt vmcnt(2)
	v_pk_fma_f32 v[2:3], v[10:11], v[174:175], v[2:3] op_sel_hi:[0,1,1]
	v_mov_b32_e32 v4, v153
	s_waitcnt vmcnt(0)
	v_pk_fma_f32 v[2:3], v[4:5], v[182:183], v[2:3] op_sel_hi:[0,1,1]
	v_fmac_f32_e32 v136, v7, v110
	v_fmac_f32_e32 v136, v164, v6
	v_fmac_f32_e32 v136, v8, v168
	v_fmac_f32_e32 v136, v10, v176
	s_waitcnt lgkmcnt(0)
	s_nop 1
	v_add_f32_dpp v2, v2, v2 quad_perm:[1,0,3,2] row_mask:0xf bank_mask:0xf
	v_add_f32_dpp v3, v3, v3 quad_perm:[1,0,3,2] row_mask:0xf bank_mask:0xf
	v_fmac_f32_e32 v135, v7, v111
	v_fmac_f32_e32 v134, v7, v28
	v_fmac_f32_e32 v133, v7, v29
	v_fmac_f32_e32 v132, v7, v30
	v_fmac_f32_e32 v131, v7, v31
	s_waitcnt lgkmcnt(0)
	s_nop 1
	v_add_f32_dpp v2, v2, v2 quad_perm:[2,3,0,1] row_mask:0xf bank_mask:0xf
	v_add_f32_dpp v3, v3, v3 quad_perm:[2,3,0,1] row_mask:0xf bank_mask:0xf
	v_fmac_f32_e32 v136, v153, v184
	v_fmac_f32_e32 v135, v165, v6
	v_fmac_f32_e32 v134, v158, v6
	v_fmac_f32_e32 v133, v159, v6
	v_fmac_f32_e32 v132, v160, v6
	v_fmac_f32_e32 v131, v161, v6
	v_fmac_f32_e32 v135, v8, v169
	v_fmac_f32_e32 v134, v8, v50
	v_fmac_f32_e32 v135, v10, v177
	s_waitcnt lgkmcnt(0)
	s_nop 1
	v_add_f32_dpp v2, v2, v2 row_half_mirror row_mask:0xf bank_mask:0xf
	v_add_f32_dpp v3, v3, v3 row_half_mirror row_mask:0xf bank_mask:0xf
	s_waitcnt lgkmcnt(0)
	s_nop 1
	v_add_f32_dpp v6, v136, v136 quad_perm:[1,0,3,2] row_mask:0xf bank_mask:0xf
	v_fmac_f32_e32 v134, v10, v170
	v_fmac_f32_e32 v135, v153, v185
	v_fmac_f32_e32 v134, v153, v178
	s_waitcnt lgkmcnt(0)
	s_nop 1
	v_add_f32_dpp v2, v2, v2 row_mirror row_mask:0xf bank_mask:0xf
	v_add_f32_dpp v3, v3, v3 row_mirror row_mask:0xf bank_mask:0xf
	s_waitcnt lgkmcnt(0)
	s_nop 1
	v_add_f32_dpp v6, v6, v6 quad_perm:[2,3,0,1] row_mask:0xf bank_mask:0xf
	v_fmac_f32_e32 v133, v8, v51
	v_fmac_f32_e32 v132, v8, v52
	v_fmac_f32_e32 v131, v8, v53
	ds_bpermute_b32 v4, v129, v2
	ds_bpermute_b32 v5, v129, v3
	v_fmac_f32_e32 v133, v10, v171
	s_waitcnt lgkmcnt(0)
	v_pk_add_f32 v[2:3], v[2:3], v[4:5]
	s_waitcnt lgkmcnt(0)
	s_nop 1
	v_add_f32_dpp v4, v135, v135 quad_perm:[1,0,3,2] row_mask:0xf bank_mask:0xf
	s_waitcnt lgkmcnt(0)
	s_nop 1
	v_add_f32_dpp v6, v6, v6 row_half_mirror row_mask:0xf bank_mask:0xf
	s_waitcnt lgkmcnt(0)
	s_nop 1
	v_add_f32_dpp v7, v134, v134 quad_perm:[1,0,3,2] row_mask:0xf bank_mask:0xf
	v_fmac_f32_e32 v132, v10, v172
	v_fmac_f32_e32 v131, v10, v173
	s_waitcnt lgkmcnt(0)
	s_nop 1
	v_add_f32_dpp v5, v4, v4 quad_perm:[2,3,0,1] row_mask:0xf bank_mask:0xf
	s_waitcnt lgkmcnt(0)
	s_nop 1
	v_add_f32_dpp v7, v7, v7 quad_perm:[2,3,0,1] row_mask:0xf bank_mask:0xf
	s_waitcnt lgkmcnt(0)
	s_nop 1
	v_add_f32_dpp v6, v6, v6 row_mirror row_mask:0xf bank_mask:0xf
	ds_bpermute_b32 v11, v129, v6
	v_fmac_f32_e32 v133, v153, v179
	s_waitcnt lgkmcnt(0)
	s_nop 1
	v_add_f32_dpp v9, v5, v5 row_half_mirror row_mask:0xf bank_mask:0xf
	s_waitcnt lgkmcnt(0)
	s_nop 1
	v_add_f32_dpp v7, v7, v7 row_half_mirror row_mask:0xf bank_mask:0xf
	s_waitcnt lgkmcnt(0)
	v_add_f32_e32 v6, v6, v11
	v_fmac_f32_e32 v132, v153, v180
	v_fmac_f32_e32 v131, v153, v181
	s_waitcnt lgkmcnt(0)
	s_nop 1
	v_add_f32_dpp v9, v9, v9 row_mirror row_mask:0xf bank_mask:0xf
	s_waitcnt lgkmcnt(0)
	s_nop 1
	v_add_f32_dpp v11, v7, v7 row_mirror row_mask:0xf bank_mask:0xf
	ds_bpermute_b32 v10, v129, v9
	ds_bpermute_b32 v12, v129, v11
	ds_bpermute_b32 v4, v130, v2
	s_waitcnt lgkmcnt(0)
	v_add_f32_e32 v8, v9, v10
	s_waitcnt lgkmcnt(0)
	v_add_f32_e32 v10, v11, v12
	s_waitcnt lgkmcnt(0)
	s_nop 1
	v_add_f32_dpp v13, v133, v133 quad_perm:[1,0,3,2] row_mask:0xf bank_mask:0xf
	s_waitcnt lgkmcnt(0)
	s_nop 1
	v_add_f32_dpp v14, v131, v131 quad_perm:[1,0,3,2] row_mask:0xf bank_mask:0xf
	s_waitcnt lgkmcnt(0)
	s_nop 1
	v_add_f32_dpp v12, v132, v132 quad_perm:[1,0,3,2] row_mask:0xf bank_mask:0xf
	ds_bpermute_b32 v5, v130, v3
	s_waitcnt lgkmcnt(0)
	s_nop 1
	v_add_f32_dpp v13, v13, v13 quad_perm:[2,3,0,1] row_mask:0xf bank_mask:0xf
	s_waitcnt lgkmcnt(0)
	s_nop 1
	v_add_f32_dpp v14, v14, v14 quad_perm:[2,3,0,1] row_mask:0xf bank_mask:0xf
	s_waitcnt lgkmcnt(0)
	s_nop 1
	v_add_f32_dpp v12, v12, v12 quad_perm:[2,3,0,1] row_mask:0xf bank_mask:0xf
	ds_bpermute_b32 v7, v130, v6
	s_waitcnt lgkmcnt(0)
	s_nop 1
	v_add_f32_dpp v13, v13, v13 row_half_mirror row_mask:0xf bank_mask:0xf
	s_waitcnt lgkmcnt(0)
	s_nop 1
	v_add_f32_dpp v12, v12, v12 row_half_mirror row_mask:0xf bank_mask:0xf
	s_waitcnt lgkmcnt(0)
	s_nop 1
	v_add_f32_dpp v14, v14, v14 row_half_mirror row_mask:0xf bank_mask:0xf
	s_waitcnt lgkmcnt(0)
	s_nop 1
	v_add_f32_dpp v13, v13, v13 row_mirror row_mask:0xf bank_mask:0xf
	ds_bpermute_b32 v15, v129, v13
	ds_bpermute_b32 v9, v130, v8
	s_waitcnt lgkmcnt(0)
	s_nop 1
	v_add_f32_dpp v16, v12, v12 row_mirror row_mask:0xf bank_mask:0xf
	s_waitcnt lgkmcnt(0)
	s_nop 1
	v_add_f32_dpp v17, v14, v14 row_mirror row_mask:0xf bank_mask:0xf
	ds_bpermute_b32 v18, v129, v16
	ds_bpermute_b32 v19, v129, v17
	s_waitcnt lgkmcnt(0)
	v_add_f32_e32 v12, v13, v15
	ds_bpermute_b32 v11, v130, v10
	ds_bpermute_b32 v13, v130, v12
	s_waitcnt lgkmcnt(0)
	v_add_f32_e32 v14, v16, v18
	s_waitcnt lgkmcnt(0)
	v_add_f32_e32 v16, v17, v19
	ds_bpermute_b32 v15, v130, v14
	ds_bpermute_b32 v17, v130, v16
	s_and_saveexec_b64 s[38:39], vcc
	s_cbranch_execz .LBB0_2024
; template <int L, bool ROUTER, bool WRITE_HB> __device__ __forceinline__ void p_ln_mix(const Args& a, LAS unsigned char* lds, XT* X) {
;     ...
;                 for (int e = 0; e < 8; ++e) lg[e] = wave_sum(lg[e]);
;                 int i0 = 0; float v0 = lg[0];
; #pragma unroll
;                 for (int e = 1; e < 8; ++e) if (lg[e] > v0) { v0 = lg[e]; i0 = e; }
;                 int i1 = -1; float v1 = -INFINITY;
; #pragma unroll
;                 for (int e = 0; e < 8; ++e) if (e != i0 && lg[e] > v1) { v1 = lg[e]; i1 = e; }
;                 const float ex = __expf(v1 - v0), w0 = 1.f / (1.f + ex), w1 = ex / (1.f + ex);
;                 if (lane == 0) { route_e[m * 2] = i0; route_e[m * 2 + 1] = i1; route_w[m * 2] = w0; route_w[m * 2 + 1] = w1; el[(wave * 8 + r) * 2] = i0; el[(wave * 8 + r) * 2 + 1] = i1; }
	v_pk_add_f32 v[2:3], v[2:3], v[4:5]
	v_add_f32_e32 v6, v6, v7
	v_cmp_gt_f32_e32 vcc, v3, v2
	v_add_f32_e32 v8, v8, v9
	s_waitcnt lgkmcnt(0)
	v_add_f32_e32 v10, v10, v11
	v_cndmask_b32_e32 v4, v2, v3, vcc
	v_cmp_gt_f32_e64 s[8:9], v6, v4
	s_waitcnt lgkmcnt(0)
	v_add_f32_e32 v12, v12, v13
	s_waitcnt lgkmcnt(0)
	v_add_f32_e32 v14, v14, v15
	v_cndmask_b32_e64 v4, v4, v6, s[8:9]
	v_cmp_gt_f32_e64 s[10:11], v8, v4
	s_waitcnt lgkmcnt(0)
	v_add_f32_e32 v16, v16, v17
	v_cmp_nlg_f32_e64 s[20:21], s49, v2
	v_cndmask_b32_e64 v4, v4, v8, s[10:11]
	v_cmp_gt_f32_e64 s[12:13], v10, v4
	s_nop 1
	v_cndmask_b32_e64 v4, v4, v10, s[12:13]
	v_cmp_gt_f32_e64 s[14:15], v12, v4
	s_nop 1
	v_cndmask_b32_e64 v4, v4, v12, s[14:15]
	v_cmp_gt_f32_e64 s[16:17], v14, v4
	s_nop 1
	v_cndmask_b32_e64 v5, v4, v14, s[16:17]
	v_cndmask_b32_e64 v4, 0, 1, vcc
	v_cndmask_b32_e64 v4, v4, 2, s[8:9]
	v_cndmask_b32_e64 v4, v4, 3, s[10:11]
	v_cndmask_b32_e64 v4, v4, 4, s[12:13]
	v_cndmask_b32_e64 v4, v4, 5, s[14:15]
	v_cndmask_b32_e64 v4, v4, 6, s[16:17]
	v_cmp_ngt_f32_e32 vcc, v16, v5
	s_and_b64 s[22:23], s[16:17], vcc
	s_nop 0
	v_cndmask_b32_e32 v4, 7, v4, vcc
	v_cmp_eq_u32_e64 s[18:19], 0, v4
	s_or_b64 s[18:19], s[18:19], s[20:21]
	v_cmp_ne_u32_e64 s[16:17], 1, v4
	v_cndmask_b32_e64 v2, v2, v124, s[18:19]
	v_cmp_gt_f32_e64 s[20:21], v3, v2
	s_and_b64 s[16:17], s[16:17], s[20:21]
	v_cndmask_b32_e64 v2, v2, v3, s[16:17]
	v_cmp_ne_u32_e64 s[14:15], 2, v4
	v_cmp_gt_f32_e64 s[20:21], v6, v2
	s_and_b64 s[14:15], s[14:15], s[20:21]
	v_cndmask_b32_e64 v2, v2, v6, s[14:15]
	v_cmp_ne_u32_e64 s[12:13], 3, v4
	v_cmp_gt_f32_e64 s[20:21], v8, v2
	s_and_b64 s[12:13], s[12:13], s[20:21]
	v_cndmask_b32_e64 v2, v2, v8, s[12:13]
	v_cmp_ne_u32_e64 s[10:11], 4, v4
	v_cmp_gt_f32_e64 s[20:21], v10, v2
	s_and_b64 s[10:11], s[10:11], s[20:21]
	v_cndmask_b32_e64 v2, v2, v10, s[10:11]
	v_cmp_ne_u32_e64 s[8:9], 5, v4
	v_cmp_gt_f32_e64 s[20:21], v12, v2
	s_and_b64 s[8:9], s[8:9], s[20:21]
	v_cndmask_b32_e64 v2, v2, v12, s[8:9]
	v_cmp_ngt_f32_e64 s[20:21], v14, v2
	s_or_b64 s[20:21], s[22:23], s[20:21]
	v_cndmask_b32_e32 v5, v16, v5, vcc
	v_cndmask_b32_e64 v2, v14, v2, s[20:21]
	v_cmp_gt_f32_e64 s[22:23], v16, v2
	s_and_b64 s[22:23], vcc, s[22:23]
	v_cndmask_b32_e64 v3, 0, -1, s[18:19]
	v_cndmask_b32_e64 v2, v2, v16, s[22:23]
	v_sub_f32_e32 v2, v2, v5
	v_cndmask_b32_e64 v3, v3, 1, s[16:17]
	v_mul_f32_e32 v2, 0x3fb8aa3b, v2
	v_cndmask_b32_e64 v3, v3, 2, s[14:15]
	v_exp_f32_e32 v2, v2
	v_cndmask_b32_e64 v3, v3, 3, s[12:13]
	v_cndmask_b32_e64 v3, v3, 4, s[10:11]
	v_cndmask_b32_e64 v3, v3, 5, s[8:9]
	v_cndmask_b32_e64 v3, 6, v3, s[20:21]
	v_add_f32_e32 v6, 1.0, v2
	v_cndmask_b32_e64 v5, v3, 7, s[22:23]
	v_div_scale_f32 v3, s[8:9], v6, v6, v2
	v_rcp_f32_e32 v7, v3
	s_add_u32 s8, s66, s36
	s_addc_u32 s9, s67, s37
	v_fma_f32 v8, -v3, v7, 1.0
	v_fmac_f32_e32 v7, v8, v7
	v_div_scale_f32 v8, vcc, v2, v6, v2
	v_mul_f32_e32 v9, v8, v7
	v_fma_f32 v10, -v3, v9, v8
	v_fmac_f32_e32 v9, v10, v7
	v_fma_f32 v3, -v3, v9, v8
	v_div_scale_f32 v8, s[10:11], v6, v6, 1.0
	v_rcp_f32_e32 v10, v8
	v_div_fmas_f32 v3, v3, v7, v9
	v_div_fixup_f32 v3, v3, v6, v2
	global_store_dwordx2 v122, v[4:5], s[8:9]
	v_fma_f32 v2, -v8, v10, 1.0
	v_fmac_f32_e32 v10, v2, v10
	v_div_scale_f32 v2, vcc, 1.0, v6, 1.0
	v_mul_f32_e32 v7, v2, v10
	v_fma_f32 v9, -v8, v7, v2
	v_fmac_f32_e32 v7, v9, v10
	v_fma_f32 v2, -v8, v7, v2
	v_div_fmas_f32 v2, v2, v10, v7
	v_div_fixup_f32 v2, v2, v6, 1.0
	global_store_dwordx2 v123, v[2:3], s[8:9]
	s_add_i32 s8, s42, s51
	v_mov_b32_e32 v2, s8
	ds_write_b64 v2, v[4:5]

; __device__ __forceinline__ f32x4 xr2f(XRaw w) { return (f32x4){bflo(w.x), bfhi(w.x), bflo(w.y), bfhi(w.y)}; }
; template <int L> __device__ __forceinline__ void p_moe_combine_ln(const Args& a, const XT* X, float* out) {
;     ...
; #pragma unroll
;             for (int j = 0; j < 8; ++j) { const int k = j * 256 + lane * 4; const f32x4 gf = *(const f32x4*)(md + 10240 + k);
;                 const f32x4 ya = (f32x4){bflo(y0v[j].x), bfhi(y0v[j].x), bflo(y0v[j].y), bfhi(y0v[j].y)}, yb = (f32x4){bflo(y1v[j].x), bfhi(y1v[j].x), bflo(y1v[j].y), bfhi(y1v[j].y)};
;                 v[j] = ALPHA * xr2f(xv[j]) + (1.f + gf) * (w0 * ya + w1 * yb); }
.LBB0_2327:
	s_ashr_i32 s0, s0, 12
	s_mul_hi_i32 s1, s0, 0xc000
	s_mul_i32 s0, s0, 0xc000
	s_add_u32 s0, s66, s0
	s_addc_u32 s1, s67, s1
	s_add_u32 s0, s0, 0x13a000
	s_addc_u32 s1, s1, 0
	v_lshlrev_b64 v[76:77], 2, v[0:1]
	v_lshl_add_u64 v[0:1], s[0:1], 0, v[76:77]
	v_lshl_add_u64 v[122:123], v[122:123], 2, s[0:1]
	v_lshl_add_u64 v[120:121], v[120:121], 2, s[0:1]
	global_load_dwordx4 v[0:3], v[0:1], off
	v_lshl_add_u64 v[118:119], v[118:119], 2, s[0:1]
	global_load_dwordx4 v[130:133], v[122:123], off
	global_load_dwordx4 v[134:137], v[118:119], off
	s_waitcnt vmcnt(18)
	v_lshlrev_b32_e32 v140, 16, v106
	global_load_dwordx4 v[120:123], v[120:121], off
	v_and_b32_e32 v141, 0xffff0000, v106
	v_lshlrev_b32_e32 v106, 16, v107
	v_and_b32_e32 v107, 0xffff0000, v107
	s_waitcnt vmcnt(18)
	v_lshlrev_b32_e32 v148, 16, v104
	v_and_b32_e32 v149, 0xffff0000, v104
	v_lshlrev_b32_e32 v104, 16, v105
	v_and_b32_e32 v105, 0xffff0000, v105
	v_lshlrev_b32_e32 v144, 16, v102
	v_and_b32_e32 v145, 0xffff0000, v102
	v_lshlrev_b32_e32 v154, 16, v92
	v_and_b32_e32 v155, 0xffff0000, v92
	v_lshlrev_b32_e32 v156, 16, v93
	v_and_b32_e32 v157, 0xffff0000, v93
	v_pk_mul_f32 v[92:93], v[58:59], v[106:107] op_sel:[1,0]
	v_pk_mul_f32 v[106:107], v[58:59], v[140:141] op_sel:[1,0]
	v_pk_mul_f32 v[140:141], v[58:59], v[104:105] op_sel:[1,0]
	v_pk_mul_f32 v[104:105], v[58:59], v[148:149] op_sel:[1,0]
	v_lshlrev_b32_e32 v138, 16, v110
	v_and_b32_e32 v139, 0xffff0000, v110
	v_pk_fma_f32 v[144:145], v[58:59], v[144:145], v[104:105] op_sel_hi:[0,1,1]
	v_lshl_add_u64 v[104:105], v[114:115], 2, s[0:1]
	v_lshlrev_b32_e32 v142, 16, v101
	v_and_b32_e32 v143, 0xffff0000, v101
	v_pk_fma_f32 v[138:139], v[58:59], v[138:139], v[106:107] op_sel_hi:[0,1,1]
	global_load_dwordx4 v[104:107], v[104:105], off
	v_lshlrev_b32_e32 v118, 16, v100
	v_and_b32_e32 v119, 0xffff0000, v100
	v_lshl_add_u64 v[100:101], v[116:117], 2, s[0:1]
	s_waitcnt vmcnt(18)
	v_lshlrev_b32_e32 v116, 16, v96
	v_and_b32_e32 v117, 0xffff0000, v96
	v_lshlrev_b32_e32 v96, 16, v97
	v_and_b32_e32 v97, 0xffff0000, v97
	v_lshlrev_b32_e32 v146, 16, v103
	v_and_b32_e32 v147, 0xffff0000, v103
	v_lshlrev_b32_e32 v150, 16, v98
	v_and_b32_e32 v151, 0xffff0000, v98
	v_lshlrev_b32_e32 v152, 16, v99
	v_and_b32_e32 v153, 0xffff0000, v99
	v_lshlrev_b32_e32 v98, 16, v94
	v_and_b32_e32 v99, 0xffff0000, v94
	v_lshlrev_b32_e32 v94, 16, v95
	global_load_dwordx4 v[100:103], v[100:101], off
	v_and_b32_e32 v95, 0xffff0000, v95
	v_pk_mul_f32 v[96:97], v[58:59], v[96:97] op_sel:[1,0]
	v_lshlrev_b32_e32 v110, 16, v111
	v_and_b32_e32 v111, 0xffff0000, v111
	v_pk_fma_f32 v[94:95], v[58:59], v[94:95], v[96:97] op_sel_hi:[0,1,1]
	v_lshl_add_u64 v[96:97], v[112:113], 2, s[0:1]
	v_pk_mul_f32 v[116:117], v[58:59], v[116:117] op_sel:[1,0]
	v_pk_fma_f32 v[92:93], v[58:59], v[110:111], v[92:93] op_sel_hi:[0,1,1]
	v_pk_fma_f32 v[114:115], v[58:59], v[146:147], v[140:141] op_sel_hi:[0,1,1]
	global_load_dwordx4 v[110:113], v[96:97], off
	v_pk_fma_f32 v[98:99], v[58:59], v[98:99], v[116:117] op_sel_hi:[0,1,1]
	v_lshlrev_b32_e32 v158, 16, v88
	v_and_b32_e32 v159, 0xffff0000, v88
	v_lshlrev_b32_e32 v88, 16, v89
	v_and_b32_e32 v89, 0xffff0000, v89
	s_waitcnt vmcnt(6)
	v_pk_add_f32 v[2:3], v[2:3], 1.0 op_sel_hi:[1,0]
	v_pk_add_f32 v[0:1], v[0:1], 1.0 op_sel_hi:[1,0]
	s_waitcnt vmcnt(5)
	v_pk_add_f32 v[96:97], v[132:133], 1.0 op_sel_hi:[1,0]
	v_pk_add_f32 v[116:117], v[130:131], 1.0 op_sel_hi:[1,0]
	v_pk_mul_f32 v[2:3], v[92:93], v[2:3]
	s_waitcnt vmcnt(3)
	v_pk_add_f32 v[122:123], v[122:123], 1.0 op_sel_hi:[1,0]
	v_pk_add_f32 v[120:121], v[120:121], 1.0 op_sel_hi:[1,0]
	v_pk_mul_f32 v[0:1], v[138:139], v[0:1]
	v_pk_mul_f32 v[92:93], v[114:115], v[96:97]
	v_pk_mul_f32 v[114:115], v[94:95], v[122:123]
	v_pk_mul_f32 v[96:97], v[144:145], v[116:117]
	v_pk_mul_f32 v[116:117], v[98:99], v[120:121]
	v_pk_fma_f32 v[98:99], v[118:119], s[18:19], v[0:1] op_sel_hi:[1,0,1]
	v_pk_fma_f32 v[0:1], v[156:157], s[18:19], v[114:115] op_sel_hi:[1,0,1]
	v_lshlrev_b32_e32 v114, 16, v90
	v_and_b32_e32 v115, 0xffff0000, v90
	v_lshlrev_b32_e32 v90, 16, v91
	v_and_b32_e32 v91, 0xffff0000, v91
	v_pk_mul_f32 v[90:91], v[58:59], v[90:91] op_sel:[1,0]
	v_pk_fma_f32 v[94:95], v[142:143], s[18:19], v[2:3] op_sel_hi:[1,0,1]
	v_pk_fma_f32 v[2:3], v[154:155], s[18:19], v[116:117] op_sel_hi:[1,0,1]
	v_pk_add_f32 v[116:117], v[136:137], 1.0 op_sel_hi:[1,0]
	v_pk_fma_f32 v[88:89], v[58:59], v[88:89], v[90:91] op_sel_hi:[0,1,1]
	v_lshlrev_b32_e32 v118, 16, v86
	v_and_b32_e32 v119, 0xffff0000, v86
	v_lshlrev_b32_e32 v86, 16, v87
	v_and_b32_e32 v87, 0xffff0000, v87
	v_pk_mul_f32 v[114:115], v[58:59], v[114:115] op_sel:[1,0]
	v_pk_mul_f32 v[88:89], v[88:89], v[116:117]
	v_pk_add_f32 v[120:121], v[134:135], 1.0 op_sel_hi:[1,0]
	v_pk_fma_f32 v[114:115], v[58:59], v[158:159], v[114:115] op_sel_hi:[0,1,1]
	v_pk_fma_f32 v[86:87], v[86:87], s[18:19], v[88:89] op_sel_hi:[1,0,1]
	v_lshl_add_u64 v[88:89], v[108:109], 2, s[0:1]
	v_pk_mul_f32 v[90:91], v[114:115], v[120:121]
	global_load_dwordx4 v[114:117], v[88:89], off
	v_lshlrev_b32_e32 v108, 16, v84
	v_and_b32_e32 v109, 0xffff0000, v84
	v_lshlrev_b32_e32 v84, 16, v85
	v_and_b32_e32 v85, 0xffff0000, v85
	v_pk_fma_f32 v[88:89], v[118:119], s[18:19], v[90:91] op_sel_hi:[1,0,1]
	v_lshlrev_b32_e32 v90, 16, v82
	v_and_b32_e32 v91, 0xffff0000, v82
	v_lshlrev_b32_e32 v82, 16, v83
	v_and_b32_e32 v83, 0xffff0000, v83
	v_pk_mul_f32 v[84:85], v[58:59], v[84:85] op_sel:[1,0]
	v_pk_mul_f32 v[108:109], v[58:59], v[108:109] op_sel:[1,0]
	v_pk_fma_f32 v[82:83], v[58:59], v[82:83], v[84:85] op_sel_hi:[0,1,1]
	s_waitcnt vmcnt(2)
; __device__ __forceinline__ f32x4 xr2f(XRaw w) { return (f32x4){bflo(w.x), bfhi(w.x), bflo(w.y), bfhi(w.y)}; }
; __device__ __forceinline__ void ln_regs(f32x4 (&v)[8], const float* g, const float* bt, int lane) {
;     float s = 0.f;
; #pragma unroll
;     for (int j = 0; j < 8; ++j) s += (v[j].x + v[j].y) + (v[j].z + v[j].w);
;     const float mean = wave_sum(s) * (1.f / D); float s2 = 0.f;
; template <int L> __device__ __forceinline__ void p_moe_combine_ln(const Args& a, const XT* X, float* out) {
;     ...
;             for (int j = 0; j < 8; ++j) { const int k = j * 256 + lane * 4; const f32x4 gf = *(const f32x4*)(md + 10240 + k);
;                 const f32x4 ya = (f32x4){bflo(y0v[j].x), bfhi(y0v[j].x), bflo(y0v[j].y), bfhi(y0v[j].y)}, yb = (f32x4){bflo(y1v[j].x), bfhi(y1v[j].x), bflo(y1v[j].y), bfhi(y1v[j].y)};
;                 v[j] = ALPHA * xr2f(xv[j]) + (1.f + gf) * (w0 * ya + w1 * yb); }
	v_pk_add_f32 v[102:103], v[102:103], 1.0 op_sel_hi:[1,0]
	v_pk_add_f32 v[100:101], v[100:101], 1.0 op_sel_hi:[1,0]
	v_pk_fma_f32 v[90:91], v[58:59], v[90:91], v[108:109] op_sel_hi:[0,1,1]
	v_lshlrev_b32_e32 v118, 16, v74
	v_and_b32_e32 v119, 0xffff0000, v74
	v_lshlrev_b32_e32 v74, 16, v75
	v_and_b32_e32 v75, 0xffff0000, v75
	v_pk_mul_f32 v[82:83], v[82:83], v[102:103]
	v_pk_mul_f32 v[84:85], v[90:91], v[100:101]
	v_lshlrev_b32_e32 v90, 16, v80
	v_and_b32_e32 v91, 0xffff0000, v80
	v_lshlrev_b32_e32 v80, 16, v81
	v_and_b32_e32 v81, 0xffff0000, v81
	v_pk_fma_f32 v[74:75], v[74:75], s[18:19], v[82:83] op_sel_hi:[1,0,1]
	v_pk_fma_f32 v[82:83], v[118:119], s[18:19], v[84:85] op_sel_hi:[1,0,1]
	v_lshlrev_b32_e32 v84, 16, v78
	v_and_b32_e32 v85, 0xffff0000, v78
	v_lshlrev_b32_e32 v78, 16, v79
	v_and_b32_e32 v79, 0xffff0000, v79
	v_pk_mul_f32 v[80:81], v[58:59], v[80:81] op_sel:[1,0]
	v_pk_mul_f32 v[90:91], v[58:59], v[90:91] op_sel:[1,0]
	v_pk_add_f32 v[102:103], v[106:107], 1.0 op_sel_hi:[1,0]
	v_pk_add_f32 v[104:105], v[104:105], 1.0 op_sel_hi:[1,0]
	v_pk_fma_f32 v[84:85], v[58:59], v[84:85], v[90:91] op_sel_hi:[0,1,1]
	v_pk_fma_f32 v[78:79], v[58:59], v[78:79], v[80:81] op_sel_hi:[0,1,1]
	v_lshlrev_b32_e32 v100, 16, v68
	v_and_b32_e32 v101, 0xffff0000, v68
	v_lshlrev_b32_e32 v68, 16, v69
	v_and_b32_e32 v69, 0xffff0000, v69
	v_pk_mul_f32 v[78:79], v[78:79], v[102:103]
	v_pk_mul_f32 v[80:81], v[84:85], v[104:105]
	v_lshlrev_b32_e32 v84, 16, v72
	v_and_b32_e32 v85, 0xffff0000, v72
	v_lshlrev_b32_e32 v72, 16, v73
	v_and_b32_e32 v73, 0xffff0000, v73
	v_pk_fma_f32 v[68:69], v[68:69], s[18:19], v[78:79] op_sel_hi:[1,0,1]
	v_pk_fma_f32 v[78:79], v[100:101], s[18:19], v[80:81] op_sel_hi:[1,0,1]
	v_lshlrev_b32_e32 v80, 16, v70
	v_and_b32_e32 v81, 0xffff0000, v70
	v_lshlrev_b32_e32 v70, 16, v71
	v_and_b32_e32 v71, 0xffff0000, v71
	v_pk_mul_f32 v[72:73], v[58:59], v[72:73] op_sel:[1,0]
	v_pk_mul_f32 v[84:85], v[58:59], v[84:85] op_sel:[1,0]
	s_waitcnt vmcnt(1)
	v_pk_add_f32 v[100:101], v[112:113], 1.0 op_sel_hi:[1,0]
	v_pk_add_f32 v[102:103], v[110:111], 1.0 op_sel_hi:[1,0]
	v_pk_fma_f32 v[80:81], v[58:59], v[80:81], v[84:85] op_sel_hi:[0,1,1]
	v_pk_fma_f32 v[70:71], v[58:59], v[70:71], v[72:73] op_sel_hi:[0,1,1]
	v_lshlrev_b32_e32 v90, 16, v62
	v_and_b32_e32 v91, 0xffff0000, v62
	v_lshlrev_b32_e32 v62, 16, v63
	v_and_b32_e32 v63, 0xffff0000, v63
	v_pk_mul_f32 v[70:71], v[70:71], v[100:101]
	v_pk_mul_f32 v[72:73], v[80:81], v[102:103]
	v_lshlrev_b32_e32 v80, 16, v66
	v_and_b32_e32 v81, 0xffff0000, v66
	v_lshlrev_b32_e32 v66, 16, v67
	v_and_b32_e32 v67, 0xffff0000, v67
	v_pk_fma_f32 v[62:63], v[62:63], s[18:19], v[70:71] op_sel_hi:[1,0,1]
	v_pk_fma_f32 v[70:71], v[90:91], s[18:19], v[72:73] op_sel_hi:[1,0,1]
	v_lshlrev_b32_e32 v72, 16, v64
	v_and_b32_e32 v73, 0xffff0000, v64
	v_lshlrev_b32_e32 v64, 16, v65
	v_and_b32_e32 v65, 0xffff0000, v65
	v_pk_mul_f32 v[66:67], v[58:59], v[66:67] op_sel:[1,0]
	v_pk_mul_f32 v[80:81], v[58:59], v[80:81] op_sel:[1,0]
	v_pk_fma_f32 v[96:97], v[150:151], s[18:19], v[96:97] op_sel_hi:[1,0,1]
	v_pk_fma_f32 v[72:73], v[58:59], v[72:73], v[80:81] op_sel_hi:[0,1,1]
	s_waitcnt vmcnt(0)
	v_pk_add_f32 v[90:91], v[116:117], 1.0 op_sel_hi:[1,0]
	v_pk_add_f32 v[100:101], v[114:115], 1.0 op_sel_hi:[1,0]
	v_pk_fma_f32 v[58:59], v[58:59], v[64:65], v[66:67] op_sel_hi:[0,1,1]
	v_lshlrev_b32_e32 v84, 16, v60
	v_and_b32_e32 v85, 0xffff0000, v60
	v_lshlrev_b32_e32 v60, 16, v61
	v_and_b32_e32 v61, 0xffff0000, v61
	v_pk_mul_f32 v[58:59], v[58:59], v[90:91]
	v_pk_mul_f32 v[64:65], v[72:73], v[100:101]
	v_pk_fma_f32 v[92:93], v[152:153], s[18:19], v[92:93] op_sel_hi:[1,0,1]
	v_pk_fma_f32 v[58:59], v[60:61], s[18:19], v[58:59] op_sel_hi:[1,0,1]
	v_pk_fma_f32 v[60:61], v[84:85], s[18:19], v[64:65] op_sel_hi:[1,0,1]
	v_mov_b32_e32 v64, v96
	v_mov_b32_e32 v65, v98
	v_mov_b32_e32 v66, v97
	v_mov_b32_e32 v67, v99
	v_pk_add_f32 v[64:65], v[64:65], v[66:67]
	v_mov_b32_e32 v66, v92
	v_mov_b32_e32 v67, v94
	v_mov_b32_e32 v72, v93
	v_mov_b32_e32 v73, v95
	v_pk_add_f32 v[66:67], v[66:67], v[72:73]
	v_mov_b32_e32 v72, v2
	v_pk_add_f32 v[64:65], v[64:65], v[66:67]
	v_pk_mov_b32 v[66:67], v[2:3], v[0:1] op_sel:[1,0]
	v_mov_b32_e32 v73, v1
	v_pk_add_f32 v[66:67], v[66:67], v[72:73]
	v_add_f32_e32 v65, 0, v65
	v_pk_add_f32 v[66:67], v[66:67], v[66:67] op_sel_hi:[0,1]
	v_add_f32_e32 v65, v64, v65
	v_add_f32_e32 v73, v88, v89
	v_add_f32_e32 v81, v86, v87
	v_mov_b32_e32 v72, v82
	v_mov_b32_e32 v80, v83
	v_mov_b32_e32 v66, v74
	v_mov_b32_e32 v64, v75
	v_pk_add_f32 v[72:73], v[72:73], v[80:81]
	v_pk_add_f32 v[64:65], v[66:67], v[64:65]
	v_pk_mov_b32 v[66:67], v[78:79], v[68:69] op_sel:[1,0]
	v_pk_add_f32 v[64:65], v[72:73], v[64:65]
	v_mov_b32_e32 v72, v78
	v_mov_b32_e32 v73, v69
	v_pk_add_f32 v[66:67], v[66:67], v[72:73]
	v_pk_add_f32 v[64:65], v[64:65], v[64:65] op_sel_hi:[0,1]
	v_pk_add_f32 v[66:67], v[66:67], v[66:67] op_sel_hi:[0,1]
	v_add_f32_e32 v73, v70, v71
	v_add_f32_e32 v81, v62, v63
	v_mov_b32_e32 v72, v60
	v_mov_b32_e32 v80, v61
	v_mov_b32_e32 v66, v58
	v_mov_b32_e32 v64, v59
	v_pk_add_f32 v[72:73], v[72:73], v[80:81]
	v_pk_add_f32 v[64:65], v[66:67], v[64:65]
	v_xor_b32_e32 v66, 1, v126
	v_pk_add_f32 v[64:65], v[72:73], v[64:65]
	s_nop 0
	v_add_f32_e32 v64, v64, v65
	v_and_b32_e32 v65, 64, v126
	v_add_u32_e32 v65, 64, v65
	v_cmp_lt_i32_e32 vcc, v66, v65
	s_nop 1
	v_cndmask_b32_e32 v66, v126, v66, vcc
	v_lshlrev_b32_e32 v84, 2, v66
	s_waitcnt lgkmcnt(0)
	s_nop 1
	v_add_f32_dpp v64, v64, v64 quad_perm:[1,0,3,2] row_mask:0xf bank_mask:0xf
	v_xor_b32_e32 v66, 2, v126
	v_cmp_lt_i32_e32 vcc, v66, v65
	s_nop 1
	v_cndmask_b32_e32 v66, v126, v66, vcc
	v_lshlrev_b32_e32 v85, 2, v66
	s_waitcnt lgkmcnt(0)
; __device__ __forceinline__ void ln_regs(f32x4 (&v)[8], const float* g, const float* bt, int lane) {
;     ...
;     const float mean = wave_sum(s) * (1.f / D); float s2 = 0.f;
; #pragma unroll
;     for (int j = 0; j < 8; ++j) { v[j] = v[j] - mean; s2 += (v[j].x * v[j].x + v[j].y * v[j].y) + (v[j].z * v[j].z + v[j].w * v[j].w); }
;     const float rstd = 1.f / sqrtf(wave_sum(s2) * (1.f / D) + LN_EPS);
; #pragma unroll
;     for (int j = 0; j < 8; ++j) { const f32x4 gv = *(const f32x4*)(g + j * 256 + lane * 4), bv = *(const f32x4*)(bt + j * 256 + lane * 4); v[j] = v[j] * rstd * gv + bv; }
	s_nop 1
	v_add_f32_dpp v64, v64, v64 quad_perm:[2,3,0,1] row_mask:0xf bank_mask:0xf
	v_xor_b32_e32 v66, 4, v126
	v_cmp_lt_i32_e32 vcc, v66, v65
	s_nop 1
	v_cndmask_b32_e32 v66, v126, v66, vcc
	v_lshlrev_b32_e32 v90, 2, v66
	s_waitcnt lgkmcnt(0)
	s_nop 1
	v_add_f32_dpp v64, v64, v64 row_half_mirror row_mask:0xf bank_mask:0xf
	v_xor_b32_e32 v66, 8, v126
	v_cmp_lt_i32_e32 vcc, v66, v65
	s_nop 1
	v_cndmask_b32_e32 v66, v126, v66, vcc
	v_lshlrev_b32_e32 v91, 2, v66
	s_waitcnt lgkmcnt(0)
	s_nop 1
	v_add_f32_dpp v64, v64, v64 row_mirror row_mask:0xf bank_mask:0xf
	v_xor_b32_e32 v66, 16, v126
	v_cmp_lt_i32_e32 vcc, v66, v65
	s_nop 1
	v_cndmask_b32_e32 v66, v126, v66, vcc
	v_lshlrev_b32_e32 v129, 2, v66
	ds_bpermute_b32 v66, v129, v64
	s_waitcnt lgkmcnt(0)
	v_add_f32_e32 v64, v64, v66
	v_xor_b32_e32 v66, 32, v126
	v_cmp_lt_i32_e32 vcc, v66, v65
	s_nop 1
	v_cndmask_b32_e32 v65, v126, v66, vcc
	v_lshlrev_b32_e32 v166, 2, v65
	ds_bpermute_b32 v65, v166, v64
	s_waitcnt lgkmcnt(0)
	v_add_f32_e32 v100, v64, v65
	v_fmamk_f32 v99, v100, 0xba000000, v99
	v_fmamk_f32 v97, v100, 0xba000000, v97
	v_fmamk_f32 v95, v100, 0xba000000, v95
	v_fmac_f32_e32 v98, 0xba000000, v100
	v_fmamk_f32 v93, v100, 0xba000000, v93
	v_fmac_f32_e32 v96, 0xba000000, v100
	v_mov_b32_e32 v66, v99
	v_mov_b32_e32 v67, v97
	v_fmac_f32_e32 v94, 0xba000000, v100
	v_fmac_f32_e32 v92, 0xba000000, v100
	v_mov_b32_e32 v64, v98
	v_mov_b32_e32 v65, v96
	v_pk_mul_f32 v[66:67], v[66:67], v[66:67]
	v_mov_b32_e32 v72, v95
	v_mov_b32_e32 v73, v93
	v_pk_fma_f32 v[64:65], v[64:65], v[64:65], v[66:67]
	v_mov_b32_e32 v66, v94
	v_mov_b32_e32 v67, v92
	v_pk_mul_f32 v[72:73], v[72:73], v[72:73]
	v_fmamk_f32 v3, v100, 0xba000000, v3
	v_pk_fma_f32 v[66:67], v[66:67], v[66:67], v[72:73]
	v_fmac_f32_e32 v2, 0xba000000, v100
	v_pk_add_f32 v[64:65], v[64:65], v[66:67]
	v_fmamk_f32 v1, v100, 0xba000000, v1
	v_fmac_f32_e32 v0, 0xba000000, v100
	v_pk_add_f32 v[64:65], v[64:65], v[64:65] op_sel_hi:[0,1]
	v_pk_mul_f32 v[66:67], v[0:1], v[0:1]
	v_pk_mul_f32 v[72:73], v[2:3], v[2:3]
	v_fmac_f32_e32 v88, 0xba000000, v100
	v_pk_mov_b32 v[80:81], v[72:73], v[66:67] op_sel:[1,0]
	v_mov_b32_e32 v73, v67
	v_fmamk_f32 v89, v100, 0xba000000, v89
	v_fmac_f32_e32 v86, 0xba000000, v100
	v_mul_f32_e32 v64, v88, v88
	v_pk_add_f32 v[66:67], v[80:81], v[72:73]
	v_fmamk_f32 v87, v100, 0xba000000, v87
	v_pk_fma_f32 v[72:73], v[88:89], v[88:89], v[64:65] op_sel_hi:[1,1,0]
	v_mul_f32_e32 v64, v86, v86
	v_pk_add_f32 v[66:67], v[66:67], v[66:67] op_sel_hi:[0,1]
	v_pk_fma_f32 v[80:81], v[86:87], v[86:87], v[64:65] op_sel_hi:[1,1,0]
	v_fmamk_f32 v75, v100, 0xba000000, v75
	v_fmac_f32_e32 v74, 0xba000000, v100
	v_fmamk_f32 v83, v100, 0xba000000, v83
	v_fmac_f32_e32 v82, 0xba000000, v100
	v_mul_f32_e32 v72, v82, v82
	v_mul_f32_e32 v80, v83, v83
	v_mul_f32_e32 v66, v74, v74
	v_mul_f32_e32 v64, v75, v75
	v_pk_add_f32 v[72:73], v[72:73], v[80:81]
	v_pk_add_f32 v[64:65], v[66:67], v[64:65]
	v_fmamk_f32 v79, v100, 0xba000000, v79
	v_pk_add_f32 v[64:65], v[72:73], v[64:65]
	v_fmac_f32_e32 v78, 0xba000000, v100
	v_fmamk_f32 v69, v100, 0xba000000, v69
	v_fmac_f32_e32 v68, 0xba000000, v100
	v_pk_add_f32 v[64:65], v[64:65], v[64:65] op_sel_hi:[0,1]
	v_pk_mul_f32 v[66:67], v[68:69], v[68:69]
	v_pk_mul_f32 v[72:73], v[78:79], v[78:79]
	v_fmac_f32_e32 v70, 0xba000000, v100
	v_pk_mov_b32 v[80:81], v[72:73], v[66:67] op_sel:[1,0]
	v_mov_b32_e32 v73, v67
	v_fmamk_f32 v71, v100, 0xba000000, v71
	v_fmac_f32_e32 v62, 0xba000000, v100
	v_mul_f32_e32 v64, v70, v70
	v_pk_add_f32 v[66:67], v[80:81], v[72:73]
	v_fmamk_f32 v63, v100, 0xba000000, v63
	v_pk_fma_f32 v[72:73], v[70:71], v[70:71], v[64:65] op_sel_hi:[1,1,0]
	v_mul_f32_e32 v64, v62, v62
	v_pk_add_f32 v[66:67], v[66:67], v[66:67] op_sel_hi:[0,1]
	v_pk_fma_f32 v[80:81], v[62:63], v[62:63], v[64:65] op_sel_hi:[1,1,0]
	v_fmamk_f32 v59, v100, 0xba000000, v59
	v_fmac_f32_e32 v58, 0xba000000, v100
	v_fmamk_f32 v61, v100, 0xba000000, v61
	v_fmac_f32_e32 v60, 0xba000000, v100
	v_mul_f32_e32 v72, v60, v60
	v_mul_f32_e32 v80, v61, v61
	v_mul_f32_e32 v66, v58, v58
	v_mul_f32_e32 v64, v59, v59
	v_pk_add_f32 v[72:73], v[72:73], v[80:81]
	v_pk_add_f32 v[64:65], v[66:67], v[64:65]
	v_lshl_add_u64 v[80:81], s[6:7], 0, v[76:77]
	v_pk_add_f32 v[64:65], v[72:73], v[64:65]
	v_lshl_add_u64 v[72:73], s[4:5], 0, v[76:77]
	v_add_f32_e32 v64, v64, v65
	s_waitcnt lgkmcnt(0)
	s_nop 1
	v_add_f32_dpp v64, v64, v64 quad_perm:[1,0,3,2] row_mask:0xf bank_mask:0xf
	s_waitcnt lgkmcnt(0)
	s_nop 1
	v_add_f32_dpp v84, v64, v64 quad_perm:[2,3,0,1] row_mask:0xf bank_mask:0xf
	global_load_dwordx4 v[64:67], v[80:81], off
	global_load_dwordx4 v[100:103], v[72:73], off
	global_load_dwordx4 v[104:107], v[72:73], off offset:1024
	global_load_dwordx4 v[108:111], v[80:81], off offset:1024
	global_load_dwordx4 v[112:115], v[72:73], off offset:2048
	global_load_dwordx4 v[116:119], v[72:73], off offset:3072
	global_load_dwordx4 v[120:123], v[80:81], off offset:2048
	global_load_dwordx4 v[130:133], v[80:81], off offset:3072
	v_add_co_u32_e32 v72, vcc, s30, v72
	s_nop 0
	v_addc_co_u32_e32 v73, vcc, 0, v73, vcc
	v_add_co_u32_e32 v80, vcc, s30, v80
	global_load_dwordx4 v[134:137], v[72:73], off
	s_nop 0
	v_addc_co_u32_e32 v81, vcc, 0, v81, vcc
	global_load_dwordx4 v[138:141], v[80:81], off
	global_load_dwordx4 v[142:145], v[72:73], off offset:1024
	global_load_dwordx4 v[146:149], v[80:81], off offset:1024
	global_load_dwordx4 v[150:153], v[72:73], off offset:2048
	global_load_dwordx4 v[154:157], v[80:81], off offset:2048
	global_load_dwordx4 v[158:161], v[72:73], off offset:3072
	global_load_dwordx4 v[162:165], v[80:81], off offset:3072
	s_waitcnt lgkmcnt(0)
; __device__ __forceinline__ void ln_regs(f32x4 (&v)[8], const float* g, const float* bt, int lane) {
;     ...
;     const float mean = wave_sum(s) * (1.f / D); float s2 = 0.f;
; #pragma unroll
;     for (int j = 0; j < 8; ++j) { v[j] = v[j] - mean; s2 += (v[j].x * v[j].x + v[j].y * v[j].y) + (v[j].z * v[j].z + v[j].w * v[j].w); }
;     const float rstd = 1.f / sqrtf(wave_sum(s2) * (1.f / D) + LN_EPS);
; #pragma unroll
;     for (int j = 0; j < 8; ++j) { const f32x4 gv = *(const f32x4*)(g + j * 256 + lane * 4), bv = *(const f32x4*)(bt + j * 256 + lane * 4); v[j] = v[j] * rstd * gv + bv; }
; template <int L> __device__ __forceinline__ void p_moe_combine_ln(const Args& a, const XT* X, float* out) {
;     ...
;         ln_regs(v, g, bt, lane);
; #pragma unroll
;         for (int j = 0; j < 8; ++j) *(f32x4*)(out + (size_t)m * D + j * 256 + lane * 4) = v[j];
	s_nop 1
	v_add_f32_dpp v84, v84, v84 row_half_mirror row_mask:0xf bank_mask:0xf
	s_waitcnt lgkmcnt(0)
	s_nop 1
	v_add_f32_dpp v84, v84, v84 row_mirror row_mask:0xf bank_mask:0xf
	ds_bpermute_b32 v72, v129, v84
	s_waitcnt lgkmcnt(0)
	v_add_f32_e32 v72, v84, v72
	ds_bpermute_b32 v73, v166, v72
	s_waitcnt lgkmcnt(0)
	v_add_f32_e32 v72, v72, v73
	v_fmamk_f32 v72, v72, 0x3a000000, v127
	v_mul_f32_e32 v73, 0x4f800000, v72
	v_cmp_gt_f32_e32 vcc, s29, v72
	s_nop 1
	v_cndmask_b32_e32 v72, v72, v73, vcc
	v_sqrt_f32_e32 v73, v72
	s_nop 0
	v_add_u32_e32 v80, -1, v73
	v_fma_f32 v81, -v80, v73, v72
	v_cmp_ge_f32_e64 s[0:1], 0, v81
	v_add_u32_e32 v81, 1, v73
	s_nop 0
	v_cndmask_b32_e64 v80, v73, v80, s[0:1]
	v_fma_f32 v73, -v81, v73, v72
	v_cmp_lt_f32_e64 s[0:1], 0, v73
	s_nop 1
	v_cndmask_b32_e64 v73, v80, v81, s[0:1]
	v_mul_f32_e32 v80, 0x37800000, v73
	v_cndmask_b32_e32 v73, v73, v80, vcc
	v_cmp_class_f32_e32 vcc, v72, v128
	s_nop 1
	v_cndmask_b32_e32 v72, v73, v72, vcc
	v_div_scale_f32 v73, s[0:1], v72, v72, 1.0
	v_rcp_f32_e32 v80, v73
	s_mov_b32 s0, s20
	v_fma_f32 v81, -v73, v80, 1.0
	v_fmac_f32_e32 v80, v81, v80
	v_div_scale_f32 v81, vcc, 1.0, v72, 1.0
	v_mul_f32_e32 v84, v81, v80
	v_fma_f32 v85, -v73, v84, v81
	v_fmac_f32_e32 v84, v85, v80
	v_fma_f32 v73, -v73, v84, v81
	v_div_fmas_f32 v73, v73, v80, v84
	v_div_fixup_f32 v166, v73, v72, 1.0
	v_pk_mul_f32 v[72:73], v[98:99], v[166:167] op_sel_hi:[1,0]
	v_pk_mul_f32 v[80:81], v[94:95], v[166:167] op_sel_hi:[1,0]
	s_waitcnt vmcnt(14)
	v_pk_fma_f32 v[64:65], v[100:101], v[72:73], v[64:65]
	v_pk_mul_f32 v[72:73], v[96:97], v[166:167] op_sel_hi:[1,0]
	v_pk_fma_f32 v[66:67], v[102:103], v[80:81], v[66:67]
	v_pk_mul_f32 v[80:81], v[92:93], v[166:167] op_sel_hi:[1,0]
	s_waitcnt vmcnt(12)
	v_pk_fma_f32 v[90:91], v[104:105], v[72:73], v[108:109]
	v_pk_mul_f32 v[72:73], v[2:3], v[166:167] op_sel_hi:[1,0]
	v_pk_mul_f32 v[0:1], v[0:1], v[166:167] op_sel_hi:[1,0]
	v_pk_fma_f32 v[92:93], v[106:107], v[80:81], v[110:111]
	s_waitcnt vmcnt(9)
	v_pk_fma_f32 v[2:3], v[114:115], v[0:1], v[122:123]
	v_pk_fma_f32 v[0:1], v[112:113], v[72:73], v[120:121]
	v_pk_mul_f32 v[72:73], v[88:89], v[166:167] op_sel_hi:[1,0]
	v_pk_mul_f32 v[80:81], v[86:87], v[166:167] op_sel_hi:[1,0]
	v_pk_mul_f32 v[68:69], v[68:69], v[166:167] op_sel_hi:[1,0]
	v_pk_mul_f32 v[62:63], v[62:63], v[166:167] op_sel_hi:[1,0]
	s_waitcnt vmcnt(8)
	v_pk_fma_f32 v[86:87], v[118:119], v[80:81], v[132:133]
	v_pk_fma_f32 v[84:85], v[116:117], v[72:73], v[130:131]
	v_pk_mul_f32 v[72:73], v[82:83], v[166:167] op_sel_hi:[1,0]
	v_pk_mul_f32 v[74:75], v[74:75], v[166:167] op_sel_hi:[1,0]
	v_pk_mul_f32 v[78:79], v[78:79], v[166:167] op_sel_hi:[1,0]
	s_waitcnt vmcnt(4)
	v_pk_fma_f32 v[80:81], v[144:145], v[68:69], v[148:149]
	v_pk_mul_f32 v[68:69], v[70:71], v[166:167] op_sel_hi:[1,0]
	s_waitcnt vmcnt(2)
	v_pk_fma_f32 v[70:71], v[152:153], v[62:63], v[156:157]
	v_pk_mul_f32 v[62:63], v[60:61], v[166:167] op_sel_hi:[1,0]
	v_pk_mul_f32 v[58:59], v[58:59], v[166:167] op_sel_hi:[1,0]
	v_pk_fma_f32 v[74:75], v[136:137], v[74:75], v[140:141]
	v_pk_fma_f32 v[72:73], v[134:135], v[72:73], v[138:139]
	v_pk_fma_f32 v[78:79], v[142:143], v[78:79], v[146:147]
	v_pk_fma_f32 v[68:69], v[150:151], v[68:69], v[154:155]
	s_waitcnt vmcnt(0)
	v_pk_fma_f32 v[60:61], v[160:161], v[58:59], v[164:165]
	v_pk_fma_f32 v[58:59], v[158:159], v[62:63], v[162:163]
	v_lshl_add_u64 v[62:63], s[10:11], 0, v[76:77]
	s_add_u32 s10, s10, s12
	global_store_dwordx4 v[62:63], v[64:67], off offset:-4096
	global_store_dwordx4 v[62:63], v[90:93], off offset:-3072
	global_store_dwordx4 v[62:63], v[0:3], off offset:-2048
	global_store_dwordx4 v[62:63], v[84:87], off offset:-1024
	global_store_dwordx4 v[62:63], v[72:75], off
	global_store_dwordx4 v[62:63], v[78:81], off offset:1024
	global_store_dwordx4 v[62:63], v[68:71], off offset:2048
	global_store_dwordx4 v[62:63], v[58:61], off offset:3072
	s_addc_u32 s11, s11, s13
	s_add_i32 s14, s14, s3
	s_andn2_b64 vcc, exec, s[22:23]
	v_mov_b64_e32 v[60:61], v[22:23]
	v_mov_b64_e32 v[62:63], v[20:21]
	v_mov_b64_e32 v[68:69], v[18:19]
	v_mov_b64_e32 v[74:75], v[16:17]
	v_mov_b64_e32 v[86:87], v[12:13]
	v_mov_b64_e32 v[92:93], v[10:11]
	v_mov_b64_e32 v[98:99], v[8:9]
	v_mov_b64_e32 v[100:101], v[6:7]
	v_mov_b64_e32 v[64:65], v[40:41]
	v_mov_b64_e32 v[70:71], v[42:43]
	v_mov_b64_e32 v[78:79], v[44:45]
	v_mov_b64_e32 v[82:83], v[46:47]
	v_mov_b64_e32 v[88:89], v[24:25]
	v_mov_b64_e32 v[94:95], v[26:27]
	v_mov_b64_e32 v[102:103], v[28:29]
	v_mov_b64_e32 v[110:111], v[30:31]
	v_mov_b64_e32 v[66:67], v[52:53]
	v_mov_b64_e32 v[72:73], v[54:55]
	v_mov_b64_e32 v[80:81], v[48:49]
	v_mov_b64_e32 v[84:85], v[50:51]
	v_mov_b64_e32 v[90:91], v[32:33]
	v_mov_b64_e32 v[96:97], v[34:35]
	v_mov_b64_e32 v[104:105], v[36:37]
	v_mov_b64_e32 v[106:107], v[38:39]
	v_mov_b64_e32 v[58:59], v[14:15]
	v_mov_b32_e32 v2, v56
	v_mov_b32_e32 v76, v57
	s_cbranch_vccz .LBB0_2334
